# norm phases: LDS weight fill unrolled, gate LDS reads pipelined, gate params hoisted; MoE gather copy batched 8 deep; placement padded
# baseline (speedup 1.0000x reference)
; #define LAS __attribute__((address_space(3)))
; template <int MODE, bool SB  > DI void norm_phase(const Params& P, const Frame& F, int L, const void* src_, const float* gain, bool combine) {
;     ...
;     if (MODE == 1) { const f32x4* w = (const f32x4*)((const float*)(ws + WS_WGT) + (size_t)L * 16 * D); for (int i = F.tid; i < 16 * D / 4; i += NTHR) ((LAS f32x4*)F.lds)[i] = w[i]; __syncthreads(); }
.LBB0_78:
	global_load_dwordx4 v[130:133], v[0:1], off
	v_lshl_add_u64 v[0:1], v[0:1], 0, s[6:7]
	global_load_dwordx4 v[134:137], v[0:1], off
	v_lshl_add_u64 v[0:1], v[0:1], 0, s[6:7]
	global_load_dwordx4 v[138:141], v[0:1], off
	v_lshl_add_u64 v[0:1], v[0:1], 0, s[6:7]
	global_load_dwordx4 v[142:145], v[0:1], off
	v_lshl_add_u64 v[0:1], v[0:1], 0, s[6:7]
	global_load_dwordx4 v[146:149], v[0:1], off
	v_lshl_add_u64 v[0:1], v[0:1], 0, s[6:7]
	global_load_dwordx4 v[150:153], v[0:1], off
	v_lshl_add_u64 v[0:1], v[0:1], 0, s[6:7]
	global_load_dwordx4 v[154:157], v[0:1], off
	v_lshl_add_u64 v[0:1], v[0:1], 0, s[6:7]
	global_load_dwordx4 v[158:161], v[0:1], off
	v_lshl_add_u64 v[0:1], v[0:1], 0, s[6:7]
	global_load_dwordx4 v[162:165], v[0:1], off
	v_lshl_add_u64 v[0:1], v[0:1], 0, s[6:7]
	global_load_dwordx4 v[166:169], v[0:1], off
	v_lshl_add_u64 v[0:1], v[0:1], 0, s[6:7]
	global_load_dwordx4 v[170:173], v[0:1], off
	v_lshl_add_u64 v[0:1], v[0:1], 0, s[6:7]
	global_load_dwordx4 v[174:177], v[0:1], off
	v_lshl_add_u64 v[0:1], v[0:1], 0, s[6:7]
	global_load_dwordx4 v[178:181], v[0:1], off
	v_lshl_add_u64 v[0:1], v[0:1], 0, s[6:7]
	global_load_dwordx4 v[182:185], v[0:1], off
	v_lshl_add_u64 v[0:1], v[0:1], 0, s[6:7]
	global_load_dwordx4 v[186:189], v[0:1], off
	v_lshl_add_u64 v[0:1], v[0:1], 0, s[6:7]
	global_load_dwordx4 v[190:193], v[0:1], off
	s_waitcnt vmcnt(15)
	ds_write_b128 v4, v[130:133]
	v_add_u32_e32 v4, 0x2000, v4
	s_waitcnt vmcnt(14)
	ds_write_b128 v4, v[134:137]
	v_add_u32_e32 v4, 0x2000, v4
	s_waitcnt vmcnt(13)
	ds_write_b128 v4, v[138:141]
	v_add_u32_e32 v4, 0x2000, v4
	s_waitcnt vmcnt(12)
	ds_write_b128 v4, v[142:145]
	v_add_u32_e32 v4, 0x2000, v4
	s_waitcnt vmcnt(11)
	ds_write_b128 v4, v[146:149]
	v_add_u32_e32 v4, 0x2000, v4
	s_waitcnt vmcnt(10)
	ds_write_b128 v4, v[150:153]
	v_add_u32_e32 v4, 0x2000, v4
	s_waitcnt vmcnt(9)
	ds_write_b128 v4, v[154:157]
	v_add_u32_e32 v4, 0x2000, v4
	s_waitcnt vmcnt(8)
	ds_write_b128 v4, v[158:161]
	v_add_u32_e32 v4, 0x2000, v4
	s_waitcnt vmcnt(7)
	ds_write_b128 v4, v[162:165]
	v_add_u32_e32 v4, 0x2000, v4
	s_waitcnt vmcnt(6)
	ds_write_b128 v4, v[166:169]
	v_add_u32_e32 v4, 0x2000, v4
	s_waitcnt vmcnt(5)
	ds_write_b128 v4, v[170:173]
	v_add_u32_e32 v4, 0x2000, v4
	s_waitcnt vmcnt(4)
	ds_write_b128 v4, v[174:177]
	v_add_u32_e32 v4, 0x2000, v4
	s_waitcnt vmcnt(3)
	ds_write_b128 v4, v[178:181]
	v_add_u32_e32 v4, 0x2000, v4
	s_waitcnt vmcnt(2)
	ds_write_b128 v4, v[182:185]
	v_add_u32_e32 v4, 0x2000, v4
	s_waitcnt vmcnt(1)
	ds_write_b128 v4, v[186:189]
	v_add_u32_e32 v4, 0x2000, v4
	s_waitcnt vmcnt(0)
	ds_write_b128 v4, v[190:193]
; #define LAS __attribute__((address_space(3)))
; DI float sigmoidf_(float x) { return __builtin_amdgcn_rcpf(1.0f + __expf(-x)); }
; DI float softplusf_(float x) { return fmaxf(x, 0.f) + log1pf(__expf(-fabsf(x))); }
; template <int MODE, bool SB  > DI void norm_phase(const Params& P, const Frame& F, int L, const void* src_, const float* gain, bool combine) {
;     ...
;     if (MODE == 1) { const f32x4* w = (const f32x4*)((const float*)(ws + WS_WGT) + (size_t)L * 16 * D); for (int i = F.tid; i < 16 * D / 4; i += NTHR) ((LAS f32x4*)F.lds)[i] = w[i]; __syncthreads(); }
;     if (MODE == 2) { const f32x4* w = (const f32x4*)(ws + WS_WRT); for (int i = F.tid; i < NEXP * D / 4; i += NTHR) ((LAS f32x4*)F.lds)[i] = w[i]; if (F.tid < 8) F.MISC[16 + F.tid] = 0u; __syncthreads(); }
;     f32x4 g[8];
; #pragma unroll
;     for (int j = 0; j < 8; ++j) g[j] = *(const f32x4*)(gain + 4 * F.lane + 256 * j);
;     f32x4 vn[SB ? 1 : 8]; u32x2 vb[SB ? 8 : 1];
; #pragma unroll
;     for (int j = 0; j < 8; ++j) { if constexpr (SB) vb[j] = *(const u32x2*)(srcb + (size_t)(r_lo + F.wave) * D + 4 * F.lane + 256 * j); else vn[j] = *(const f32x4*)(src + (size_t)(r_lo + F.wave) * D + 4 * F.lane + 256 * j); }
;     ...
;             if ((F.lane & 3) == 0) { const int gi = ((F.lane >> 5) & 1) * 8 + ((F.lane >> 4) & 1) * 4 + ((F.lane >> 3) & 1) * 2 + ((F.lane >> 2) & 1), h = gi & 3; float r;
;                 if (gi < 4) r = sigmoidf_(mine);
;                 else if (gi < 8) r = -__expf(P.in[I_DN_A_LOG][L * 4 + h]) * softplusf_(mine + P.in[I_DN_DT_BIAS][L * 4 + h]);
;                 else if (gi < 12) r = mine + P.in[I_ML_I_BIAS][L * 4 + h];
;                 else r = -softplusf_(-(mine + P.in[I_ML_F_BIAS][L * 4 + h]));
.LBB0_79:
	s_or_b64 exec, exec, s[0:1]
	s_lshl_b32 s0, s2, 6
	s_add_i32 s3, s0, 64
	s_add_i32 s0, s86, s0
	s_cmp_lt_i32 s0, s3
	s_waitcnt lgkmcnt(0)
	s_barrier
	s_cbranch_scc0 .LBB0_96
	v_lshlrev_b32_e32 v0, 2, v64
	v_ashrrev_i32_e32 v1, 31, v0
	s_ashr_i32 s1, s0, 31
	v_lshlrev_b64 v[0:1], 2, v[0:1]
	s_lshl_b64 s[4:5], s[0:1], 13
	v_lshl_add_u64 v[12:13], s[72:73], 0, v[0:1]
	s_add_u32 s4, s68, s4
	v_add_co_u32_e32 v28, vcc, 0x1000, v12
	s_addc_u32 s5, s69, s5
	s_movk_i32 s30, 0x1000
	v_addc_co_u32_e32 v29, vcc, 0, v13, vcc
	v_lshl_add_u64 v[32:33], s[4:5], 0, v[0:1]
	v_add_co_u32_e32 v34, vcc, s30, v32
	v_and_b32_e32 v4, 64, v2
	s_nop 0
	v_addc_co_u32_e32 v35, vcc, 0, v33, vcc
	v_xor_b32_e32 v3, 32, v2
	v_add_u32_e32 v4, 64, v4
	v_cmp_lt_i32_e32 vcc, v3, v4
	v_lshl_add_u64 v[96:97], s[68:69], 0, v[0:1]
	v_and_b32_e32 v66, 32, v64
	v_cndmask_b32_e32 v2, v2, v3, vcc
	v_lshlrev_b32_e32 v116, 2, v2
	global_load_dwordx4 v[0:3], v[12:13], off
	global_load_dwordx4 v[4:7], v[12:13], off offset:1024
	global_load_dwordx4 v[8:11], v[12:13], off offset:2048
	s_nop 0
	global_load_dwordx4 v[12:15], v[12:13], off offset:3072
	s_nop 0
	global_load_dwordx4 v[16:19], v[28:29], off
	global_load_dwordx4 v[20:23], v[28:29], off offset:1024
	global_load_dwordx4 v[24:27], v[28:29], off offset:2048
	s_nop 0
	global_load_dwordx4 v[28:31], v[28:29], off offset:3072
	s_nop 0
	global_load_dwordx4 v[60:63], v[34:35], off offset:3072
	global_load_dwordx4 v[56:59], v[34:35], off offset:2048
	global_load_dwordx4 v[52:55], v[34:35], off offset:1024
	global_load_dwordx4 v[48:51], v[34:35], off
	global_load_dwordx4 v[44:47], v[32:33], off offset:3072
	global_load_dwordx4 v[40:43], v[32:33], off offset:2048
	global_load_dwordx4 v[36:39], v[32:33], off offset:1024
	s_nop 0
	global_load_dwordx4 v[32:35], v[32:33], off
	v_cmp_eq_u32_e64 s[4:5], 0, v66
	v_cmp_ne_u32_e64 s[6:7], 0, v66
	v_and_b32_e32 v66, 16, v64
	v_cmp_eq_u32_e64 s[8:9], 0, v66
	v_and_b32_e32 v66, 8, v64
	v_cmp_eq_u32_e64 s[10:11], 0, v66
	v_and_b32_e32 v66, 4, v64
	s_load_dwordx16 s[68:83], s[62:63], 0x40
	v_cmp_eq_u32_e64 s[12:13], 0, v66
	v_and_b32_e32 v66, 3, v64
	v_cmp_eq_u32_e64 s[14:15], 0, v66
	v_lshrrev_b32_e32 v66, 2, v64
	v_and_b32_e32 v66, 12, v66
	v_cmp_ne_u32_e64 s[16:17], 0, v66
	v_cmp_ne_u32_e64 s[18:19], 12, v66
	v_and_b32_e32 v66, 12, v64
	v_mov_b32_e32 v67, 0
	s_waitcnt lgkmcnt(0)
	v_lshl_add_u64 v[98:99], s[80:81], 0, v[66:67]
	v_lshl_add_u64 v[100:101], s[82:83], 0, v[66:67]
	s_load_dwordx16 s[68:83], s[62:63], 0x0
	s_lshl_b64 s[20:21], s[0:1], 6
	v_ashrrev_i32_e32 v65, 31, v64
	v_lshl_add_u32 v117, v64, 4, 0
	v_add_u32_e32 v118, 0x10000, v117
	s_waitcnt lgkmcnt(0)
	v_lshl_add_u64 v[102:103], s[80:81], 0, v[66:67]
	v_lshl_add_u64 v[104:105], s[82:83], 0, v[66:67]
	v_and_or_b32 v66, v64, 60, s20
	v_mov_b32_e32 v67, s21
	s_mov_b64 s[20:21], 0x200000
	v_lshl_add_u64 v[106:107], v[66:67], 0, s[20:21]
	s_lshl_b64 s[20:21], s[0:1], 12
	v_add_u32_e32 v119, 0x10400, v117
	v_add_u32_e32 v120, 0x10800, v117
	v_add_u32_e32 v121, 0x10c00, v117
	v_add_u32_e32 v122, 0x11000, v117
	v_add_u32_e32 v123, 0x11400, v117
	v_add_u32_e32 v124, 0x11800, v117
	v_add_u32_e32 v125, 0x11c00, v117
	v_add_u32_e32 v126, 0x12000, v117
	v_add_u32_e32 v127, 0x12400, v117
	v_add_u32_e32 v128, 0x12800, v117
	v_add_u32_e32 v129, 0x12c00, v117
	v_add_u32_e32 v130, 0x13000, v117
	v_add_u32_e32 v131, 0x13400, v117
	v_add_u32_e32 v132, 0x13800, v117
	v_add_u32_e32 v133, 0x13c00, v117
	v_add_u32_e32 v134, 0x14000, v117
	v_add_u32_e32 v135, 0x14400, v117
	v_add_u32_e32 v136, 0x14800, v117
	v_add_u32_e32 v137, 0x14c00, v117
	v_add_u32_e32 v138, 0x15000, v117
	v_add_u32_e32 v139, 0x15400, v117
	v_add_u32_e32 v140, 0x15800, v117
	v_add_u32_e32 v141, 0x15c00, v117
	v_add_u32_e32 v142, 0x16000, v117
	v_add_u32_e32 v143, 0x16400, v117
	v_add_u32_e32 v144, 0x16800, v117
	v_add_u32_e32 v145, 0x16c00, v117
	v_add_u32_e32 v146, 0x17000, v117
	v_add_u32_e32 v147, 0x17400, v117
	v_add_u32_e32 v148, 0x17800, v117
	v_add_u32_e32 v149, 0x17c00, v117
	v_add_u32_e32 v150, 0x18000, v117
	v_add_u32_e32 v151, 0x18400, v117
	v_add_u32_e32 v152, 0x18800, v117
	v_add_u32_e32 v153, 0x18c00, v117
	v_add_u32_e32 v154, 0x19000, v117
	v_add_u32_e32 v155, 0x19400, v117
	v_add_u32_e32 v156, 0x19800, v117
	v_add_u32_e32 v157, 0x19c00, v117
	v_add_u32_e32 v158, 0x1a000, v117
	v_add_u32_e32 v159, 0x1a400, v117
	v_add_u32_e32 v160, 0x1a800, v117
	v_add_u32_e32 v161, 0x1ac00, v117
	v_lshl_add_u64 v[108:109], v[64:65], 3, s[20:21]
	s_mov_b32 s1, 0xbfb8aa3b
	s_mov_b32 s31, 0x3f2aaaab
	s_mov_b32 s33, 0x3f317218
	s_mov_b32 s34, 0x7f800000
	s_mov_b32 s35, 0x33800000
	v_add_u32_e32 v162, 0x1b000, v117
	v_add_u32_e32 v163, 0x1b400, v117
	v_add_u32_e32 v164, 0x1b800, v117
	v_add_u32_e32 v165, 0x1bc00, v117
	v_add_u32_e32 v166, 0x1c000, v117
	v_add_u32_e32 v167, 0x1c400, v117
	v_add_u32_e32 v168, 0x1c800, v117
	v_add_u32_e32 v169, 0x1cc00, v117
	v_add_u32_e32 v170, 0x1d000, v117
	v_add_u32_e32 v171, 0x1d400, v117
	v_add_u32_e32 v172, 0x1d800, v117
	v_add_u32_e32 v173, 0x1dc00, v117
	v_add_u32_e32 v174, 0x1e000, v117
	v_add_u32_e32 v175, 0x1e400, v117
	v_add_u32_e32 v176, 0x1e800, v117
	v_add_u32_e32 v177, 0x1ec00, v117
	v_add_u32_e32 v178, 0x1f000, v117
	v_add_u32_e32 v179, 0x1f400, v117
	v_add_u32_e32 v180, 0x1f800, v117
	v_add_u32_e32 v181, 0x1fc00, v117
	v_mov_b32_e32 v182, 0x358637bd
	v_mov_b32_e32 v183, 0x260
	v_mov_b32_e32 v184, 0x3ecc95a3
	v_mov_b32_e32 v185, 0x7f800000
	v_mov_b32_e32 v186, 0x7fc00000
	v_mov_b32_e32 v187, 0xff800000
	v_mov_b32_e32 v110, 0x3f317218
	global_load_dword v203, v[98:99], off
	global_load_dword v204, v[100:101], off
	global_load_dword v205, v[104:105], off
	global_load_dword v206, v[102:103], off
	s_branch .LBB0_83

; DI unsigned pk2(float lo, float hi) { const f32x2 v = {lo, hi}; return __builtin_bit_cast(unsigned, __builtin_convertvector(v, bf16x2_t)); }
; DI float wave_sum(float v) { v += shx<1>(v); v += shx<2>(v); v += shx<4>(v); v += shx<8>(v); v += shx<16>(v); v += shx<32>(v); return v; }
; template <int MODE, bool SB  > DI void norm_phase(const Params& P, const Frame& F, int L, const void* src_, const float* gain, bool combine) {
;     ...
;     for (int row = r_lo + F.wave; row < r_hi; row += NWAVES) {
;         f32x4 v[8];
; #pragma unroll
;         for (int j = 0; j < 8; ++j) { if constexpr (SB) v[j] = (f32x4){bflo(vb[j].x), bfhi(vb[j].x), bflo(vb[j].y), bfhi(vb[j].y)}; else v[j] = vn[j]; }
;         { const int rnx = (row + NWAVES < r_hi) ? row + NWAVES : row;
; #pragma unroll
;           for (int j = 0; j < 8; ++j) { if constexpr (SB) vb[j] = *(const u32x2*)(srcb + (size_t)rnx * D + 4 * F.lane + 256 * j); else vn[j] = *(const f32x4*)(src + (size_t)rnx * D + 4 * F.lane + 256 * j); } }
;         if (MODE == 3 && combine) {
;             const int* SLOT = (const int*)(ws + WS_SLOT); const float* TOPW = (const float*)(ws + WS_TOPW); const bf16* Y = (const bf16*)(ws + WS_T + T_YPERM);
;             const int s1 = SLOT[row * 2], s2 = SLOT[row * 2 + 1]; const float w1 = TOPW[row * 2], w2 = TOPW[row * 2 + 1];
;             u32x2 ya[8], yb[8];
; #pragma unroll
;             for (int j = 0; j < 8; ++j) { ya[j] = *(const u32x2*)(Y + (size_t)s1 * D + 4 * F.lane + 256 * j); yb[j] = *(const u32x2*)(Y + (size_t)s2 * D + 4 * F.lane + 256 * j); }
; #pragma unroll
;             for (int j = 0; j < 8; ++j) { const f32x4 y1 = (f32x4){bflo(ya[j].x), bfhi(ya[j].x), bflo(ya[j].y), bfhi(ya[j].y)}, y2 = (f32x4){bflo(yb[j].x), bfhi(yb[j].x), bflo(yb[j].y), bfhi(yb[j].y)};
;                 v[j] = v[j] + w1 * y1 + w2 * y2;
;                 const u32x2 hb = {pk2(v[j][0], v[j][1]), pk2(v[j][2], v[j][3])}; *(u32x2*)(const_cast<bf16*>(srcb) + (size_t)row * D + 4 * F.lane + 256 * j) = hb;
;                 v[j] = (f32x4){bflo(hb.x), bfhi(hb.x), bflo(hb.y), bfhi(hb.y)}; }
;         }
;         float ss = 0.f;
; #pragma unroll
;         for (int j = 0; j < 8; ++j) ss += (v[j][0] * v[j][0] + v[j][1] * v[j][1]) + (v[j][2] * v[j][2] + v[j][3] * v[j][3]);
;         const float rstd = 1.0f / sqrtf(wave_sum(ss) * (1.0f / D) + EPS);
.LBB0_83:
	s_waitcnt vmcnt(1)
	v_mov_b64_e32 v[90:91], v[38:39]
	s_waitcnt vmcnt(0)
	v_mov_b64_e32 v[94:95], v[34:35]
	v_mov_b64_e32 v[88:89], v[36:37]
	v_mov_b64_e32 v[92:93], v[32:33]
	v_mov_b32_e32 v114, v93
	v_mov_b32_e32 v115, v89
	v_mov_b32_e32 v112, v92
	v_mov_b32_e32 v113, v88
	v_pk_mul_f32 v[114:115], v[114:115], v[114:115]
	v_mov_b32_e32 v188, v95
	v_mov_b32_e32 v189, v91
	v_mov_b64_e32 v[86:87], v[42:43]
	v_pk_fma_f32 v[112:113], v[112:113], v[112:113], v[114:115]
	v_mov_b32_e32 v114, v94
	v_mov_b32_e32 v115, v90
	v_pk_mul_f32 v[188:189], v[188:189], v[188:189]
	v_mov_b64_e32 v[84:85], v[40:41]
	v_pk_fma_f32 v[114:115], v[114:115], v[114:115], v[188:189]
	v_pk_mul_f32 v[188:189], v[84:85], v[84:85]
	v_pk_add_f32 v[112:113], v[112:113], v[114:115]
	v_pk_mul_f32 v[114:115], v[86:87], v[86:87]
	v_mov_b64_e32 v[78:79], v[50:51]
	v_pk_mov_b32 v[190:191], v[188:189], v[114:115] op_sel:[1,0]
	v_mov_b32_e32 v189, v115
	v_mov_b64_e32 v[76:77], v[48:49]
	v_pk_add_f32 v[114:115], v[190:191], v[188:189]
	v_mov_b64_e32 v[82:83], v[46:47]
	v_mul_f32_e32 v111, v76, v76
	v_mul_f32_e32 v188, v77, v77
	v_pk_add_f32 v[112:113], v[112:113], v[112:113] op_sel:[0,1] op_sel_hi:[1,0]
	v_pk_add_f32 v[114:115], v[114:115], v[114:115] op_sel:[0,1] op_sel_hi:[1,0]
	v_mov_b64_e32 v[80:81], v[44:45]
	v_mov_b32_e32 v113, v111
	v_mov_b32_e32 v115, v188
	v_pk_add_f32 v[112:113], v[112:113], v[114:115]
	v_mul_f32_e32 v114, v81, v81
	v_mul_f32_e32 v189, v78, v78
	v_pk_fma_f32 v[114:115], v[80:81], v[80:81], v[114:115] op_sel_hi:[1,1,0]
	v_mul_f32_e32 v188, v83, v83
	v_mul_f32_e32 v190, v79, v79
	v_mov_b32_e32 v115, v189
	v_pk_fma_f32 v[188:189], v[82:83], v[82:83], v[188:189] op_sel_hi:[1,1,0]
	v_mov_b64_e32 v[74:75], v[54:55]
	v_mov_b32_e32 v189, v190
	v_mov_b64_e32 v[72:73], v[52:53]
	v_pk_add_f32 v[114:115], v[114:115], v[188:189]
	v_pk_mul_f32 v[188:189], v[72:73], v[72:73]
	v_pk_add_f32 v[112:113], v[112:113], v[114:115]
	v_pk_mul_f32 v[114:115], v[74:75], v[74:75]
	v_mov_b64_e32 v[66:67], v[62:63]
	v_pk_mov_b32 v[190:191], v[188:189], v[114:115] op_sel:[1,0]
	v_mov_b32_e32 v189, v115
	v_mov_b64_e32 v[64:65], v[60:61]
	v_pk_add_f32 v[114:115], v[190:191], v[188:189]
	v_mov_b64_e32 v[70:71], v[58:59]
	v_mul_f32_e32 v111, v64, v64
	v_mul_f32_e32 v188, v65, v65
	v_pk_add_f32 v[112:113], v[112:113], v[112:113] op_sel:[0,1] op_sel_hi:[1,0]
	v_pk_add_f32 v[114:115], v[114:115], v[114:115] op_sel:[0,1] op_sel_hi:[1,0]
	v_mov_b64_e32 v[68:69], v[56:57]
	v_mov_b32_e32 v113, v111
	v_mov_b32_e32 v115, v188
	v_pk_add_f32 v[112:113], v[112:113], v[114:115]
	v_mul_f32_e32 v114, v69, v69
	v_mul_f32_e32 v189, v66, v66
	v_pk_fma_f32 v[114:115], v[68:69], v[68:69], v[114:115] op_sel_hi:[1,1,0]
	v_mul_f32_e32 v188, v71, v71
	v_mul_f32_e32 v190, v67, v67
	v_mov_b32_e32 v115, v189
	v_pk_fma_f32 v[188:189], v[70:71], v[70:71], v[188:189] op_sel_hi:[1,1,0]
	s_mov_b32 s20, s0
	v_mov_b32_e32 v189, v190
	v_pk_add_f32 v[114:115], v[114:115], v[188:189]
	s_add_i32 s0, s0, 8
	v_pk_add_f32 v[112:113], v[112:113], v[114:115]
	s_cmp_ge_i32 s0, s3
	v_add_f32_e32 v111, v112, v113
	s_cselect_b64 s[22:23], -1, 0
	s_cmp_lt_i32 s0, s3
	v_add_f32_dpp v111, v111, v111 quad_perm:[1,0,3,2] row_mask:0xf bank_mask:0xf bound_ctrl:1
	s_cselect_b32 s20, s0, s20
	s_ashr_i32 s21, s20, 31
	v_add_f32_dpp v111, v111, v111 quad_perm:[2,3,0,1] row_mask:0xf bank_mask:0xf bound_ctrl:1
	ds_swizzle_b32 v112, v111 offset:swizzle(SWAP,4)
	s_lshl_b64 s[20:21], s[20:21], 13
	v_lshl_add_u64 v[48:49], v[96:97], 0, s[20:21]
	v_add_co_u32_e32 v60, vcc, s30, v48
	s_waitcnt lgkmcnt(0)
	v_add_f32_e32 v111, v111, v112
	ds_swizzle_b32 v112, v111 offset:swizzle(SWAP,8)
	v_addc_co_u32_e32 v61, vcc, 0, v49, vcc
	s_mov_b32 s20, 0xf800000
	global_load_dwordx4 v[32:35], v[48:49], off
	global_load_dwordx4 v[36:39], v[48:49], off offset:1024
	global_load_dwordx4 v[40:43], v[48:49], off offset:2048
	global_load_dwordx4 v[44:47], v[48:49], off offset:3072
	s_waitcnt lgkmcnt(0)
	v_add_f32_e32 v111, v111, v112
	ds_swizzle_b32 v112, v111 offset:swizzle(SWAP,16)
	global_load_dwordx4 v[48:51], v[60:61], off
	global_load_dwordx4 v[52:55], v[60:61], off offset:1024
	global_load_dwordx4 v[56:59], v[60:61], off offset:2048
	s_nop 0
	global_load_dwordx4 v[60:63], v[60:61], off offset:3072
	s_waitcnt lgkmcnt(0)
	v_add_f32_e32 v111, v111, v112
	ds_bpermute_b32 v112, v116, v111
	s_waitcnt lgkmcnt(0)
; #define LAS __attribute__((address_space(3)))
; DI unsigned pk2(float lo, float hi) { const f32x2 v = {lo, hi}; return __builtin_bit_cast(unsigned, __builtin_convertvector(v, bf16x2_t)); }
; DI unsigned pk4_fp8(float a, float b, float c, float d) { unsigned w = 0u; w = __builtin_amdgcn_cvt_pk_fp8_f32(a, b, w, false); w = __builtin_amdgcn_cvt_pk_fp8_f32(c, d, w, true); return w; }
; DI float wave_sum(float v) { v += shx<1>(v); v += shx<2>(v); v += shx<4>(v); v += shx<8>(v); v += shx<16>(v); v += shx<32>(v); return v; }
; template <int MODE, bool SB  > DI void norm_phase(const Params& P, const Frame& F, int L, const void* src_, const float* gain, bool combine) {
;     ...
;         const float rstd = 1.0f / sqrtf(wave_sum(ss) * (1.0f / D) + EPS);
; #pragma unroll
;         for (int j = 0; j < 8; ++j) v[j] = v[j] * rstd * g[j];
;         if (MODE == 4) {
; #pragma unroll
;             for (int j = 0; j < 8; ++j) *(f32x4*)(P.out + (size_t)row * D + 4 * F.lane + 256 * j) = v[j];
;         } else if (MODE == 0 || MODE == 2 || (MODE == 3 && L == 1)) {
;             unsigned* o4 = (unsigned*)((unsigned char*)HN + (size_t)row * D) + F.lane; const float hs = (float)(1 << LS_HN);
; #pragma unroll
;             for (int j = 0; j < 8; ++j) o4[64 * j] = pk4_fp8(v[j][0] * hs, v[j][1] * hs, v[j][2] * hs, v[j][3] * hs);
;         } else {
;             unsigned long long* o8 = (unsigned long long*)(HN + (size_t)row * D) + F.lane;
; #pragma unroll
;             for (int j = 0; j < 8; ++j) o8[64 * j] = (unsigned long long)pk2(v[j][0], v[j][1]) | ((unsigned long long)pk2(v[j][2], v[j][3]) << 32);
;         }
;         if (MODE == 1) {
;             float s[16];
; #pragma unroll
;             for (int q = 0; q < 16; ++q) { float t = 0.f;
; #pragma unroll
;                 for (int j = 0; j < 8; ++j) { const f32x4 w = *(const LAS f32x4*)(F.lds + (size_t)(q * D + 256 * j + 4 * F.lane) * 4); t += (v[j][0] * w[0] + v[j][1] * w[1]) + (v[j][2] * w[2] + v[j][3] * w[3]); }
;                 s[q] = t; if ((q & 3) == 3) asm volatile("" ::: "memory"); }
	v_add_f32_e32 v111, v111, v112
	v_fmamk_f32 v111, v111, 0x3a000000, v182
	v_cmp_gt_f32_e32 vcc, s20, v111
	v_mul_f32_e32 v112, 0x4f800000, v111
	s_nop 0
	v_cndmask_b32_e32 v111, v111, v112, vcc
	v_sqrt_f32_e32 v112, v111
	s_nop 0
	v_add_u32_e32 v113, -1, v112
	v_fma_f32 v114, -v113, v112, v111
	v_cmp_ge_f32_e64 s[20:21], 0, v114
	v_add_u32_e32 v114, 1, v112
	s_nop 0
	v_cndmask_b32_e64 v113, v112, v113, s[20:21]
	v_fma_f32 v112, -v114, v112, v111
	v_cmp_lt_f32_e64 s[20:21], 0, v112
	s_nop 1
	v_cndmask_b32_e64 v112, v113, v114, s[20:21]
	v_mul_f32_e32 v113, 0x37800000, v112
	v_cndmask_b32_e32 v112, v112, v113, vcc
	v_cmp_class_f32_e32 vcc, v111, v183
	s_nop 1
	v_cndmask_b32_e32 v111, v112, v111, vcc
	v_div_scale_f32 v112, s[20:21], v111, v111, 1.0
	v_rcp_f32_e32 v113, v112
	s_mov_b32 s20, 0x3d600000
	v_fma_f32 v114, -v112, v113, 1.0
	v_fmac_f32_e32 v113, v114, v113
	v_div_scale_f32 v114, vcc, 1.0, v111, 1.0
	v_mul_f32_e32 v115, v114, v113
	v_fma_f32 v188, -v112, v115, v114
	v_fmac_f32_e32 v115, v188, v113
	v_fma_f32 v112, -v112, v115, v114
	v_div_fmas_f32 v112, v112, v113, v115
	v_div_fixup_f32 v188, v112, v111, 1.0
	v_pk_mul_f32 v[94:95], v[94:95], v[188:189] op_sel_hi:[1,0]
	v_pk_mul_f32 v[88:89], v[88:89], v[188:189] op_sel_hi:[1,0]
	v_pk_mul_f32 v[86:87], v[86:87], v[188:189] op_sel_hi:[1,0]
	v_pk_mul_f32 v[80:81], v[80:81], v[188:189] op_sel_hi:[1,0]
	v_pk_mul_f32 v[78:79], v[78:79], v[188:189] op_sel_hi:[1,0]
	v_pk_mul_f32 v[72:73], v[72:73], v[188:189] op_sel_hi:[1,0]
	v_pk_mul_f32 v[70:71], v[70:71], v[188:189] op_sel_hi:[1,0]
	v_pk_mul_f32 v[64:65], v[64:65], v[188:189] op_sel_hi:[1,0]
	v_pk_mul_f32 v[92:93], v[92:93], v[188:189] op_sel_hi:[1,0]
	v_pk_mul_f32 v[112:113], v[2:3], v[94:95]
	v_pk_mul_f32 v[94:95], v[4:5], v[88:89]
	v_pk_mul_f32 v[88:89], v[10:11], v[86:87]
	v_pk_mul_f32 v[86:87], v[12:13], v[80:81]
	v_pk_mul_f32 v[80:81], v[18:19], v[78:79]
	v_pk_mul_f32 v[78:79], v[20:21], v[72:73]
	v_pk_mul_f32 v[72:73], v[26:27], v[70:71]
	v_pk_mul_f32 v[70:71], v[28:29], v[64:65]
	v_lshl_add_u64 v[64:65], s[54:55], 0, v[108:109]
	v_pk_mul_f32 v[114:115], v[0:1], v[92:93]
	v_pk_mul_f32 v[90:91], v[90:91], v[188:189] op_sel_hi:[1,0]
	v_pk_mul_f32 v[84:85], v[84:85], v[188:189] op_sel_hi:[1,0]
	v_pk_mul_f32 v[82:83], v[82:83], v[188:189] op_sel_hi:[1,0]
	v_pk_mul_f32 v[76:77], v[76:77], v[188:189] op_sel_hi:[1,0]
	v_pk_mul_f32 v[74:75], v[74:75], v[188:189] op_sel_hi:[1,0]
	v_pk_mul_f32 v[68:69], v[68:69], v[188:189] op_sel_hi:[1,0]
	v_pk_mul_f32 v[66:67], v[66:67], v[188:189] op_sel_hi:[1,0]
	v_add_co_u32_e32 v64, vcc, s20, v64
	v_pk_mul_f32 v[92:93], v[6:7], v[90:91]
	v_pk_mul_f32 v[90:91], v[8:9], v[84:85]
	v_pk_mul_f32 v[84:85], v[14:15], v[82:83]
	v_pk_mul_f32 v[82:83], v[16:17], v[76:77]
	v_pk_mul_f32 v[76:77], v[22:23], v[74:75]
	v_pk_mul_f32 v[74:75], v[24:25], v[68:69]
	v_pk_mul_f32 v[68:69], v[30:31], v[66:67]
	v_cvt_pk_bf16_f32 v66, v114, v115
	v_cvt_pk_bf16_f32 v67, v112, v113
	v_addc_co_u32_e32 v65, vcc, 0, v65, vcc
	global_store_dwordx2 v[64:65], v[66:67], off
	v_cvt_pk_bf16_f32 v66, v94, v95
	v_cvt_pk_bf16_f32 v67, v92, v93
	global_store_dwordx2 v[64:65], v[66:67], off offset:512
	v_cvt_pk_bf16_f32 v66, v90, v91
	v_cvt_pk_bf16_f32 v67, v88, v89
	global_store_dwordx2 v[64:65], v[66:67], off offset:1024
	v_cvt_pk_bf16_f32 v66, v86, v87
	v_cvt_pk_bf16_f32 v67, v84, v85
	global_store_dwordx2 v[64:65], v[66:67], off offset:1536
	v_cvt_pk_bf16_f32 v66, v82, v83
	v_cvt_pk_bf16_f32 v67, v80, v81
	global_store_dwordx2 v[64:65], v[66:67], off offset:2048
	v_cvt_pk_bf16_f32 v66, v78, v79
	v_cvt_pk_bf16_f32 v67, v76, v77
	global_store_dwordx2 v[64:65], v[66:67], off offset:2560
	v_cvt_pk_bf16_f32 v66, v74, v75
	v_cvt_pk_bf16_f32 v67, v72, v73
	global_store_dwordx2 v[64:65], v[66:67], off offset:3072
	v_cvt_pk_bf16_f32 v66, v70, v71
	v_cvt_pk_bf16_f32 v67, v68, v69
	global_store_dwordx2 v[64:65], v[66:67], off offset:3584
	ds_read_b128 v[216:219], v117
	ds_read_b128 v[220:223], v117 offset:1024
	ds_read_b128 v[224:227], v117 offset:2048
	ds_read_b128 v[228:231], v117 offset:3072
	ds_read_b128 v[232:235], v117 offset:4096
	ds_read_b128 v[236:239], v117 offset:5120
	ds_read_b128 v[240:243], v117 offset:6144
	ds_read_b128 v[248:251], v117 offset:7168
	s_waitcnt lgkmcnt(7)
	v_mul_f32_e32 v217, v217, v115
	v_fmac_f32_e32 v217, v216, v114
	v_mul_f32_e32 v216, v219, v113
	v_fmac_f32_e32 v216, v218, v112
	v_add_f32_e32 v216, v217, v216
	v_add_f32_e32 v111, 0, v216
	ds_read_b128 v[216:219], v117 offset:8192
	s_waitcnt lgkmcnt(7)
	v_mul_f32_e32 v221, v95, v221
	v_fmac_f32_e32 v221, v94, v220
	v_mul_f32_e32 v220, v93, v223
	v_fmac_f32_e32 v220, v92, v222
	v_add_f32_e32 v220, v221, v220
	v_add_f32_e32 v111, v220, v111
	ds_read_b128 v[220:223], v117 offset:9216
	s_waitcnt lgkmcnt(7)
	v_mul_f32_e32 v225, v91, v225
	v_fmac_f32_e32 v225, v90, v224
	v_mul_f32_e32 v224, v89, v227
	v_fmac_f32_e32 v224, v88, v226
	v_add_f32_e32 v224, v225, v224
	v_add_f32_e32 v111, v224, v111
	ds_read_b128 v[224:227], v117 offset:10240
	s_waitcnt lgkmcnt(7)
	v_mul_f32_e32 v229, v87, v229
	v_fmac_f32_e32 v229, v86, v228
	v_mul_f32_e32 v228, v85, v231
	v_fmac_f32_e32 v228, v84, v230
	v_add_f32_e32 v228, v229, v228
	v_add_f32_e32 v111, v228, v111
	ds_read_b128 v[228:231], v117 offset:11264
	s_waitcnt lgkmcnt(7)
	v_mul_f32_e32 v233, v83, v233
	v_fmac_f32_e32 v233, v82, v232
	v_mul_f32_e32 v232, v81, v235
	v_fmac_f32_e32 v232, v80, v234
	v_add_f32_e32 v232, v233, v232
	v_add_f32_e32 v111, v232, v111
	ds_read_b128 v[232:235], v117 offset:12288
	s_waitcnt lgkmcnt(7)
; #define LAS __attribute__((address_space(3)))
; template <int MODE, bool SB  > DI void norm_phase(const Params& P, const Frame& F, int L, const void* src_, const float* gain, bool combine) {
;     ...
;             for (int q = 0; q < 16; ++q) { float t = 0.f;
; #pragma unroll
;                 for (int j = 0; j < 8; ++j) { const f32x4 w = *(const LAS f32x4*)(F.lds + (size_t)(q * D + 256 * j + 4 * F.lane) * 4); t += (v[j][0] * w[0] + v[j][1] * w[1]) + (v[j][2] * w[2] + v[j][3] * w[3]); }
;                 s[q] = t; if ((q & 3) == 3) asm volatile("" ::: "memory"); }
	v_mul_f32_e32 v237, v79, v237
	v_fmac_f32_e32 v237, v78, v236
	v_mul_f32_e32 v236, v77, v239
	v_fmac_f32_e32 v236, v76, v238
	v_add_f32_e32 v236, v237, v236
	v_add_f32_e32 v111, v236, v111
	ds_read_b128 v[236:239], v117 offset:13312
	s_waitcnt lgkmcnt(7)
	v_mul_f32_e32 v241, v75, v241
	v_fmac_f32_e32 v241, v74, v240
	v_mul_f32_e32 v240, v73, v243
	v_fmac_f32_e32 v240, v72, v242
	v_add_f32_e32 v240, v241, v240
	v_add_f32_e32 v111, v240, v111
	ds_read_b128 v[240:243], v117 offset:14336
	s_waitcnt lgkmcnt(7)
	v_mul_f32_e32 v249, v71, v249
	v_fmac_f32_e32 v249, v70, v248
	v_mul_f32_e32 v248, v69, v251
	v_fmac_f32_e32 v248, v68, v250
	v_add_f32_e32 v248, v249, v248
	v_add_f32_e32 v111, v248, v111
	ds_read_b128 v[248:251], v117 offset:15360
	s_waitcnt lgkmcnt(7)
	v_mul_f32_e32 v217, v115, v217
	v_fmac_f32_e32 v217, v114, v216
	v_mul_f32_e32 v216, v113, v219
	v_fmac_f32_e32 v216, v112, v218
	v_add_f32_e32 v216, v217, v216
	v_add_f32_e32 v188, 0, v216
	ds_read_b128 v[216:219], v117 offset:16384
	s_waitcnt lgkmcnt(7)
	v_mul_f32_e32 v221, v95, v221
	v_fmac_f32_e32 v221, v94, v220
	v_mul_f32_e32 v220, v93, v223
	v_fmac_f32_e32 v220, v92, v222
	v_add_f32_e32 v220, v221, v220
	v_add_f32_e32 v188, v188, v220
	ds_read_b128 v[220:223], v117 offset:17408
	s_waitcnt lgkmcnt(7)
	v_mul_f32_e32 v225, v91, v225
	v_fmac_f32_e32 v225, v90, v224
	v_mul_f32_e32 v224, v89, v227
	v_fmac_f32_e32 v224, v88, v226
	v_add_f32_e32 v224, v225, v224
	v_add_f32_e32 v188, v188, v224
	ds_read_b128 v[224:227], v117 offset:18432
	s_waitcnt lgkmcnt(7)
	v_mul_f32_e32 v229, v87, v229
	v_fmac_f32_e32 v229, v86, v228
	v_mul_f32_e32 v228, v85, v231
	v_fmac_f32_e32 v228, v84, v230
	v_add_f32_e32 v228, v229, v228
	v_add_f32_e32 v188, v188, v228
	ds_read_b128 v[228:231], v117 offset:19456
	s_waitcnt lgkmcnt(7)
	v_mul_f32_e32 v233, v83, v233
	v_fmac_f32_e32 v233, v82, v232
	v_mul_f32_e32 v232, v81, v235
	v_fmac_f32_e32 v232, v80, v234
	v_add_f32_e32 v232, v233, v232
	v_add_f32_e32 v188, v188, v232
	ds_read_b128 v[232:235], v117 offset:20480
	s_waitcnt lgkmcnt(7)
	v_mul_f32_e32 v237, v79, v237
	v_fmac_f32_e32 v237, v78, v236
	v_mul_f32_e32 v236, v77, v239
	v_fmac_f32_e32 v236, v76, v238
	v_add_f32_e32 v236, v237, v236
	v_add_f32_e32 v188, v188, v236
	ds_read_b128 v[236:239], v117 offset:21504
	s_waitcnt lgkmcnt(7)
	v_mul_f32_e32 v241, v75, v241
	v_fmac_f32_e32 v241, v74, v240
	v_mul_f32_e32 v240, v73, v243
	v_fmac_f32_e32 v240, v72, v242
	v_add_f32_e32 v240, v241, v240
	v_add_f32_e32 v188, v188, v240
	ds_read_b128 v[240:243], v117 offset:22528
	s_waitcnt lgkmcnt(7)
	v_mul_f32_e32 v249, v71, v249
	v_fmac_f32_e32 v249, v70, v248
	v_mul_f32_e32 v248, v69, v251
	v_fmac_f32_e32 v248, v68, v250
	v_add_f32_e32 v248, v249, v248
	v_add_f32_e32 v188, v188, v248
	ds_read_b128 v[248:251], v117 offset:23552
	s_waitcnt lgkmcnt(7)
	v_mul_f32_e32 v217, v115, v217
	v_fmac_f32_e32 v217, v114, v216
	v_mul_f32_e32 v216, v113, v219
	v_fmac_f32_e32 v216, v112, v218
	v_add_f32_e32 v216, v217, v216
	v_add_f32_e32 v189, 0, v216
	ds_read_b128 v[216:219], v117 offset:24576
	s_waitcnt lgkmcnt(7)
	v_mul_f32_e32 v221, v95, v221
	v_fmac_f32_e32 v221, v94, v220
	v_mul_f32_e32 v220, v93, v223
	v_fmac_f32_e32 v220, v92, v222
	v_add_f32_e32 v220, v221, v220
	v_add_f32_e32 v189, v189, v220
	ds_read_b128 v[220:223], v117 offset:25600
	s_waitcnt lgkmcnt(7)
	v_mul_f32_e32 v225, v91, v225
	v_fmac_f32_e32 v225, v90, v224
	v_mul_f32_e32 v224, v89, v227
	v_fmac_f32_e32 v224, v88, v226
	v_add_f32_e32 v224, v225, v224
	v_add_f32_e32 v189, v189, v224
	ds_read_b128 v[224:227], v117 offset:26624
	s_waitcnt lgkmcnt(7)
	v_mul_f32_e32 v229, v87, v229
	v_fmac_f32_e32 v229, v86, v228
	v_mul_f32_e32 v228, v85, v231
	v_fmac_f32_e32 v228, v84, v230
	v_add_f32_e32 v228, v229, v228
	v_add_f32_e32 v189, v189, v228
	ds_read_b128 v[228:231], v117 offset:27648
	s_waitcnt lgkmcnt(7)
	v_mul_f32_e32 v233, v83, v233
	v_fmac_f32_e32 v233, v82, v232
	v_mul_f32_e32 v232, v81, v235
	v_fmac_f32_e32 v232, v80, v234
	v_add_f32_e32 v232, v233, v232
	v_add_f32_e32 v189, v189, v232
	ds_read_b128 v[232:235], v117 offset:28672
	s_waitcnt lgkmcnt(7)
	v_mul_f32_e32 v237, v79, v237
	v_fmac_f32_e32 v237, v78, v236
	v_mul_f32_e32 v236, v77, v239
	v_fmac_f32_e32 v236, v76, v238
	v_add_f32_e32 v236, v237, v236
	v_add_f32_e32 v189, v189, v236
	ds_read_b128 v[236:239], v117 offset:29696
	s_waitcnt lgkmcnt(7)
	v_mul_f32_e32 v241, v75, v241
	v_fmac_f32_e32 v241, v74, v240
	v_mul_f32_e32 v240, v73, v243
	v_fmac_f32_e32 v240, v72, v242
	v_add_f32_e32 v240, v241, v240
	v_add_f32_e32 v189, v189, v240
	ds_read_b128 v[240:243], v117 offset:30720
	s_waitcnt lgkmcnt(7)
	v_mul_f32_e32 v249, v71, v249
	v_fmac_f32_e32 v249, v70, v248
	v_mul_f32_e32 v248, v69, v251
	v_fmac_f32_e32 v248, v68, v250
	v_add_f32_e32 v248, v249, v248
	v_add_f32_e32 v189, v189, v248
	ds_read_b128 v[248:251], v117 offset:31744
	s_waitcnt lgkmcnt(7)
	v_mul_f32_e32 v217, v115, v217
	v_fmac_f32_e32 v217, v114, v216
	v_mul_f32_e32 v216, v113, v219
	v_fmac_f32_e32 v216, v112, v218
	v_add_f32_e32 v216, v217, v216
	v_add_f32_e32 v190, 0, v216
	ds_read_b128 v[216:219], v117 offset:32768
	s_waitcnt lgkmcnt(7)
	v_mul_f32_e32 v221, v95, v221
	v_fmac_f32_e32 v221, v94, v220
	v_mul_f32_e32 v220, v93, v223
	v_fmac_f32_e32 v220, v92, v222
	v_add_f32_e32 v220, v221, v220
	v_add_f32_e32 v190, v190, v220
	ds_read_b128 v[220:223], v117 offset:33792
	s_waitcnt lgkmcnt(7)
	v_mul_f32_e32 v225, v91, v225
	v_fmac_f32_e32 v225, v90, v224
	v_mul_f32_e32 v224, v89, v227
	v_fmac_f32_e32 v224, v88, v226
	v_add_f32_e32 v224, v225, v224
	v_add_f32_e32 v190, v190, v224
	ds_read_b128 v[224:227], v117 offset:34816
	s_waitcnt lgkmcnt(7)
; #define LAS __attribute__((address_space(3)))
; template <int MODE, bool SB  > DI void norm_phase(const Params& P, const Frame& F, int L, const void* src_, const float* gain, bool combine) {
;     ...
;             for (int q = 0; q < 16; ++q) { float t = 0.f;
; #pragma unroll
;                 for (int j = 0; j < 8; ++j) { const f32x4 w = *(const LAS f32x4*)(F.lds + (size_t)(q * D + 256 * j + 4 * F.lane) * 4); t += (v[j][0] * w[0] + v[j][1] * w[1]) + (v[j][2] * w[2] + v[j][3] * w[3]); }
;                 s[q] = t; if ((q & 3) == 3) asm volatile("" ::: "memory"); }
	v_mul_f32_e32 v229, v87, v229
	v_fmac_f32_e32 v229, v86, v228
	v_mul_f32_e32 v228, v85, v231
	v_fmac_f32_e32 v228, v84, v230
	v_add_f32_e32 v228, v229, v228
	v_add_f32_e32 v190, v190, v228
	ds_read_b128 v[228:231], v117 offset:35840
	s_waitcnt lgkmcnt(7)
	v_mul_f32_e32 v233, v83, v233
	v_fmac_f32_e32 v233, v82, v232
	v_mul_f32_e32 v232, v81, v235
	v_fmac_f32_e32 v232, v80, v234
	v_add_f32_e32 v232, v233, v232
	v_add_f32_e32 v190, v190, v232
	ds_read_b128 v[232:235], v117 offset:36864
	s_waitcnt lgkmcnt(7)
	v_mul_f32_e32 v237, v79, v237
	v_fmac_f32_e32 v237, v78, v236
	v_mul_f32_e32 v236, v77, v239
	v_fmac_f32_e32 v236, v76, v238
	v_add_f32_e32 v236, v237, v236
	v_add_f32_e32 v190, v190, v236
	ds_read_b128 v[236:239], v117 offset:37888
	s_waitcnt lgkmcnt(7)
	v_mul_f32_e32 v241, v75, v241
	v_fmac_f32_e32 v241, v74, v240
	v_mul_f32_e32 v240, v73, v243
	v_fmac_f32_e32 v240, v72, v242
	v_add_f32_e32 v240, v241, v240
	v_add_f32_e32 v190, v190, v240
	ds_read_b128 v[240:243], v117 offset:38912
	s_waitcnt lgkmcnt(7)
	v_mul_f32_e32 v249, v71, v249
	v_fmac_f32_e32 v249, v70, v248
	v_mul_f32_e32 v248, v69, v251
	v_fmac_f32_e32 v248, v68, v250
	v_add_f32_e32 v248, v249, v248
	v_add_f32_e32 v190, v190, v248
	ds_read_b128 v[248:251], v117 offset:39936
	s_waitcnt lgkmcnt(7)
	v_mul_f32_e32 v217, v115, v217
	v_fmac_f32_e32 v217, v114, v216
	v_mul_f32_e32 v216, v113, v219
	v_fmac_f32_e32 v216, v112, v218
	v_add_f32_e32 v216, v217, v216
	v_add_f32_e32 v191, 0, v216
	ds_read_b128 v[216:219], v117 offset:40960
	s_waitcnt lgkmcnt(7)
	v_mul_f32_e32 v221, v95, v221
	v_fmac_f32_e32 v221, v94, v220
	v_mul_f32_e32 v220, v93, v223
	v_fmac_f32_e32 v220, v92, v222
	v_add_f32_e32 v220, v221, v220
	v_add_f32_e32 v191, v191, v220
	ds_read_b128 v[220:223], v117 offset:41984
	s_waitcnt lgkmcnt(7)
	v_mul_f32_e32 v225, v91, v225
	v_fmac_f32_e32 v225, v90, v224
	v_mul_f32_e32 v224, v89, v227
	v_fmac_f32_e32 v224, v88, v226
	v_add_f32_e32 v224, v225, v224
	v_add_f32_e32 v191, v191, v224
	ds_read_b128 v[224:227], v117 offset:43008
	s_waitcnt lgkmcnt(7)
	v_mul_f32_e32 v229, v87, v229
	v_fmac_f32_e32 v229, v86, v228
	v_mul_f32_e32 v228, v85, v231
	v_fmac_f32_e32 v228, v84, v230
	v_add_f32_e32 v228, v229, v228
	v_add_f32_e32 v191, v191, v228
	ds_read_b128 v[228:231], v117 offset:44032
	s_waitcnt lgkmcnt(7)
	v_mul_f32_e32 v233, v83, v233
	v_fmac_f32_e32 v233, v82, v232
	v_mul_f32_e32 v232, v81, v235
	v_fmac_f32_e32 v232, v80, v234
	v_add_f32_e32 v232, v233, v232
	v_add_f32_e32 v191, v191, v232
	ds_read_b128 v[232:235], v117 offset:45056
	s_waitcnt lgkmcnt(7)
	v_mul_f32_e32 v237, v79, v237
	v_fmac_f32_e32 v237, v78, v236
	v_mul_f32_e32 v236, v77, v239
	v_fmac_f32_e32 v236, v76, v238
	v_add_f32_e32 v236, v237, v236
	v_add_f32_e32 v191, v191, v236
	ds_read_b128 v[236:239], v117 offset:46080
	s_waitcnt lgkmcnt(7)
	v_mul_f32_e32 v241, v75, v241
	v_fmac_f32_e32 v241, v74, v240
	v_mul_f32_e32 v240, v73, v243
	v_fmac_f32_e32 v240, v72, v242
	v_add_f32_e32 v240, v241, v240
	v_add_f32_e32 v191, v191, v240
	ds_read_b128 v[240:243], v117 offset:47104
	s_waitcnt lgkmcnt(7)
	v_mul_f32_e32 v249, v71, v249
	v_fmac_f32_e32 v249, v70, v248
	v_mul_f32_e32 v248, v69, v251
	v_fmac_f32_e32 v248, v68, v250
	v_add_f32_e32 v248, v249, v248
	v_add_f32_e32 v191, v191, v248
	ds_read_b128 v[248:251], v117 offset:48128
	s_waitcnt lgkmcnt(7)
	v_mul_f32_e32 v217, v115, v217
	v_fmac_f32_e32 v217, v114, v216
	v_mul_f32_e32 v216, v113, v219
	v_fmac_f32_e32 v216, v112, v218
	v_add_f32_e32 v216, v217, v216
	v_add_f32_e32 v192, 0, v216
	ds_read_b128 v[216:219], v117 offset:49152
	s_waitcnt lgkmcnt(7)
	v_mul_f32_e32 v221, v95, v221
	v_fmac_f32_e32 v221, v94, v220
	v_mul_f32_e32 v220, v93, v223
	v_fmac_f32_e32 v220, v92, v222
	v_add_f32_e32 v220, v221, v220
	v_add_f32_e32 v192, v192, v220
	ds_read_b128 v[220:223], v117 offset:50176
	s_waitcnt lgkmcnt(7)
	v_mul_f32_e32 v225, v91, v225
	v_fmac_f32_e32 v225, v90, v224
	v_mul_f32_e32 v224, v89, v227
	v_fmac_f32_e32 v224, v88, v226
	v_add_f32_e32 v224, v225, v224
	v_add_f32_e32 v192, v192, v224
	ds_read_b128 v[224:227], v117 offset:51200
	s_waitcnt lgkmcnt(7)
	v_mul_f32_e32 v229, v87, v229
	v_fmac_f32_e32 v229, v86, v228
	v_mul_f32_e32 v228, v85, v231
	v_fmac_f32_e32 v228, v84, v230
	v_add_f32_e32 v228, v229, v228
	v_add_f32_e32 v192, v192, v228
	ds_read_b128 v[228:231], v117 offset:52224
	s_waitcnt lgkmcnt(7)
	v_mul_f32_e32 v233, v83, v233
	v_fmac_f32_e32 v233, v82, v232
	v_mul_f32_e32 v232, v81, v235
	v_fmac_f32_e32 v232, v80, v234
	v_add_f32_e32 v232, v233, v232
	v_add_f32_e32 v192, v192, v232
	ds_read_b128 v[232:235], v117 offset:53248
	s_waitcnt lgkmcnt(7)
	v_mul_f32_e32 v237, v79, v237
	v_fmac_f32_e32 v237, v78, v236
	v_mul_f32_e32 v236, v77, v239
	v_fmac_f32_e32 v236, v76, v238
	v_add_f32_e32 v236, v237, v236
	v_add_f32_e32 v192, v192, v236
	ds_read_b128 v[236:239], v117 offset:54272
	s_waitcnt lgkmcnt(7)
	v_mul_f32_e32 v241, v75, v241
	v_fmac_f32_e32 v241, v74, v240
	v_mul_f32_e32 v240, v73, v243
	v_fmac_f32_e32 v240, v72, v242
	v_add_f32_e32 v240, v241, v240
	v_add_f32_e32 v192, v192, v240
	ds_read_b128 v[240:243], v117 offset:55296
	s_waitcnt lgkmcnt(7)
	v_mul_f32_e32 v249, v71, v249
	v_fmac_f32_e32 v249, v70, v248
	v_mul_f32_e32 v248, v69, v251
	v_fmac_f32_e32 v248, v68, v250
	v_add_f32_e32 v248, v249, v248
	v_add_f32_e32 v193, v192, v248
	ds_read_b128 v[248:251], v117 offset:56320
	s_waitcnt lgkmcnt(7)
	v_mul_f32_e32 v217, v115, v217
	v_fmac_f32_e32 v217, v114, v216
	v_mul_f32_e32 v216, v113, v219
	v_fmac_f32_e32 v216, v112, v218
	v_add_f32_e32 v216, v217, v216
	v_add_f32_e32 v192, 0, v216
	ds_read_b128 v[216:219], v117 offset:57344
	s_waitcnt lgkmcnt(7)
; #define LAS __attribute__((address_space(3)))
; template <int MODE, bool SB  > DI void norm_phase(const Params& P, const Frame& F, int L, const void* src_, const float* gain, bool combine) {
;     ...
;             for (int q = 0; q < 16; ++q) { float t = 0.f;
; #pragma unroll
;                 for (int j = 0; j < 8; ++j) { const f32x4 w = *(const LAS f32x4*)(F.lds + (size_t)(q * D + 256 * j + 4 * F.lane) * 4); t += (v[j][0] * w[0] + v[j][1] * w[1]) + (v[j][2] * w[2] + v[j][3] * w[3]); }
;                 s[q] = t; if ((q & 3) == 3) asm volatile("" ::: "memory"); }
	v_mul_f32_e32 v221, v95, v221
	v_fmac_f32_e32 v221, v94, v220
	v_mul_f32_e32 v220, v93, v223
	v_fmac_f32_e32 v220, v92, v222
	v_add_f32_e32 v220, v221, v220
	v_add_f32_e32 v192, v192, v220
	ds_read_b128 v[220:223], v117 offset:58368
	s_waitcnt lgkmcnt(7)
	v_mul_f32_e32 v225, v91, v225
	v_fmac_f32_e32 v225, v90, v224
	v_mul_f32_e32 v224, v89, v227
	v_fmac_f32_e32 v224, v88, v226
	v_add_f32_e32 v224, v225, v224
	v_add_f32_e32 v192, v192, v224
	ds_read_b128 v[224:227], v117 offset:59392
	s_waitcnt lgkmcnt(7)
	v_mul_f32_e32 v229, v87, v229
	v_fmac_f32_e32 v229, v86, v228
	v_mul_f32_e32 v228, v85, v231
	v_fmac_f32_e32 v228, v84, v230
	v_add_f32_e32 v228, v229, v228
	v_add_f32_e32 v192, v192, v228
	ds_read_b128 v[228:231], v117 offset:60416
	s_waitcnt lgkmcnt(7)
	v_mul_f32_e32 v233, v83, v233
	v_fmac_f32_e32 v233, v82, v232
	v_mul_f32_e32 v232, v81, v235
	v_fmac_f32_e32 v232, v80, v234
	v_add_f32_e32 v232, v233, v232
	v_add_f32_e32 v192, v192, v232
	ds_read_b128 v[232:235], v117 offset:61440
	s_waitcnt lgkmcnt(7)
	v_mul_f32_e32 v237, v79, v237
	v_fmac_f32_e32 v237, v78, v236
	v_mul_f32_e32 v236, v77, v239
	v_fmac_f32_e32 v236, v76, v238
	v_add_f32_e32 v236, v237, v236
	v_add_f32_e32 v192, v192, v236
	ds_read_b128 v[236:239], v117 offset:62464
	s_waitcnt lgkmcnt(7)
	v_mul_f32_e32 v241, v75, v241
	v_fmac_f32_e32 v241, v74, v240
	v_mul_f32_e32 v240, v73, v243
	v_fmac_f32_e32 v240, v72, v242
	v_add_f32_e32 v240, v241, v240
	v_add_f32_e32 v192, v192, v240
	ds_read_b128 v[240:243], v117 offset:63488
	s_waitcnt lgkmcnt(7)
	v_mul_f32_e32 v249, v71, v249
	v_fmac_f32_e32 v249, v70, v248
	v_mul_f32_e32 v248, v69, v251
	v_fmac_f32_e32 v248, v68, v250
	v_add_f32_e32 v248, v249, v248
	v_add_f32_e32 v194, v192, v248
	ds_read_b128 v[248:251], v117 offset:64512
	s_waitcnt lgkmcnt(7)
	v_mul_f32_e32 v217, v115, v217
	v_fmac_f32_e32 v217, v114, v216
	v_mul_f32_e32 v216, v113, v219
	v_fmac_f32_e32 v216, v112, v218
	v_add_f32_e32 v216, v217, v216
	v_add_f32_e32 v192, 0, v216
	ds_read_b128 v[216:219], v118
	s_waitcnt lgkmcnt(7)
	v_mul_f32_e32 v221, v95, v221
	v_fmac_f32_e32 v221, v94, v220
	v_mul_f32_e32 v220, v93, v223
	v_fmac_f32_e32 v220, v92, v222
	v_add_f32_e32 v220, v221, v220
	v_add_f32_e32 v192, v192, v220
	ds_read_b128 v[220:223], v119
	s_waitcnt lgkmcnt(7)
	v_mul_f32_e32 v225, v91, v225
	v_fmac_f32_e32 v225, v90, v224
	v_mul_f32_e32 v224, v89, v227
	v_fmac_f32_e32 v224, v88, v226
	v_add_f32_e32 v224, v225, v224
	v_add_f32_e32 v192, v192, v224
	ds_read_b128 v[224:227], v120
	s_waitcnt lgkmcnt(7)
	v_mul_f32_e32 v229, v87, v229
	v_fmac_f32_e32 v229, v86, v228
	v_mul_f32_e32 v228, v85, v231
	v_fmac_f32_e32 v228, v84, v230
	v_add_f32_e32 v228, v229, v228
	v_add_f32_e32 v192, v192, v228
	ds_read_b128 v[228:231], v121
	s_waitcnt lgkmcnt(7)
	v_mul_f32_e32 v233, v83, v233
	v_fmac_f32_e32 v233, v82, v232
	v_mul_f32_e32 v232, v81, v235
	v_fmac_f32_e32 v232, v80, v234
	v_add_f32_e32 v232, v233, v232
	v_add_f32_e32 v192, v192, v232
	ds_read_b128 v[232:235], v122
	s_waitcnt lgkmcnt(7)
	v_mul_f32_e32 v237, v79, v237
	v_fmac_f32_e32 v237, v78, v236
	v_mul_f32_e32 v236, v77, v239
	v_fmac_f32_e32 v236, v76, v238
	v_add_f32_e32 v236, v237, v236
	v_add_f32_e32 v192, v192, v236
	ds_read_b128 v[236:239], v123
	s_waitcnt lgkmcnt(7)
	v_mul_f32_e32 v241, v75, v241
	v_fmac_f32_e32 v241, v74, v240
	v_mul_f32_e32 v240, v73, v243
	v_fmac_f32_e32 v240, v72, v242
	v_add_f32_e32 v240, v241, v240
	v_add_f32_e32 v192, v192, v240
	ds_read_b128 v[240:243], v124
	s_waitcnt lgkmcnt(7)
	v_mul_f32_e32 v249, v71, v249
	v_fmac_f32_e32 v249, v70, v248
	v_mul_f32_e32 v248, v69, v251
	v_fmac_f32_e32 v248, v68, v250
	v_add_f32_e32 v248, v249, v248
	v_add_f32_e32 v195, v192, v248
	ds_read_b128 v[248:251], v125
	s_waitcnt lgkmcnt(7)
	v_mul_f32_e32 v217, v115, v217
	v_fmac_f32_e32 v217, v114, v216
	v_mul_f32_e32 v216, v113, v219
	v_fmac_f32_e32 v216, v112, v218
	v_add_f32_e32 v216, v217, v216
	v_add_f32_e32 v192, 0, v216
	ds_read_b128 v[216:219], v126
	s_waitcnt lgkmcnt(7)
	v_mul_f32_e32 v221, v95, v221
	v_fmac_f32_e32 v221, v94, v220
	v_mul_f32_e32 v220, v93, v223
	v_fmac_f32_e32 v220, v92, v222
	v_add_f32_e32 v220, v221, v220
	v_add_f32_e32 v192, v192, v220
	ds_read_b128 v[220:223], v127
	s_waitcnt lgkmcnt(7)
	v_mul_f32_e32 v225, v91, v225
	v_fmac_f32_e32 v225, v90, v224
	v_mul_f32_e32 v224, v89, v227
	v_fmac_f32_e32 v224, v88, v226
	v_add_f32_e32 v224, v225, v224
	v_add_f32_e32 v192, v192, v224
	ds_read_b128 v[224:227], v128
	s_waitcnt lgkmcnt(7)
	v_mul_f32_e32 v229, v87, v229
	v_fmac_f32_e32 v229, v86, v228
	v_mul_f32_e32 v228, v85, v231
	v_fmac_f32_e32 v228, v84, v230
	v_add_f32_e32 v228, v229, v228
	v_add_f32_e32 v192, v192, v228
	ds_read_b128 v[228:231], v129
	s_waitcnt lgkmcnt(7)
	v_mul_f32_e32 v233, v83, v233
	v_fmac_f32_e32 v233, v82, v232
	v_mul_f32_e32 v232, v81, v235
	v_fmac_f32_e32 v232, v80, v234
	v_add_f32_e32 v232, v233, v232
	v_add_f32_e32 v192, v192, v232
	ds_read_b128 v[232:235], v130
	s_waitcnt lgkmcnt(7)
	v_mul_f32_e32 v237, v79, v237
	v_fmac_f32_e32 v237, v78, v236
	v_mul_f32_e32 v236, v77, v239
	v_fmac_f32_e32 v236, v76, v238
	v_add_f32_e32 v236, v237, v236
	v_add_f32_e32 v192, v192, v236
	ds_read_b128 v[236:239], v131
	s_waitcnt lgkmcnt(7)
	v_mul_f32_e32 v241, v75, v241
	v_fmac_f32_e32 v241, v74, v240
	v_mul_f32_e32 v240, v73, v243
	v_fmac_f32_e32 v240, v72, v242
	v_add_f32_e32 v240, v241, v240
	v_add_f32_e32 v192, v192, v240
	ds_read_b128 v[240:243], v132
	s_waitcnt lgkmcnt(7)
	v_mul_f32_e32 v249, v71, v249
	v_fmac_f32_e32 v249, v70, v248
	v_mul_f32_e32 v248, v69, v251
	v_fmac_f32_e32 v248, v68, v250
	v_add_f32_e32 v248, v249, v248
	v_add_f32_e32 v196, v192, v248
	ds_read_b128 v[248:251], v133
	s_waitcnt lgkmcnt(7)
; #define LAS __attribute__((address_space(3)))
; template <int MODE, bool SB  > DI void norm_phase(const Params& P, const Frame& F, int L, const void* src_, const float* gain, bool combine) {
;     ...
;             for (int q = 0; q < 16; ++q) { float t = 0.f;
; #pragma unroll
;                 for (int j = 0; j < 8; ++j) { const f32x4 w = *(const LAS f32x4*)(F.lds + (size_t)(q * D + 256 * j + 4 * F.lane) * 4); t += (v[j][0] * w[0] + v[j][1] * w[1]) + (v[j][2] * w[2] + v[j][3] * w[3]); }
;                 s[q] = t; if ((q & 3) == 3) asm volatile("" ::: "memory"); }
	v_mul_f32_e32 v217, v115, v217
	v_fmac_f32_e32 v217, v114, v216
	v_mul_f32_e32 v216, v113, v219
	v_fmac_f32_e32 v216, v112, v218
	v_add_f32_e32 v216, v217, v216
	v_add_f32_e32 v192, 0, v216
	ds_read_b128 v[216:219], v134
	s_waitcnt lgkmcnt(7)
	v_mul_f32_e32 v221, v95, v221
	v_fmac_f32_e32 v221, v94, v220
	v_mul_f32_e32 v220, v93, v223
	v_fmac_f32_e32 v220, v92, v222
	v_add_f32_e32 v220, v221, v220
	v_add_f32_e32 v192, v192, v220
	ds_read_b128 v[220:223], v135
	s_waitcnt lgkmcnt(7)
	v_mul_f32_e32 v225, v91, v225
	v_fmac_f32_e32 v225, v90, v224
	v_mul_f32_e32 v224, v89, v227
	v_fmac_f32_e32 v224, v88, v226
	v_add_f32_e32 v224, v225, v224
	v_add_f32_e32 v192, v192, v224
	ds_read_b128 v[224:227], v136
	s_waitcnt lgkmcnt(7)
	v_mul_f32_e32 v229, v87, v229
	v_fmac_f32_e32 v229, v86, v228
	v_mul_f32_e32 v228, v85, v231
	v_fmac_f32_e32 v228, v84, v230
	v_add_f32_e32 v228, v229, v228
	v_add_f32_e32 v192, v192, v228
	ds_read_b128 v[228:231], v137
	s_waitcnt lgkmcnt(7)
	v_mul_f32_e32 v233, v83, v233
	v_fmac_f32_e32 v233, v82, v232
	v_mul_f32_e32 v232, v81, v235
	v_fmac_f32_e32 v232, v80, v234
	v_add_f32_e32 v232, v233, v232
	v_add_f32_e32 v192, v192, v232
	ds_read_b128 v[232:235], v138
	s_waitcnt lgkmcnt(7)
	v_mul_f32_e32 v237, v79, v237
	v_fmac_f32_e32 v237, v78, v236
	v_mul_f32_e32 v236, v77, v239
	v_fmac_f32_e32 v236, v76, v238
	v_add_f32_e32 v236, v237, v236
	v_add_f32_e32 v192, v192, v236
	ds_read_b128 v[236:239], v139
	s_waitcnt lgkmcnt(7)
	v_mul_f32_e32 v241, v75, v241
	v_fmac_f32_e32 v241, v74, v240
	v_mul_f32_e32 v240, v73, v243
	v_fmac_f32_e32 v240, v72, v242
	v_add_f32_e32 v240, v241, v240
	v_add_f32_e32 v192, v192, v240
	ds_read_b128 v[240:243], v140
	s_waitcnt lgkmcnt(7)
	v_mul_f32_e32 v249, v71, v249
	v_fmac_f32_e32 v249, v70, v248
	v_mul_f32_e32 v248, v69, v251
	v_fmac_f32_e32 v248, v68, v250
	v_add_f32_e32 v248, v249, v248
	v_add_f32_e32 v197, v192, v248
	ds_read_b128 v[248:251], v141
	s_waitcnt lgkmcnt(7)
	v_mul_f32_e32 v217, v115, v217
	v_fmac_f32_e32 v217, v114, v216
	v_mul_f32_e32 v216, v113, v219
	v_fmac_f32_e32 v216, v112, v218
	v_add_f32_e32 v216, v217, v216
	v_add_f32_e32 v192, 0, v216
	ds_read_b128 v[216:219], v142
	s_waitcnt lgkmcnt(7)
	v_mul_f32_e32 v221, v95, v221
	v_fmac_f32_e32 v221, v94, v220
	v_mul_f32_e32 v220, v93, v223
	v_fmac_f32_e32 v220, v92, v222
	v_add_f32_e32 v220, v221, v220
	v_add_f32_e32 v192, v192, v220
	ds_read_b128 v[220:223], v143
	s_waitcnt lgkmcnt(7)
	v_mul_f32_e32 v225, v91, v225
	v_fmac_f32_e32 v225, v90, v224
	v_mul_f32_e32 v224, v89, v227
	v_fmac_f32_e32 v224, v88, v226
	v_add_f32_e32 v224, v225, v224
	v_add_f32_e32 v192, v192, v224
	ds_read_b128 v[224:227], v144
	s_waitcnt lgkmcnt(7)
	v_mul_f32_e32 v229, v87, v229
	v_fmac_f32_e32 v229, v86, v228
	v_mul_f32_e32 v228, v85, v231
	v_fmac_f32_e32 v228, v84, v230
	v_add_f32_e32 v228, v229, v228
	v_add_f32_e32 v192, v192, v228
	ds_read_b128 v[228:231], v145
	s_waitcnt lgkmcnt(7)
	v_mul_f32_e32 v233, v83, v233
	v_fmac_f32_e32 v233, v82, v232
	v_mul_f32_e32 v232, v81, v235
	v_fmac_f32_e32 v232, v80, v234
	v_add_f32_e32 v232, v233, v232
	v_add_f32_e32 v192, v192, v232
	ds_read_b128 v[232:235], v146
	s_waitcnt lgkmcnt(7)
	v_mul_f32_e32 v237, v79, v237
	v_fmac_f32_e32 v237, v78, v236
	v_mul_f32_e32 v236, v77, v239
	v_fmac_f32_e32 v236, v76, v238
	v_add_f32_e32 v236, v237, v236
	v_add_f32_e32 v192, v192, v236
	ds_read_b128 v[236:239], v147
	s_waitcnt lgkmcnt(7)
	v_mul_f32_e32 v241, v75, v241
	v_fmac_f32_e32 v241, v74, v240
	v_mul_f32_e32 v240, v73, v243
	v_fmac_f32_e32 v240, v72, v242
	v_add_f32_e32 v240, v241, v240
	v_add_f32_e32 v192, v192, v240
	ds_read_b128 v[240:243], v148
	s_waitcnt lgkmcnt(7)
	v_mul_f32_e32 v249, v71, v249
	v_fmac_f32_e32 v249, v70, v248
	v_mul_f32_e32 v248, v69, v251
	v_fmac_f32_e32 v248, v68, v250
	v_add_f32_e32 v248, v249, v248
	v_add_f32_e32 v198, v192, v248
	ds_read_b128 v[248:251], v149
	s_waitcnt lgkmcnt(7)
	v_mul_f32_e32 v217, v115, v217
	v_fmac_f32_e32 v217, v114, v216
	v_mul_f32_e32 v216, v113, v219
	v_fmac_f32_e32 v216, v112, v218
	v_add_f32_e32 v216, v217, v216
	v_add_f32_e32 v192, 0, v216
	ds_read_b128 v[216:219], v150
	s_waitcnt lgkmcnt(7)
	v_mul_f32_e32 v221, v95, v221
	v_fmac_f32_e32 v221, v94, v220
	v_mul_f32_e32 v220, v93, v223
	v_fmac_f32_e32 v220, v92, v222
	v_add_f32_e32 v220, v221, v220
	v_add_f32_e32 v192, v192, v220
	ds_read_b128 v[220:223], v151
	s_waitcnt lgkmcnt(7)
	v_mul_f32_e32 v225, v91, v225
	v_fmac_f32_e32 v225, v90, v224
	v_mul_f32_e32 v224, v89, v227
	v_fmac_f32_e32 v224, v88, v226
	v_add_f32_e32 v224, v225, v224
	v_add_f32_e32 v192, v192, v224
	ds_read_b128 v[224:227], v152
	s_waitcnt lgkmcnt(7)
	v_mul_f32_e32 v229, v87, v229
	v_fmac_f32_e32 v229, v86, v228
	v_mul_f32_e32 v228, v85, v231
	v_fmac_f32_e32 v228, v84, v230
	v_add_f32_e32 v228, v229, v228
	v_add_f32_e32 v192, v192, v228
	ds_read_b128 v[228:231], v153
	s_waitcnt lgkmcnt(7)
	v_mul_f32_e32 v233, v83, v233
	v_fmac_f32_e32 v233, v82, v232
	v_mul_f32_e32 v232, v81, v235
	v_fmac_f32_e32 v232, v80, v234
	v_add_f32_e32 v232, v233, v232
	v_add_f32_e32 v192, v192, v232
	ds_read_b128 v[232:235], v154
	s_waitcnt lgkmcnt(7)
	v_mul_f32_e32 v237, v79, v237
	v_fmac_f32_e32 v237, v78, v236
	v_mul_f32_e32 v236, v77, v239
	v_fmac_f32_e32 v236, v76, v238
	v_add_f32_e32 v236, v237, v236
	v_add_f32_e32 v192, v192, v236
	ds_read_b128 v[236:239], v155
	s_waitcnt lgkmcnt(7)
	v_mul_f32_e32 v241, v75, v241
	v_fmac_f32_e32 v241, v74, v240
	v_mul_f32_e32 v240, v73, v243
	v_fmac_f32_e32 v240, v72, v242
	v_add_f32_e32 v240, v241, v240
	v_add_f32_e32 v192, v192, v240
	ds_read_b128 v[240:243], v156
	s_waitcnt lgkmcnt(7)
; #define LAS __attribute__((address_space(3)))
; template <int MODE, bool SB  > DI void norm_phase(const Params& P, const Frame& F, int L, const void* src_, const float* gain, bool combine) {
;     ...
;             for (int q = 0; q < 16; ++q) { float t = 0.f;
; #pragma unroll
;                 for (int j = 0; j < 8; ++j) { const f32x4 w = *(const LAS f32x4*)(F.lds + (size_t)(q * D + 256 * j + 4 * F.lane) * 4); t += (v[j][0] * w[0] + v[j][1] * w[1]) + (v[j][2] * w[2] + v[j][3] * w[3]); }
;                 s[q] = t; if ((q & 3) == 3) asm volatile("" ::: "memory"); }
	v_mul_f32_e32 v249, v71, v249
	v_fmac_f32_e32 v249, v70, v248
	v_mul_f32_e32 v248, v69, v251
	v_fmac_f32_e32 v248, v68, v250
	v_add_f32_e32 v248, v249, v248
	v_add_f32_e32 v199, v192, v248
	ds_read_b128 v[248:251], v157
	s_waitcnt lgkmcnt(7)
	v_mul_f32_e32 v217, v115, v217
	v_fmac_f32_e32 v217, v114, v216
	v_mul_f32_e32 v216, v113, v219
	v_fmac_f32_e32 v216, v112, v218
	v_add_f32_e32 v216, v217, v216
	v_add_f32_e32 v192, 0, v216
	ds_read_b128 v[216:219], v158
	s_waitcnt lgkmcnt(7)
	v_mul_f32_e32 v221, v95, v221
	v_fmac_f32_e32 v221, v94, v220
	v_mul_f32_e32 v220, v93, v223
	v_fmac_f32_e32 v220, v92, v222
	v_add_f32_e32 v220, v221, v220
	v_add_f32_e32 v192, v192, v220
	ds_read_b128 v[220:223], v159
	s_waitcnt lgkmcnt(7)
	v_mul_f32_e32 v225, v91, v225
	v_fmac_f32_e32 v225, v90, v224
	v_mul_f32_e32 v224, v89, v227
	v_fmac_f32_e32 v224, v88, v226
	v_add_f32_e32 v224, v225, v224
	v_add_f32_e32 v192, v192, v224
	ds_read_b128 v[224:227], v160
	s_waitcnt lgkmcnt(7)
	v_mul_f32_e32 v229, v87, v229
	v_fmac_f32_e32 v229, v86, v228
	v_mul_f32_e32 v228, v85, v231
	v_fmac_f32_e32 v228, v84, v230
	v_add_f32_e32 v228, v229, v228
	v_add_f32_e32 v192, v192, v228
	ds_read_b128 v[228:231], v161
	s_waitcnt lgkmcnt(7)
	v_mul_f32_e32 v233, v83, v233
	v_fmac_f32_e32 v233, v82, v232
	v_mul_f32_e32 v232, v81, v235
	v_fmac_f32_e32 v232, v80, v234
	v_add_f32_e32 v232, v233, v232
	v_add_f32_e32 v192, v192, v232
	ds_read_b128 v[232:235], v162
	s_waitcnt lgkmcnt(7)
	v_mul_f32_e32 v237, v79, v237
	v_fmac_f32_e32 v237, v78, v236
	v_mul_f32_e32 v236, v77, v239
	v_fmac_f32_e32 v236, v76, v238
	v_add_f32_e32 v236, v237, v236
	v_add_f32_e32 v192, v192, v236
	ds_read_b128 v[236:239], v163
	s_waitcnt lgkmcnt(7)
	v_mul_f32_e32 v241, v75, v241
	v_fmac_f32_e32 v241, v74, v240
	v_mul_f32_e32 v240, v73, v243
	v_fmac_f32_e32 v240, v72, v242
	v_add_f32_e32 v240, v241, v240
	v_add_f32_e32 v192, v192, v240
	ds_read_b128 v[240:243], v164
	s_waitcnt lgkmcnt(7)
	v_mul_f32_e32 v249, v71, v249
	v_fmac_f32_e32 v249, v70, v248
	v_mul_f32_e32 v248, v69, v251
	v_fmac_f32_e32 v248, v68, v250
	v_add_f32_e32 v248, v249, v248
	v_add_f32_e32 v200, v192, v248
	ds_read_b128 v[248:251], v165
	s_waitcnt lgkmcnt(7)
	v_mul_f32_e32 v217, v115, v217
	v_fmac_f32_e32 v217, v114, v216
	v_mul_f32_e32 v216, v113, v219
	v_fmac_f32_e32 v216, v112, v218
	v_add_f32_e32 v216, v217, v216
	v_add_f32_e32 v192, 0, v216
	ds_read_b128 v[216:219], v166
	s_waitcnt lgkmcnt(7)
	v_mul_f32_e32 v221, v95, v221
	v_fmac_f32_e32 v221, v94, v220
	v_mul_f32_e32 v220, v93, v223
	v_fmac_f32_e32 v220, v92, v222
	v_add_f32_e32 v220, v221, v220
	v_add_f32_e32 v192, v192, v220
	ds_read_b128 v[220:223], v167
	s_waitcnt lgkmcnt(7)
	v_mul_f32_e32 v225, v91, v225
	v_fmac_f32_e32 v225, v90, v224
	v_mul_f32_e32 v224, v89, v227
	v_fmac_f32_e32 v224, v88, v226
	v_add_f32_e32 v224, v225, v224
	v_add_f32_e32 v192, v192, v224
	ds_read_b128 v[224:227], v168
	s_waitcnt lgkmcnt(7)
	v_mul_f32_e32 v229, v87, v229
	v_fmac_f32_e32 v229, v86, v228
	v_mul_f32_e32 v228, v85, v231
	v_fmac_f32_e32 v228, v84, v230
	v_add_f32_e32 v228, v229, v228
	v_add_f32_e32 v192, v192, v228
	ds_read_b128 v[228:231], v169
	s_waitcnt lgkmcnt(7)
	v_mul_f32_e32 v233, v83, v233
	v_fmac_f32_e32 v233, v82, v232
	v_mul_f32_e32 v232, v81, v235
	v_fmac_f32_e32 v232, v80, v234
	v_add_f32_e32 v232, v233, v232
	v_add_f32_e32 v192, v192, v232
	ds_read_b128 v[232:235], v170
	s_waitcnt lgkmcnt(7)
	v_mul_f32_e32 v237, v79, v237
	v_fmac_f32_e32 v237, v78, v236
	v_mul_f32_e32 v236, v77, v239
	v_fmac_f32_e32 v236, v76, v238
	v_add_f32_e32 v236, v237, v236
	v_add_f32_e32 v192, v192, v236
	ds_read_b128 v[236:239], v171
	s_waitcnt lgkmcnt(7)
	v_mul_f32_e32 v241, v75, v241
	v_fmac_f32_e32 v241, v74, v240
	v_mul_f32_e32 v240, v73, v243
	v_fmac_f32_e32 v240, v72, v242
	v_add_f32_e32 v240, v241, v240
	v_add_f32_e32 v192, v192, v240
	ds_read_b128 v[240:243], v172
	s_waitcnt lgkmcnt(7)
	v_mul_f32_e32 v249, v71, v249
	v_fmac_f32_e32 v249, v70, v248
	v_mul_f32_e32 v248, v69, v251
	v_fmac_f32_e32 v248, v68, v250
	v_add_f32_e32 v248, v249, v248
	v_add_f32_e32 v201, v192, v248
	ds_read_b128 v[248:251], v173
	s_waitcnt lgkmcnt(7)
	v_mul_f32_e32 v217, v115, v217
	v_fmac_f32_e32 v217, v114, v216
	v_mul_f32_e32 v216, v113, v219
	v_fmac_f32_e32 v216, v112, v218
	v_add_f32_e32 v216, v217, v216
	v_add_f32_e32 v192, 0, v216
	ds_read_b128 v[216:219], v174
	s_waitcnt lgkmcnt(7)
	v_mul_f32_e32 v221, v95, v221
	v_fmac_f32_e32 v221, v94, v220
	v_mul_f32_e32 v220, v93, v223
	v_fmac_f32_e32 v220, v92, v222
	v_add_f32_e32 v220, v221, v220
	v_add_f32_e32 v192, v192, v220
	ds_read_b128 v[220:223], v175
	s_waitcnt lgkmcnt(7)
	v_mul_f32_e32 v225, v91, v225
	v_fmac_f32_e32 v225, v90, v224
	v_mul_f32_e32 v224, v89, v227
	v_fmac_f32_e32 v224, v88, v226
	v_add_f32_e32 v224, v225, v224
	v_add_f32_e32 v192, v192, v224
	ds_read_b128 v[224:227], v176
	s_waitcnt lgkmcnt(7)
	v_mul_f32_e32 v229, v87, v229
	v_fmac_f32_e32 v229, v86, v228
	v_mul_f32_e32 v228, v85, v231
	v_fmac_f32_e32 v228, v84, v230
	v_add_f32_e32 v228, v229, v228
	v_add_f32_e32 v192, v192, v228
	ds_read_b128 v[228:231], v177
	s_waitcnt lgkmcnt(7)
	v_mul_f32_e32 v233, v83, v233
	v_fmac_f32_e32 v233, v82, v232
	v_mul_f32_e32 v232, v81, v235
	v_fmac_f32_e32 v232, v80, v234
	v_add_f32_e32 v232, v233, v232
	v_add_f32_e32 v192, v192, v232
	ds_read_b128 v[232:235], v178
	s_waitcnt lgkmcnt(7)
	v_mul_f32_e32 v237, v79, v237
	v_fmac_f32_e32 v237, v78, v236
	v_mul_f32_e32 v236, v77, v239
	v_fmac_f32_e32 v236, v76, v238
	v_add_f32_e32 v236, v237, v236
	v_add_f32_e32 v192, v192, v236
	ds_read_b128 v[236:239], v179
	s_waitcnt lgkmcnt(7)
; #define LAS __attribute__((address_space(3)))
; DI float sigmoidf_(float x) { return __builtin_amdgcn_rcpf(1.0f + __expf(-x)); }
; DI float softplusf_(float x) { return fmaxf(x, 0.f) + log1pf(__expf(-fabsf(x))); }
; template <int MODE, bool SB  > DI void norm_phase(const Params& P, const Frame& F, int L, const void* src_, const float* gain, bool combine) {
;     ...
;                 for (int j = 0; j < 8; ++j) { const f32x4 w = *(const LAS f32x4*)(F.lds + (size_t)(q * D + 256 * j + 4 * F.lane) * 4); t += (v[j][0] * w[0] + v[j][1] * w[1]) + (v[j][2] * w[2] + v[j][3] * w[3]); }
;                 s[q] = t; if ((q & 3) == 3) asm volatile("" ::: "memory"); }
; #pragma unroll
;             for (int i = 0; i < 8; ++i) { const bool hi = (F.lane & 32) != 0; const float send = hi ? s[i] : s[i + 8], keep = hi ? s[i + 8] : s[i]; s[i] = keep + shx<32>(send); }
; #pragma unroll
;             for (int i = 0; i < 4; ++i) { const bool hi = (F.lane & 16) != 0; const float send = hi ? s[i] : s[i + 4], keep = hi ? s[i + 4] : s[i]; s[i] = keep + shx<16>(send); }
; #pragma unroll
;             for (int i = 0; i < 2; ++i) { const bool hi = (F.lane & 8) != 0; const float send = hi ? s[i] : s[i + 2], keep = hi ? s[i + 2] : s[i]; s[i] = keep + shx<8>(send); }
;             { const bool hi = (F.lane & 4) != 0; const float send = hi ? s[0] : s[1], keep = hi ? s[1] : s[0]; s[0] = keep + shx<4>(send); }
;             float mine = s[0]; mine += shx<2>(mine); mine += shx<1>(mine);
;             if ((F.lane & 3) == 0) { const int gi = ((F.lane >> 5) & 1) * 8 + ((F.lane >> 4) & 1) * 4 + ((F.lane >> 3) & 1) * 2 + ((F.lane >> 2) & 1), h = gi & 3; float r;
;                 if (gi < 4) r = sigmoidf_(mine);
;                 else if (gi < 8) r = -__expf(P.in[I_DN_A_LOG][L * 4 + h]) * softplusf_(mine + P.in[I_DN_DT_BIAS][L * 4 + h]);
;                 else if (gi < 12) r = mine + P.in[I_ML_I_BIAS][L * 4 + h];
;                 else r = -softplusf_(-(mine + P.in[I_ML_F_BIAS][L * 4 + h]));
;                 ((float*)(ws + WS_GD))[(size_t)row * 16 + gi] = r; }
	v_mul_f32_e32 v241, v75, v241
	v_fmac_f32_e32 v241, v74, v240
	v_mul_f32_e32 v240, v73, v243
	v_fmac_f32_e32 v240, v72, v242
	v_add_f32_e32 v240, v241, v240
	v_add_f32_e32 v192, v192, v240
	ds_read_b128 v[240:243], v180
	s_waitcnt lgkmcnt(7)
	v_mul_f32_e32 v249, v71, v249
	v_fmac_f32_e32 v249, v70, v248
	v_mul_f32_e32 v248, v69, v251
	v_fmac_f32_e32 v248, v68, v250
	v_add_f32_e32 v248, v249, v248
	v_add_f32_e32 v202, v192, v248
	ds_read_b128 v[64:67], v181
	s_waitcnt lgkmcnt(7)
	v_mul_f32_e32 v217, v115, v217
	v_fmac_f32_e32 v217, v114, v216
	v_mul_f32_e32 v216, v113, v219
	v_fmac_f32_e32 v216, v112, v218
	v_add_f32_e32 v216, v217, v216
	v_add_f32_e32 v112, 0, v216
	s_waitcnt lgkmcnt(6)
	v_mul_f32_e32 v221, v95, v221
	v_fmac_f32_e32 v221, v94, v220
	v_mul_f32_e32 v220, v93, v223
	v_fmac_f32_e32 v220, v92, v222
	v_add_f32_e32 v220, v221, v220
	v_add_f32_e32 v92, v112, v220
	s_waitcnt lgkmcnt(5)
	v_mul_f32_e32 v225, v91, v225
	v_fmac_f32_e32 v225, v90, v224
	v_mul_f32_e32 v224, v89, v227
	v_fmac_f32_e32 v224, v88, v226
	v_add_f32_e32 v224, v225, v224
	v_add_f32_e32 v88, v92, v224
	s_waitcnt lgkmcnt(4)
	v_mul_f32_e32 v229, v87, v229
	v_fmac_f32_e32 v229, v86, v228
	v_mul_f32_e32 v228, v85, v231
	v_fmac_f32_e32 v228, v84, v230
	v_add_f32_e32 v228, v229, v228
	v_add_f32_e32 v84, v88, v228
	s_waitcnt lgkmcnt(3)
	v_mul_f32_e32 v233, v83, v233
	v_fmac_f32_e32 v233, v82, v232
	v_mul_f32_e32 v232, v81, v235
	v_fmac_f32_e32 v232, v80, v234
	v_add_f32_e32 v232, v233, v232
	v_add_f32_e32 v80, v84, v232
	s_waitcnt lgkmcnt(2)
	v_mul_f32_e32 v237, v79, v237
	v_fmac_f32_e32 v237, v78, v236
	v_mul_f32_e32 v236, v77, v239
	v_fmac_f32_e32 v236, v76, v238
	v_add_f32_e32 v236, v237, v236
	v_add_f32_e32 v76, v80, v236
	s_waitcnt lgkmcnt(1)
	v_mul_f32_e32 v241, v75, v241
	v_fmac_f32_e32 v241, v74, v240
	v_mul_f32_e32 v240, v73, v243
	v_fmac_f32_e32 v240, v72, v242
	v_add_f32_e32 v240, v241, v240
	v_add_f32_e32 v72, v76, v240
	s_waitcnt lgkmcnt(0)
	v_mul_f32_e32 v65, v71, v65
	v_fmac_f32_e32 v65, v70, v64
	v_mul_f32_e32 v64, v69, v67
	v_fmac_f32_e32 v64, v68, v66
	v_add_f32_e32 v64, v65, v64
	v_cndmask_b32_e64 v65, v111, v196, s[4:5]
	ds_bpermute_b32 v65, v116, v65
	v_cndmask_b32_e64 v66, v196, v111, s[4:5]
	v_cndmask_b32_e64 v67, v197, v188, s[4:5]
	v_cndmask_b32_e64 v68, v198, v189, s[4:5]
	v_cndmask_b32_e64 v69, v199, v190, s[4:5]
	s_waitcnt lgkmcnt(0)
	v_add_f32_e32 v65, v66, v65
	v_cndmask_b32_e64 v66, v188, v197, s[4:5]
	ds_bpermute_b32 v66, v116, v66
	v_cndmask_b32_e64 v70, v200, v191, s[4:5]
	v_cndmask_b32_e64 v71, v201, v193, s[4:5]
	v_add_f32_e32 v64, v72, v64
	v_cndmask_b32_e64 v72, v202, v194, s[4:5]
	s_waitcnt lgkmcnt(0)
	v_add_f32_e32 v66, v67, v66
	v_cndmask_b32_e64 v67, v189, v198, s[4:5]
	ds_bpermute_b32 v67, v116, v67
	s_waitcnt lgkmcnt(0)
	v_add_f32_e32 v67, v68, v67
	v_cndmask_b32_e64 v68, v190, v199, s[4:5]
	ds_bpermute_b32 v68, v116, v68
	s_waitcnt lgkmcnt(0)
	v_add_f32_e32 v68, v69, v68
	v_cndmask_b32_e64 v69, v191, v200, s[4:5]
	ds_bpermute_b32 v69, v116, v69
	s_waitcnt lgkmcnt(0)
	v_add_f32_e32 v69, v70, v69
	v_cndmask_b32_e64 v70, v193, v201, s[4:5]
	ds_bpermute_b32 v70, v116, v70
	s_waitcnt lgkmcnt(0)
	v_add_f32_e32 v70, v71, v70
	v_cndmask_b32_e64 v71, v194, v202, s[4:5]
	ds_bpermute_b32 v71, v116, v71
	s_waitcnt lgkmcnt(0)
	v_add_f32_e32 v71, v72, v71
	v_cndmask_b32_e64 v72, v195, v64, s[4:5]
	ds_bpermute_b32 v72, v116, v72
	v_cndmask_b32_e64 v64, v64, v195, s[4:5]
	s_waitcnt lgkmcnt(0)
	v_add_f32_e32 v64, v64, v72
	v_cndmask_b32_e64 v72, v65, v69, s[8:9]
	v_cndmask_b32_e64 v65, v69, v65, s[8:9]
	ds_swizzle_b32 v69, v72 offset:swizzle(SWAP,16)
	s_waitcnt lgkmcnt(0)
	v_add_f32_e32 v65, v65, v69
	v_cndmask_b32_e64 v69, v66, v70, s[8:9]
	ds_swizzle_b32 v69, v69 offset:swizzle(SWAP,16)
	v_cndmask_b32_e64 v66, v70, v66, s[8:9]
	s_waitcnt lgkmcnt(0)
	v_add_f32_e32 v66, v66, v69
	v_cndmask_b32_e64 v69, v67, v71, s[8:9]
	ds_swizzle_b32 v69, v69 offset:swizzle(SWAP,16)
	v_cndmask_b32_e64 v67, v71, v67, s[8:9]
	s_waitcnt lgkmcnt(0)
	v_add_f32_e32 v67, v67, v69
	v_cndmask_b32_e64 v69, v68, v64, s[8:9]
	v_cndmask_b32_e64 v64, v64, v68, s[8:9]
	ds_swizzle_b32 v68, v69 offset:swizzle(SWAP,16)
	s_waitcnt lgkmcnt(0)
	v_add_f32_e32 v64, v64, v68
	v_cndmask_b32_e64 v68, v65, v67, s[10:11]
	v_cndmask_b32_e64 v65, v67, v65, s[10:11]
	ds_swizzle_b32 v67, v68 offset:swizzle(SWAP,8)
	s_waitcnt lgkmcnt(0)
	v_add_f32_e32 v65, v65, v67
	v_cndmask_b32_e64 v67, v66, v64, s[10:11]
	v_cndmask_b32_e64 v64, v64, v66, s[10:11]
	ds_swizzle_b32 v66, v67 offset:swizzle(SWAP,8)
	s_waitcnt lgkmcnt(0)
	v_add_f32_e32 v64, v64, v66
	v_cndmask_b32_e64 v66, v65, v64, s[12:13]
	v_cndmask_b32_e64 v64, v64, v65, s[12:13]
	ds_swizzle_b32 v65, v66 offset:swizzle(SWAP,4)
	s_waitcnt lgkmcnt(0)
	v_add_f32_e32 v64, v64, v65
	s_nop 1
	v_add_f32_dpp v64, v64, v64 quad_perm:[2,3,0,1] row_mask:0xf bank_mask:0xf bound_ctrl:1
	s_nop 1
	v_mov_b32_dpp v65, v64 quad_perm:[1,0,3,2] row_mask:0xf bank_mask:0xf bound_ctrl:1
	s_and_saveexec_b64 s[20:21], s[14:15]
	s_cbranch_execz .LBB0_82
	v_add_f32_e32 v65, v64, v65
	s_and_saveexec_b64 s[24:25], s[16:17]
	s_xor_b64 s[24:25], exec, s[24:25]
	s_cbranch_execz .LBB0_94
	s_and_saveexec_b64 s[26:27], s[6:7]
	s_xor_b64 s[26:27], exec, s[26:27]
	s_cbranch_execz .LBB0_91
	s_and_saveexec_b64 s[28:29], s[18:19]
	s_xor_b64 s[28:29], exec, s[28:29]
	s_cbranch_execz .LBB0_88
	v_mov_b32_e32 v64, v203
	v_add_f32_e32 v64, v65, v64
; DI float sigmoidf_(float x) { return __builtin_amdgcn_rcpf(1.0f + __expf(-x)); }
; DI float softplusf_(float x) { return fmaxf(x, 0.f) + log1pf(__expf(-fabsf(x))); }
; template <int MODE, bool SB  > DI void norm_phase(const Params& P, const Frame& F, int L, const void* src_, const float* gain, bool combine) {
;     ...
;             if ((F.lane & 3) == 0) { const int gi = ((F.lane >> 5) & 1) * 8 + ((F.lane >> 4) & 1) * 4 + ((F.lane >> 3) & 1) * 2 + ((F.lane >> 2) & 1), h = gi & 3; float r;
;                 if (gi < 4) r = sigmoidf_(mine);
;                 else if (gi < 8) r = -__expf(P.in[I_DN_A_LOG][L * 4 + h]) * softplusf_(mine + P.in[I_DN_DT_BIAS][L * 4 + h]);
;                 else if (gi < 12) r = mine + P.in[I_ML_I_BIAS][L * 4 + h];
;                 else r = -softplusf_(-(mine + P.in[I_ML_F_BIAS][L * 4 + h]));
;                 ((float*)(ws + WS_GD))[(size_t)row * 16 + gi] = r; }
.LBB0_88:
	s_andn2_saveexec_b64 s[28:29], s[28:29]
	s_cbranch_execz .LBB0_90
	v_mov_b32_e32 v64, v204
	v_add_f32_e32 v65, v65, v64
	v_max_f32_e64 v64, -v65, 0
	v_mul_f32_e64 v65, |v65|, s1
	v_exp_f32_e32 v65, v65
	s_nop 0
	v_add_f32_e32 v68, 1.0, v65
	v_add_f32_e32 v66, -1.0, v68
	v_sub_f32_e32 v67, v66, v68
	v_add_f32_e32 v67, 1.0, v67
	v_sub_f32_e32 v66, v65, v66
	v_add_f32_e32 v69, v66, v67
	v_frexp_mant_f32_e32 v66, v68
	v_cmp_gt_f32_e32 vcc, s31, v66
	v_cvt_f64_f32_e32 v[66:67], v68
	v_frexp_exp_i32_f64_e32 v66, v[66:67]
	v_subbrev_co_u32_e32 v74, vcc, 0, v66, vcc
	v_sub_u32_e32 v66, 0, v74
	v_ldexp_f32 v67, v68, v66
	v_add_f32_e32 v68, -1.0, v67
	v_add_f32_e32 v70, 1.0, v67
	v_ldexp_f32 v66, v69, v66
	v_add_f32_e32 v69, 1.0, v68
	v_add_f32_e32 v71, -1.0, v70
	v_sub_f32_e32 v69, v67, v69
	v_sub_f32_e32 v67, v67, v71
	v_add_f32_e32 v69, v66, v69
	v_add_f32_e32 v66, v66, v67
	v_add_f32_e32 v75, v70, v66
	v_rcp_f32_e32 v77, v75
	v_sub_f32_e32 v67, v75, v70
	v_sub_f32_e32 v76, v66, v67
	v_add_f32_e32 v67, v68, v69
	v_mul_f32_e32 v79, v67, v77
	v_sub_f32_e32 v66, v67, v68
	v_mul_f32_e32 v68, v75, v79
	v_fma_f32 v70, v79, v75, -v68
	v_fmac_f32_e32 v70, v79, v76
	v_sub_f32_e32 v78, v69, v66
	v_add_f32_e32 v66, v68, v70
	v_sub_f32_e32 v69, v67, v66
	v_pk_add_f32 v[72:73], v[66:67], v[68:69] neg_lo:[0,1] neg_hi:[0,1]
	v_mov_b32_e32 v71, v66
	v_pk_add_f32 v[66:67], v[72:73], v[70:71] neg_lo:[0,1] neg_hi:[0,1]
	v_cmp_neq_f32_e32 vcc, s34, v65
	v_add_f32_e32 v67, v78, v67
	v_add_f32_e32 v66, v66, v67
	v_add_f32_e32 v67, v69, v66
	v_mul_f32_e32 v78, v77, v67
	v_mul_f32_e32 v68, v75, v78
	v_fma_f32 v70, v78, v75, -v68
	v_fmac_f32_e32 v70, v78, v76
	v_sub_f32_e32 v69, v69, v67
	v_add_f32_e32 v75, v66, v69
	v_add_f32_e32 v66, v68, v70
	v_sub_f32_e32 v69, v67, v66
	v_pk_add_f32 v[72:73], v[66:67], v[68:69] neg_lo:[0,1] neg_hi:[0,1]
	v_mov_b32_e32 v71, v66
	v_pk_add_f32 v[66:67], v[72:73], v[70:71] neg_lo:[0,1] neg_hi:[0,1]
	s_nop 0
	v_add_f32_e32 v67, v75, v67
	v_add_f32_e32 v66, v66, v67
	v_add_f32_e32 v67, v79, v78
	v_add_f32_e32 v66, v69, v66
	v_sub_f32_e32 v68, v67, v79
	v_mul_f32_e32 v66, v77, v66
	v_sub_f32_e32 v68, v78, v68
	v_add_f32_e32 v68, v68, v66
	v_add_f32_e32 v70, v67, v68
	v_mul_f32_e32 v71, v70, v70
	v_fmamk_f32 v66, v71, 0x3e9b6dac, v184
	v_fmaak_f32 v111, v71, v66, 0x3f2aaada
	v_cvt_f32_i32_e32 v66, v74
	v_sub_f32_e32 v67, v70, v67
	v_sub_f32_e32 v67, v68, v67
	v_ldexp_f32 v72, v67, 1
	v_mul_f32_e32 v67, v70, v71
	v_ldexp_f32 v69, v70, 1
	v_pk_mul_f32 v[70:71], v[66:67], v[110:111]
	s_nop 0
	v_fma_f32 v68, v66, s33, -v70
	v_fmac_f32_e32 v68, 0xb102e308, v66
	v_pk_add_f32 v[66:67], v[70:71], v[68:69]
	s_nop 0
	v_sub_f32_e32 v69, v67, v69
	v_sub_f32_e32 v69, v71, v69
	v_add_f32_e32 v73, v72, v69
	v_mov_b32_e32 v72, v70
	v_pk_add_f32 v[70:71], v[66:67], v[70:71] neg_lo:[0,1] neg_hi:[0,1]
	v_pk_add_f32 v[74:75], v[66:67], v[72:73]
	v_mov_b32_e32 v69, v66
	v_mov_b32_e32 v71, v75
	v_pk_add_f32 v[76:77], v[68:69], v[70:71] neg_lo:[0,1] neg_hi:[0,1]
	v_pk_add_f32 v[68:69], v[68:69], v[70:71]
	v_mov_b32_e32 v72, v73
	v_pk_add_f32 v[70:71], v[68:69], v[66:67] op_sel:[1,0] op_sel_hi:[0,1] neg_lo:[0,1] neg_hi:[0,1]
	v_pk_add_f32 v[78:79], v[74:75], v[70:71] op_sel_hi:[1,0] neg_lo:[0,1] neg_hi:[0,1]
	v_mov_b32_e32 v74, v75
	v_mov_b32_e32 v75, v69
	v_pk_mov_b32 v[70:71], v[66:67], v[70:71] op_sel:[1,0]
	v_mov_b32_e32 v73, v66
	v_pk_add_f32 v[70:71], v[74:75], v[70:71] neg_lo:[0,1] neg_hi:[0,1]
	v_mov_b32_e32 v78, v76
	v_pk_add_f32 v[66:67], v[72:73], v[70:71] neg_lo:[0,1] neg_hi:[0,1]
	v_mov_b32_e32 v77, v69
	v_pk_add_f32 v[70:71], v[78:79], v[66:67]
	s_nop 0
	v_pk_add_f32 v[72:73], v[70:71], v[70:71] op_sel:[0,1] op_sel_hi:[1,0]
	s_nop 0
	v_pk_add_f32 v[68:69], v[68:69], v[72:73] op_sel:[1,0] op_sel_hi:[0,1]
	v_mov_b32_e32 v71, v68
	v_pk_add_f32 v[74:75], v[70:71], v[76:77] neg_lo:[0,1] neg_hi:[0,1]
	v_mov_b32_e32 v67, v72
	v_sub_f32_e32 v69, v70, v74
	v_pk_add_f32 v[66:67], v[66:67], v[74:75] neg_lo:[0,1] neg_hi:[0,1]
	v_sub_f32_e32 v69, v76, v69
	v_add_f32_e32 v66, v66, v69
	v_add_f32_e32 v66, v66, v67
	v_add_f32_e32 v66, v68, v66
	v_cndmask_b32_e32 v66, v185, v66, vcc
	v_cmp_ngt_f32_e32 vcc, -1.0, v65
	s_nop 1
	v_cndmask_b32_e32 v66, v186, v66, vcc
	v_cmp_neq_f32_e32 vcc, -1.0, v65
	s_nop 1
	v_cndmask_b32_e32 v66, v187, v66, vcc
	v_cmp_lt_f32_e64 vcc, |v65|, s35
	s_nop 1
	v_cndmask_b32_e32 v65, v66, v65, vcc
	v_add_f32_e32 v64, v64, v65
	v_xor_b32_e32 v64, 0x80000000, v64

; DI float sigmoidf_(float x) { return __builtin_amdgcn_rcpf(1.0f + __expf(-x)); }
; DI float softplusf_(float x) { return fmaxf(x, 0.f) + log1pf(__expf(-fabsf(x))); }
; template <int MODE, bool SB  > DI void norm_phase(const Params& P, const Frame& F, int L, const void* src_, const float* gain, bool combine) {
;     ...
;             if ((F.lane & 3) == 0) { const int gi = ((F.lane >> 5) & 1) * 8 + ((F.lane >> 4) & 1) * 4 + ((F.lane >> 3) & 1) * 2 + ((F.lane >> 2) & 1), h = gi & 3; float r;
;                 if (gi < 4) r = sigmoidf_(mine);
;                 else if (gi < 8) r = -__expf(P.in[I_DN_A_LOG][L * 4 + h]) * softplusf_(mine + P.in[I_DN_DT_BIAS][L * 4 + h]);
;                 else if (gi < 12) r = mine + P.in[I_ML_I_BIAS][L * 4 + h];
;                 else r = -softplusf_(-(mine + P.in[I_ML_F_BIAS][L * 4 + h]));
;                 ((float*)(ws + WS_GD))[(size_t)row * 16 + gi] = r; }
.LBB0_91:
	s_andn2_saveexec_b64 s[26:27], s[26:27]
	s_cbranch_execz .LBB0_93
	v_mov_b32_e32 v66, v205
	v_mov_b32_e32 v64, v206
	v_add_f32_e32 v66, v65, v66
	v_max_f32_e32 v65, 0, v66
	v_mul_f32_e64 v66, |v66|, s1
	v_exp_f32_e32 v66, v66
	v_mul_f32_e32 v64, 0x3fb8aa3b, v64
	v_exp_f32_e32 v64, v64
	v_add_f32_e32 v67, 1.0, v66
	v_add_f32_e32 v68, -1.0, v67
	v_sub_f32_e32 v69, v68, v67
	v_add_f32_e32 v69, 1.0, v69
	v_sub_f32_e32 v68, v66, v68
	v_add_f32_e32 v70, v68, v69
	v_frexp_mant_f32_e32 v68, v67
	v_cmp_gt_f32_e32 vcc, s31, v68
	v_cvt_f64_f32_e32 v[68:69], v67
	v_frexp_exp_i32_f64_e32 v68, v[68:69]
	v_subbrev_co_u32_e32 v76, vcc, 0, v68, vcc
	v_sub_u32_e32 v68, 0, v76
	v_ldexp_f32 v67, v67, v68
	v_ldexp_f32 v68, v70, v68
	v_add_f32_e32 v70, -1.0, v67
	v_add_f32_e32 v69, 1.0, v70
	v_sub_f32_e32 v69, v67, v69
	v_add_f32_e32 v71, v68, v69
	v_add_f32_e32 v69, 1.0, v67
	v_add_f32_e32 v72, -1.0, v69
	v_sub_f32_e32 v67, v67, v72
	v_add_f32_e32 v67, v68, v67
	v_add_f32_e32 v77, v69, v67
	v_rcp_f32_e32 v78, v77
	v_sub_f32_e32 v68, v77, v69
	v_add_f32_e32 v69, v70, v71
	v_sub_f32_e32 v67, v67, v68
	v_mul_f32_e32 v80, v69, v78
	v_sub_f32_e32 v68, v69, v70
	v_mul_f32_e32 v70, v77, v80
	v_fma_f32 v72, v80, v77, -v70
	v_fmac_f32_e32 v72, v80, v67
	v_sub_f32_e32 v79, v71, v68
	v_add_f32_e32 v68, v70, v72
	v_sub_f32_e32 v71, v69, v68
	v_pk_add_f32 v[74:75], v[68:69], v[70:71] neg_lo:[0,1] neg_hi:[0,1]
	v_mov_b32_e32 v73, v68
	v_pk_add_f32 v[68:69], v[74:75], v[72:73] neg_lo:[0,1] neg_hi:[0,1]
	v_cmp_neq_f32_e32 vcc, s34, v66
	v_add_f32_e32 v69, v79, v69
	v_add_f32_e32 v68, v68, v69
	v_add_f32_e32 v69, v71, v68
	v_mul_f32_e32 v79, v78, v69
	v_mul_f32_e32 v70, v77, v79
	v_fma_f32 v72, v79, v77, -v70
	v_fmac_f32_e32 v72, v79, v67
	v_sub_f32_e32 v67, v71, v69
	v_add_f32_e32 v67, v68, v67
	v_add_f32_e32 v68, v70, v72
	v_sub_f32_e32 v71, v69, v68
	v_pk_add_f32 v[74:75], v[68:69], v[70:71] neg_lo:[0,1] neg_hi:[0,1]
	v_mov_b32_e32 v73, v68
	v_pk_add_f32 v[68:69], v[74:75], v[72:73] neg_lo:[0,1] neg_hi:[0,1]
	s_nop 0
	v_add_f32_e32 v67, v67, v69
	v_add_f32_e32 v67, v68, v67
	v_add_f32_e32 v69, v80, v79
	v_add_f32_e32 v67, v71, v67
	v_sub_f32_e32 v68, v69, v80
	v_mul_f32_e32 v67, v78, v67
	v_sub_f32_e32 v68, v79, v68
	v_add_f32_e32 v67, v68, v67
	v_add_f32_e32 v70, v69, v67
	v_mul_f32_e32 v72, v70, v70
	v_fmamk_f32 v68, v72, 0x3e9b6dac, v184
	v_fmaak_f32 v111, v72, v68, 0x3f2aaada
	v_cvt_f32_i32_e32 v68, v76
	v_sub_f32_e32 v69, v70, v69
	v_sub_f32_e32 v67, v67, v69
	v_mul_f32_e32 v69, v70, v72
	v_pk_mul_f32 v[72:73], v[68:69], v[110:111]
	v_ldexp_f32 v71, v70, 1
	v_fma_f32 v70, v68, s33, -v72
	v_fmac_f32_e32 v70, 0xb102e308, v68
	v_pk_add_f32 v[68:69], v[72:73], v[70:71]
	v_ldexp_f32 v67, v67, 1
	v_sub_f32_e32 v71, v69, v71
	v_sub_f32_e32 v71, v73, v71
	v_add_f32_e32 v75, v67, v71
	v_mov_b32_e32 v74, v72
	v_pk_add_f32 v[72:73], v[68:69], v[72:73] neg_lo:[0,1] neg_hi:[0,1]
	v_pk_add_f32 v[76:77], v[68:69], v[74:75]
	v_mov_b32_e32 v71, v68
	v_mov_b32_e32 v73, v77
	v_pk_add_f32 v[78:79], v[70:71], v[72:73] neg_lo:[0,1] neg_hi:[0,1]
	v_pk_add_f32 v[70:71], v[70:71], v[72:73]
	v_mov_b32_e32 v74, v75
	v_pk_add_f32 v[72:73], v[70:71], v[68:69] op_sel:[1,0] op_sel_hi:[0,1] neg_lo:[0,1] neg_hi:[0,1]
	v_pk_add_f32 v[80:81], v[76:77], v[72:73] op_sel_hi:[1,0] neg_lo:[0,1] neg_hi:[0,1]
	v_mov_b32_e32 v76, v77
	v_mov_b32_e32 v77, v71
	v_pk_mov_b32 v[72:73], v[68:69], v[72:73] op_sel:[1,0]
	v_mov_b32_e32 v75, v68
	v_pk_add_f32 v[72:73], v[76:77], v[72:73] neg_lo:[0,1] neg_hi:[0,1]
	v_mov_b32_e32 v80, v78
	v_pk_add_f32 v[68:69], v[74:75], v[72:73] neg_lo:[0,1] neg_hi:[0,1]
	v_mov_b32_e32 v79, v71
	v_pk_add_f32 v[72:73], v[80:81], v[68:69]
	s_nop 0
	v_pk_add_f32 v[74:75], v[72:73], v[72:73] op_sel:[0,1] op_sel_hi:[1,0]
	s_nop 0
	v_pk_add_f32 v[70:71], v[70:71], v[74:75] op_sel:[1,0] op_sel_hi:[0,1]
	v_mov_b32_e32 v73, v70
	v_pk_add_f32 v[76:77], v[72:73], v[78:79] neg_lo:[0,1] neg_hi:[0,1]
	v_mov_b32_e32 v69, v74
	v_sub_f32_e32 v67, v72, v76
	v_pk_add_f32 v[68:69], v[68:69], v[76:77] neg_lo:[0,1] neg_hi:[0,1]
	v_sub_f32_e32 v67, v78, v67
	v_add_f32_e32 v67, v68, v67
	v_add_f32_e32 v67, v67, v69
	v_add_f32_e32 v67, v70, v67
	v_cndmask_b32_e32 v67, v185, v67, vcc
	v_cmp_ngt_f32_e32 vcc, -1.0, v66
	s_nop 1
	v_cndmask_b32_e32 v67, v186, v67, vcc
	v_cmp_neq_f32_e32 vcc, -1.0, v66
	s_nop 1
	v_cndmask_b32_e32 v67, v187, v67, vcc
	v_cmp_lt_f32_e64 vcc, |v66|, s35
	s_nop 1
	v_cndmask_b32_e32 v66, v67, v66, vcc
	v_add_f32_e32 v65, v65, v66
	v_mul_f32_e64 v64, v65, -v64

.LBB0_141:
	s_cmp_lt_u32 s3, 0x40001
	s_mov_b64 s[18:19], 0
	s_cselect_b64 s[20:21], -1, 0
	s_mov_b64 s[22:23], -1
	s_and_b64 vcc, exec, s[20:21]
	s_cbranch_vccnz .LBB0_138
	s_branch .LBB0_135
	s_nop 0
	s_nop 0
	s_nop 0

; #define LAS __attribute__((address_space(3)))
; template <int MODE, bool SB  > DI void norm_phase(const Params& P, const Frame& F, int L, const void* src_, const float* gain, bool combine) {
;     ...
;     if (MODE == 1) { const f32x4* w = (const f32x4*)((const float*)(ws + WS_WGT) + (size_t)L * 16 * D); for (int i = F.tid; i < 16 * D / 4; i += NTHR) ((LAS f32x4*)F.lds)[i] = w[i]; __syncthreads(); }
.LBB0_1643:
	global_load_dwordx4 v[190:193], v[0:1], off
	v_lshl_add_u64 v[0:1], v[0:1], 0, s[6:7]
	global_load_dwordx4 v[194:197], v[0:1], off
	v_lshl_add_u64 v[0:1], v[0:1], 0, s[6:7]
	global_load_dwordx4 v[198:201], v[0:1], off
	v_lshl_add_u64 v[0:1], v[0:1], 0, s[6:7]
	global_load_dwordx4 v[202:205], v[0:1], off
	v_lshl_add_u64 v[0:1], v[0:1], 0, s[6:7]
	global_load_dwordx4 v[206:209], v[0:1], off
	v_lshl_add_u64 v[0:1], v[0:1], 0, s[6:7]
	global_load_dwordx4 v[210:213], v[0:1], off
	v_lshl_add_u64 v[0:1], v[0:1], 0, s[6:7]
	global_load_dwordx4 v[214:217], v[0:1], off
	v_lshl_add_u64 v[0:1], v[0:1], 0, s[6:7]
	global_load_dwordx4 v[218:221], v[0:1], off
	v_lshl_add_u64 v[0:1], v[0:1], 0, s[6:7]
	global_load_dwordx4 v[222:225], v[0:1], off
	v_lshl_add_u64 v[0:1], v[0:1], 0, s[6:7]
	global_load_dwordx4 v[226:229], v[0:1], off
	v_lshl_add_u64 v[0:1], v[0:1], 0, s[6:7]
	global_load_dwordx4 v[230:233], v[0:1], off
	v_lshl_add_u64 v[0:1], v[0:1], 0, s[6:7]
	global_load_dwordx4 v[234:237], v[0:1], off
	v_lshl_add_u64 v[0:1], v[0:1], 0, s[6:7]
	global_load_dwordx4 v[238:241], v[0:1], off
	v_lshl_add_u64 v[0:1], v[0:1], 0, s[6:7]
	global_load_dwordx4 v[242:245], v[0:1], off
	v_lshl_add_u64 v[0:1], v[0:1], 0, s[6:7]
	global_load_dwordx4 v[246:249], v[0:1], off
	v_lshl_add_u64 v[0:1], v[0:1], 0, s[6:7]
	global_load_dwordx4 v[250:253], v[0:1], off
	s_waitcnt vmcnt(15)
	ds_write_b128 v3, v[190:193]
	v_add_u32_e32 v3, 0x2000, v3
	s_waitcnt vmcnt(14)
	ds_write_b128 v3, v[194:197]
	v_add_u32_e32 v3, 0x2000, v3
	s_waitcnt vmcnt(13)
	ds_write_b128 v3, v[198:201]
	v_add_u32_e32 v3, 0x2000, v3
	s_waitcnt vmcnt(12)
	ds_write_b128 v3, v[202:205]
	v_add_u32_e32 v3, 0x2000, v3
	s_waitcnt vmcnt(11)
	ds_write_b128 v3, v[206:209]
	v_add_u32_e32 v3, 0x2000, v3
	s_waitcnt vmcnt(10)
	ds_write_b128 v3, v[210:213]
	v_add_u32_e32 v3, 0x2000, v3
	s_waitcnt vmcnt(9)
	ds_write_b128 v3, v[214:217]
	v_add_u32_e32 v3, 0x2000, v3
	s_waitcnt vmcnt(8)
	ds_write_b128 v3, v[218:221]
	v_add_u32_e32 v3, 0x2000, v3
	s_waitcnt vmcnt(7)
	ds_write_b128 v3, v[222:225]
	v_add_u32_e32 v3, 0x2000, v3
	s_waitcnt vmcnt(6)
	ds_write_b128 v3, v[226:229]
	v_add_u32_e32 v3, 0x2000, v3
	s_waitcnt vmcnt(5)
	ds_write_b128 v3, v[230:233]
	v_add_u32_e32 v3, 0x2000, v3
	s_waitcnt vmcnt(4)
	ds_write_b128 v3, v[234:237]
	v_add_u32_e32 v3, 0x2000, v3
	s_waitcnt vmcnt(3)
	ds_write_b128 v3, v[238:241]
	v_add_u32_e32 v3, 0x2000, v3
	s_waitcnt vmcnt(2)
	ds_write_b128 v3, v[242:245]
	v_add_u32_e32 v3, 0x2000, v3
	s_waitcnt vmcnt(1)
	ds_write_b128 v3, v[246:249]
	v_add_u32_e32 v3, 0x2000, v3
	s_waitcnt vmcnt(0)
	ds_write_b128 v3, v[250:253]
; #define LAS __attribute__((address_space(3)))
; DI float sigmoidf_(float x) { return __builtin_amdgcn_rcpf(1.0f + __expf(-x)); }
; DI float softplusf_(float x) { return fmaxf(x, 0.f) + log1pf(__expf(-fabsf(x))); }
; template <int MODE, bool SB  > DI void norm_phase(const Params& P, const Frame& F, int L, const void* src_, const float* gain, bool combine) {
;     ...
;     if (MODE == 1) { const f32x4* w = (const f32x4*)((const float*)(ws + WS_WGT) + (size_t)L * 16 * D); for (int i = F.tid; i < 16 * D / 4; i += NTHR) ((LAS f32x4*)F.lds)[i] = w[i]; __syncthreads(); }
;     if (MODE == 2) { const f32x4* w = (const f32x4*)(ws + WS_WRT); for (int i = F.tid; i < NEXP * D / 4; i += NTHR) ((LAS f32x4*)F.lds)[i] = w[i]; if (F.tid < 8) F.MISC[16 + F.tid] = 0u; __syncthreads(); }
;     f32x4 g[8];
; #pragma unroll
;     for (int j = 0; j < 8; ++j) g[j] = *(const f32x4*)(gain + 4 * F.lane + 256 * j);
;     f32x4 vn[SB ? 1 : 8]; u32x2 vb[SB ? 8 : 1];
; #pragma unroll
;     for (int j = 0; j < 8; ++j) { if constexpr (SB) vb[j] = *(const u32x2*)(srcb + (size_t)(r_lo + F.wave) * D + 4 * F.lane + 256 * j); else vn[j] = *(const f32x4*)(src + (size_t)(r_lo + F.wave) * D + 4 * F.lane + 256 * j); }
;     ...
;             if ((F.lane & 3) == 0) { const int gi = ((F.lane >> 5) & 1) * 8 + ((F.lane >> 4) & 1) * 4 + ((F.lane >> 3) & 1) * 2 + ((F.lane >> 2) & 1), h = gi & 3; float r;
;                 if (gi < 4) r = sigmoidf_(mine);
;                 else if (gi < 8) r = -__expf(P.in[I_DN_A_LOG][L * 4 + h]) * softplusf_(mine + P.in[I_DN_DT_BIAS][L * 4 + h]);
;                 else if (gi < 12) r = mine + P.in[I_ML_I_BIAS][L * 4 + h];
;                 else r = -softplusf_(-(mine + P.in[I_ML_F_BIAS][L * 4 + h]));
.LBB0_1644:
	s_or_b64 exec, exec, s[0:1]
	s_lshl_b32 s0, s2, 6
	s_add_i32 s3, s0, 64
	s_add_i32 s0, s86, s0
	s_cmp_lt_i32 s0, s3
	s_waitcnt vmcnt(8) lgkmcnt(0)
	s_barrier
	s_cbranch_scc0 .LBB0_1661
	v_lshlrev_b32_e32 v34, 2, v44
	v_ashrrev_i32_e32 v35, 31, v34
	v_lshl_add_u64 v[16:17], v[34:35], 2, s[72:73]
	s_ashr_i32 s1, s0, 31
	s_mov_b64 s[4:5], 0x2000
	v_add_co_u32_e32 v8, vcc, 0x2000, v16
	s_lshl_b64 s[20:21], s[0:1], 12
	v_lshl_add_u64 v[12:13], v[16:17], 0, s[4:5]
	v_addc_co_u32_e32 v9, vcc, 0, v17, vcc
	s_add_u32 s4, s38, s20
	v_add_co_u32_e32 v28, vcc, 0x3000, v16
	s_addc_u32 s5, s39, s21
	v_lshlrev_b64 v[34:35], 1, v[34:35]
	v_addc_co_u32_e32 v29, vcc, 0, v17, vcc
	v_lshl_add_u64 v[36:37], s[4:5], 0, v[34:35]
	global_load_dwordx4 v[0:3], v[12:13], off offset:1024
	global_load_dwordx4 v[4:7], v[12:13], off offset:2048
	s_nop 0
	global_load_dwordx4 v[8:11], v[8:9], off
	s_nop 0
	global_load_dwordx4 v[12:15], v[12:13], off offset:3072
	s_nop 0
	global_load_dwordx4 v[16:19], v[28:29], off
	global_load_dwordx4 v[20:23], v[28:29], off offset:1024
	global_load_dwordx4 v[24:27], v[28:29], off offset:2048
	s_nop 0
	global_load_dwordx4 v[28:31], v[28:29], off offset:3072
	s_nop 0
	global_load_dwordx2 v[56:57], v[36:37], off offset:3584
	global_load_dwordx2 v[62:63], v[36:37], off offset:3072
	global_load_dwordx2 v[60:61], v[36:37], off offset:2560
	global_load_dwordx2 v[58:59], v[36:37], off offset:2048
	global_load_dwordx2 v[48:49], v[36:37], off offset:1536
	global_load_dwordx2 v[54:55], v[36:37], off offset:1024
	global_load_dwordx2 v[52:53], v[36:37], off offset:512
	global_load_dwordx2 v[50:51], v[36:37], off
	v_and_b32_e32 v36, 64, v32
	v_xor_b32_e32 v33, 32, v32
	v_add_u32_e32 v36, 64, v36
	v_cmp_lt_i32_e32 vcc, v33, v36
	v_readlane_b32 s56, v254, 5
	v_and_b32_e32 v40, 12, v44
	v_cndmask_b32_e32 v32, v32, v33, vcc
	v_lshlrev_b32_e32 v98, 2, v32
	v_lshl_add_u64 v[32:33], s[38:39], 0, v[34:35]
	v_and_b32_e32 v34, 32, v44
	v_cmp_eq_u32_e64 s[4:5], 0, v34
	v_cmp_ne_u32_e64 s[6:7], 0, v34
	v_and_b32_e32 v34, 16, v44
	v_cmp_eq_u32_e64 s[8:9], 0, v34
	v_and_b32_e32 v34, 8, v44
	v_cmp_eq_u32_e64 s[10:11], 0, v34
	v_and_b32_e32 v34, 4, v44
	v_cmp_eq_u32_e64 s[12:13], 0, v34
	v_and_b32_e32 v34, 3, v44
	v_cmp_eq_u32_e64 s[14:15], 0, v34
	v_lshrrev_b32_e32 v34, 2, v44
	v_and_b32_e32 v34, 12, v34
	v_mov_b32_e32 v41, 0
	v_readlane_b32 s68, v254, 17
	v_readlane_b32 s69, v254, 18
	v_readlane_b32 s70, v254, 19
	v_readlane_b32 s71, v254, 20
	v_cmp_ne_u32_e64 s[16:17], 0, v34
	v_cmp_ne_u32_e64 s[18:19], 12, v34
	v_lshl_add_u64 v[34:35], s[68:69], 0, v[40:41]
	v_lshl_add_u64 v[36:37], s[70:71], 0, v[40:41]
	v_readlane_b32 s68, v254, 37
	s_lshl_b64 s[22:23], s[0:1], 6
	v_ashrrev_i32_e32 v45, 31, v44
	v_lshl_add_u32 v99, v44, 4, 0
	v_readlane_b32 s80, v254, 49
	v_readlane_b32 s81, v254, 50
	v_readlane_b32 s82, v254, 51
	v_readlane_b32 s83, v254, 52
	v_and_or_b32 v42, v44, 60, s22
	v_mov_b32_e32 v43, s23
	s_mov_b64 s[22:23], 0x200000
	v_add_u32_e32 v100, 0x10000, v99
	v_add_u32_e32 v101, 0x10400, v99
	v_add_u32_e32 v102, 0x10800, v99
	v_add_u32_e32 v103, 0x10c00, v99
	v_add_u32_e32 v104, 0x11000, v99
	v_add_u32_e32 v105, 0x11400, v99
	v_add_u32_e32 v106, 0x11800, v99
	v_add_u32_e32 v107, 0x11c00, v99
	v_add_u32_e32 v108, 0x12000, v99
	v_add_u32_e32 v109, 0x12400, v99
	v_add_u32_e32 v110, 0x12800, v99
	v_add_u32_e32 v111, 0x12c00, v99
	v_add_u32_e32 v112, 0x13000, v99
	v_add_u32_e32 v113, 0x13400, v99
	v_add_u32_e32 v114, 0x13800, v99
	v_add_u32_e32 v115, 0x13c00, v99
	v_add_u32_e32 v116, 0x14000, v99
	v_add_u32_e32 v117, 0x14400, v99
	v_add_u32_e32 v118, 0x14800, v99
	v_add_u32_e32 v119, 0x14c00, v99
	v_add_u32_e32 v120, 0x15000, v99
	v_add_u32_e32 v121, 0x15400, v99
	v_add_u32_e32 v122, 0x15800, v99
	v_add_u32_e32 v123, 0x15c00, v99
	v_add_u32_e32 v124, 0x16000, v99
	v_add_u32_e32 v125, 0x16400, v99
	v_add_u32_e32 v126, 0x16800, v99
	v_add_u32_e32 v127, 0x16c00, v99
	v_add_u32_e32 v128, 0x17000, v99
	v_add_u32_e32 v129, 0x17400, v99
	v_add_u32_e32 v130, 0x17800, v99
	v_add_u32_e32 v131, 0x17c00, v99
	v_add_u32_e32 v132, 0x18000, v99
	v_add_u32_e32 v133, 0x18400, v99
	v_add_u32_e32 v134, 0x18800, v99
	v_add_u32_e32 v135, 0x18c00, v99
	v_add_u32_e32 v136, 0x19000, v99
	v_add_u32_e32 v137, 0x19400, v99
	v_add_u32_e32 v138, 0x19800, v99
	v_add_u32_e32 v139, 0x19c00, v99
	v_add_u32_e32 v140, 0x1a000, v99
	v_add_u32_e32 v141, 0x1a400, v99
	v_add_u32_e32 v142, 0x1a800, v99
	v_add_u32_e32 v143, 0x1ac00, v99
	v_add_u32_e32 v144, 0x1b000, v99
	v_add_u32_e32 v145, 0x1b400, v99
	v_add_u32_e32 v146, 0x1b800, v99
	v_add_u32_e32 v147, 0x1bc00, v99
	v_add_u32_e32 v148, 0x1c000, v99
	v_add_u32_e32 v149, 0x1c400, v99
	v_add_u32_e32 v150, 0x1c800, v99
	v_add_u32_e32 v151, 0x1cc00, v99
	v_add_u32_e32 v152, 0x1d000, v99
	v_add_u32_e32 v153, 0x1d400, v99
	v_add_u32_e32 v154, 0x1d800, v99
	v_add_u32_e32 v155, 0x1dc00, v99
	v_add_u32_e32 v156, 0x1e000, v99
	v_add_u32_e32 v157, 0x1e400, v99
	v_add_u32_e32 v158, 0x1e800, v99
	v_add_u32_e32 v159, 0x1ec00, v99
	v_add_u32_e32 v160, 0x1f000, v99
	v_add_u32_e32 v161, 0x1f400, v99
	v_add_u32_e32 v162, 0x1f800, v99
	v_add_u32_e32 v163, 0x1fc00, v99
	v_readlane_b32 s70, v254, 39
	v_readlane_b32 s71, v254, 40
	v_readlane_b32 s74, v254, 43
	v_readlane_b32 s75, v254, 44
	v_readlane_b32 s76, v254, 45
	v_readlane_b32 s77, v254, 46
	v_readlane_b32 s78, v254, 47
	v_readlane_b32 s79, v254, 48
	v_lshl_add_u64 v[38:39], s[80:81], 0, v[40:41]
	v_lshl_add_u64 v[40:41], s[82:83], 0, v[40:41]
	v_lshl_add_u64 v[42:43], v[42:43], 0, s[22:23]
	v_lshl_add_u64 v[44:45], v[44:45], 3, s[20:21]
	v_mov_b32_e32 v164, 0x358637bd
	v_mov_b32_e32 v165, 0x260
	s_mov_b32 s1, 0xbfb8aa3b
	s_mov_b32 s30, 0x3f2aaaab
	v_mov_b32_e32 v166, 0x3ecc95a3
	s_mov_b32 s31, 0x3f317218
	s_mov_b32 s33, 0x7f800000
	s_mov_b32 s34, 0x33800000
	v_mov_b32_e32 v46, 0x3f317218
	v_mov_b32_e32 v167, 0x7f800000
	v_mov_b32_e32 v168, 0x7fc00000
	v_mov_b32_e32 v169, 0xff800000
	v_readlane_b32 s57, v254, 6
	v_readlane_b32 s58, v254, 7
	v_readlane_b32 s59, v254, 8
	v_readlane_b32 s60, v254, 9
	v_readlane_b32 s61, v254, 10
	v_readlane_b32 s62, v254, 11
	v_readlane_b32 s63, v254, 12
	v_readlane_b32 s64, v254, 13
	v_readlane_b32 s65, v254, 14
	v_readlane_b32 s66, v254, 15
	v_readlane_b32 s67, v254, 16
	v_readlane_b32 s69, v254, 38
	v_readlane_b32 s72, v254, 41
	v_readlane_b32 s73, v254, 42
	global_load_dword v190, v[34:35], off offset:16
	global_load_dword v191, v[36:37], off offset:16
	global_load_dword v192, v[40:41], off offset:16
	global_load_dword v193, v[38:39], off offset:16
	s_branch .LBB0_1648

; DI unsigned pk2(float lo, float hi) { const f32x2 v = {lo, hi}; return __builtin_bit_cast(unsigned, __builtin_convertvector(v, bf16x2_t)); }
; DI float wave_sum(float v) { v += shx<1>(v); v += shx<2>(v); v += shx<4>(v); v += shx<8>(v); v += shx<16>(v); v += shx<32>(v); return v; }
; template <int MODE, bool SB  > DI void norm_phase(const Params& P, const Frame& F, int L, const void* src_, const float* gain, bool combine) {
;     ...
;     for (int row = r_lo + F.wave; row < r_hi; row += NWAVES) {
;         f32x4 v[8];
; #pragma unroll
;         for (int j = 0; j < 8; ++j) { if constexpr (SB) v[j] = (f32x4){bflo(vb[j].x), bfhi(vb[j].x), bflo(vb[j].y), bfhi(vb[j].y)}; else v[j] = vn[j]; }
;         { const int rnx = (row + NWAVES < r_hi) ? row + NWAVES : row;
; #pragma unroll
;           for (int j = 0; j < 8; ++j) { if constexpr (SB) vb[j] = *(const u32x2*)(srcb + (size_t)rnx * D + 4 * F.lane + 256 * j); else vn[j] = *(const f32x4*)(src + (size_t)rnx * D + 4 * F.lane + 256 * j); } }
;         if (MODE == 3 && combine) {
;             const int* SLOT = (const int*)(ws + WS_SLOT); const float* TOPW = (const float*)(ws + WS_TOPW); const bf16* Y = (const bf16*)(ws + WS_T + T_YPERM);
;             const int s1 = SLOT[row * 2], s2 = SLOT[row * 2 + 1]; const float w1 = TOPW[row * 2], w2 = TOPW[row * 2 + 1];
;             u32x2 ya[8], yb[8];
; #pragma unroll
;             for (int j = 0; j < 8; ++j) { ya[j] = *(const u32x2*)(Y + (size_t)s1 * D + 4 * F.lane + 256 * j); yb[j] = *(const u32x2*)(Y + (size_t)s2 * D + 4 * F.lane + 256 * j); }
; #pragma unroll
;             for (int j = 0; j < 8; ++j) { const f32x4 y1 = (f32x4){bflo(ya[j].x), bfhi(ya[j].x), bflo(ya[j].y), bfhi(ya[j].y)}, y2 = (f32x4){bflo(yb[j].x), bfhi(yb[j].x), bflo(yb[j].y), bfhi(yb[j].y)};
;                 v[j] = v[j] + w1 * y1 + w2 * y2;
;                 const u32x2 hb = {pk2(v[j][0], v[j][1]), pk2(v[j][2], v[j][3])}; *(u32x2*)(const_cast<bf16*>(srcb) + (size_t)row * D + 4 * F.lane + 256 * j) = hb;
;                 v[j] = (f32x4){bflo(hb.x), bfhi(hb.x), bflo(hb.y), bfhi(hb.y)}; }
;         }
;         float ss = 0.f;
; #pragma unroll
;         for (int j = 0; j < 8; ++j) ss += (v[j][0] * v[j][0] + v[j][1] * v[j][1]) + (v[j][2] * v[j][2] + v[j][3] * v[j][3]);
;         const float rstd = 1.0f / sqrtf(wave_sum(ss) * (1.0f / D) + EPS);
.LBB0_1648:
	s_waitcnt vmcnt(0)
	v_and_b32_e32 v75, 0xffff0000, v50
	v_and_b32_e32 v77, 0xffff0000, v51
	v_lshlrev_b32_e32 v65, 16, v48
	v_and_b32_e32 v69, 0xffff0000, v48
	v_lshlrev_b32_e32 v74, 16, v50
	v_lshlrev_b32_e32 v76, 16, v51
	v_mul_f32_e32 v48, v77, v77
	v_lshlrev_b32_e32 v78, 16, v52
	v_and_b32_e32 v81, 0xffff0000, v53
	v_and_b32_e32 v80, 0xffff0000, v52
	v_mul_f32_e32 v52, v75, v75
	v_lshlrev_b32_e32 v72, 16, v49
	v_and_b32_e32 v73, 0xffff0000, v49
	v_pk_fma_f32 v[48:49], v[76:77], v[76:77], v[48:49] op_sel_hi:[1,1,0]
	v_lshlrev_b32_e32 v79, 16, v53
	v_pk_mul_f32 v[50:51], v[80:81], v[80:81]
	v_pk_fma_f32 v[52:53], v[74:75], v[74:75], v[52:53] op_sel_hi:[1,1,0]
	v_pk_fma_f32 v[50:51], v[78:79], v[78:79], v[50:51]
	v_lshlrev_b32_e32 v82, 16, v54
	v_and_b32_e32 v83, 0xffff0000, v54
	v_lshlrev_b32_e32 v84, 16, v55
	v_and_b32_e32 v85, 0xffff0000, v55
	v_mov_b32_e32 v64, v52
	v_mov_b32_e32 v54, v48
	v_mov_b32_e32 v55, v65
	v_mul_f32_e32 v47, v69, v69
	v_pk_add_f32 v[48:49], v[52:53], v[48:49]
	v_pk_mul_f32 v[52:53], v[64:65], v[54:55]
	v_pk_add_f32 v[50:51], v[50:51], v[50:51] op_sel:[0,1] op_sel_hi:[1,0]
	v_mov_b32_e32 v49, v53
	v_mov_b32_e32 v51, v47
	v_pk_add_f32 v[48:49], v[48:49], v[50:51]
	v_mul_f32_e32 v50, v83, v83
	v_mul_f32_e32 v52, v85, v85
	v_lshlrev_b32_e32 v97, 16, v56
	v_and_b32_e32 v71, 0xffff0000, v56
	v_lshlrev_b32_e32 v66, 16, v57
	v_and_b32_e32 v67, 0xffff0000, v57
	v_mul_f32_e32 v56, v72, v72
	v_mul_f32_e32 v57, v73, v73
	v_pk_fma_f32 v[50:51], v[82:83], v[82:83], v[50:51] op_sel_hi:[1,1,0]
	v_pk_fma_f32 v[52:53], v[84:85], v[84:85], v[52:53] op_sel_hi:[1,1,0]
	v_mov_b32_e32 v51, v56
	v_mov_b32_e32 v53, v57
	v_pk_add_f32 v[50:51], v[50:51], v[52:53]
	v_and_b32_e32 v173, 0xffff0000, v59
	v_and_b32_e32 v172, 0xffff0000, v58
	v_pk_add_f32 v[48:49], v[48:49], v[50:51]
	v_lshlrev_b32_e32 v171, 16, v59
	v_lshlrev_b32_e32 v170, 16, v58
	v_pk_mul_f32 v[50:51], v[172:173], v[172:173]
	v_and_b32_e32 v177, 0xffff0000, v61
	v_pk_fma_f32 v[50:51], v[170:171], v[170:171], v[50:51]
	v_and_b32_e32 v176, 0xffff0000, v60
	v_pk_add_f32 v[50:51], v[50:51], v[50:51] op_sel:[0,1] op_sel_hi:[1,0]
	v_pk_add_f32 v[48:49], v[48:49], v[48:49] op_sel:[0,1] op_sel_hi:[1,0]
	v_lshlrev_b32_e32 v175, 16, v61
	v_lshlrev_b32_e32 v174, 16, v60
	v_pk_mul_f32 v[52:53], v[176:177], v[176:177]
	v_mov_b32_e32 v96, v48
	v_mov_b32_e32 v54, v50
	v_mov_b32_e32 v55, v97
	v_pk_fma_f32 v[52:53], v[174:175], v[174:175], v[52:53]
	v_pk_add_f32 v[48:49], v[48:49], v[50:51]
	v_pk_mul_f32 v[50:51], v[96:97], v[54:55]
	v_mul_f32_e32 v47, v71, v71
	v_mov_b32_e32 v49, v51
	v_pk_add_f32 v[50:51], v[52:53], v[52:53] op_sel:[0,1] op_sel_hi:[1,0]
	v_and_b32_e32 v179, 0xffff0000, v62
	v_and_b32_e32 v181, 0xffff0000, v63
	v_mov_b32_e32 v51, v47
	v_lshlrev_b32_e32 v178, 16, v62
	v_lshlrev_b32_e32 v180, 16, v63
	v_pk_add_f32 v[48:49], v[48:49], v[50:51]
	v_mul_f32_e32 v50, v179, v179
	v_mul_f32_e32 v52, v181, v181
	v_mul_f32_e32 v56, v66, v66
	v_mul_f32_e32 v57, v67, v67
	v_pk_fma_f32 v[50:51], v[178:179], v[178:179], v[50:51] op_sel_hi:[1,1,0]
	v_pk_fma_f32 v[52:53], v[180:181], v[180:181], v[52:53] op_sel_hi:[1,1,0]
	v_mov_b32_e32 v51, v56
	v_mov_b32_e32 v53, v57
	v_pk_add_f32 v[50:51], v[50:51], v[52:53]
	s_mov_b32 s20, s0
	v_pk_add_f32 v[48:49], v[48:49], v[50:51]
	s_add_i32 s0, s0, 8
	v_add_f32_e32 v47, v48, v49
	s_cmp_ge_i32 s0, s3
	s_cselect_b64 s[22:23], -1, 0
	v_add_f32_dpp v47, v47, v47 quad_perm:[1,0,3,2] row_mask:0xf bank_mask:0xf bound_ctrl:1
	s_cmp_lt_i32 s0, s3
	s_cselect_b32 s20, s0, s20
	v_add_f32_dpp v47, v47, v47 quad_perm:[2,3,0,1] row_mask:0xf bank_mask:0xf bound_ctrl:1
	ds_swizzle_b32 v48, v47 offset:swizzle(SWAP,4)
	s_ashr_i32 s21, s20, 31
	s_lshl_b64 s[20:21], s[20:21], 12
	v_lshl_add_u64 v[56:57], v[32:33], 0, s[20:21]
	s_mov_b32 s20, 0xf800000
	s_waitcnt lgkmcnt(0)
	v_add_f32_e32 v47, v47, v48
	ds_swizzle_b32 v48, v47 offset:swizzle(SWAP,8)
	s_waitcnt lgkmcnt(0)
	v_add_f32_e32 v47, v47, v48
	ds_swizzle_b32 v48, v47 offset:swizzle(SWAP,16)
	s_waitcnt lgkmcnt(0)
	v_add_f32_e32 v47, v47, v48
	ds_bpermute_b32 v48, v98, v47
	s_waitcnt lgkmcnt(0)
	v_add_f32_e32 v47, v47, v48
	v_fmamk_f32 v47, v47, 0x3a000000, v164
	v_mul_f32_e32 v48, 0x4f800000, v47
	v_cmp_gt_f32_e32 vcc, s20, v47
	s_nop 1
	v_cndmask_b32_e32 v47, v47, v48, vcc
	v_sqrt_f32_e32 v58, v47
	global_load_dwordx2 v[50:51], v[56:57], off
	global_load_dwordx2 v[52:53], v[56:57], off offset:512
	global_load_dwordx2 v[54:55], v[56:57], off offset:1024
	global_load_dwordx2 v[48:49], v[56:57], off offset:1536
	v_add_u32_e32 v59, -1, v58
	v_fma_f32 v60, -v59, v58, v47
	v_cmp_ge_f32_e64 s[20:21], 0, v60
	v_add_u32_e32 v60, 1, v58
	s_nop 0
	v_cndmask_b32_e64 v59, v58, v59, s[20:21]
	v_fma_f32 v58, -v60, v58, v47
	v_cmp_lt_f32_e64 s[20:21], 0, v58
	s_nop 1
	v_cndmask_b32_e64 v58, v59, v60, s[20:21]
	v_mul_f32_e32 v59, 0x37800000, v58
	v_cndmask_b32_e32 v58, v58, v59, vcc
	v_cmp_class_f32_e32 vcc, v47, v165
	s_nop 1
	v_cndmask_b32_e32 v47, v58, v47, vcc
	v_div_scale_f32 v64, s[20:21], v47, v47, 1.0
	v_rcp_f32_e32 v68, v64
	s_mov_b32 s20, 0x3d600000
	global_load_dwordx2 v[58:59], v[56:57], off offset:2048
	global_load_dwordx2 v[60:61], v[56:57], off offset:2560
	global_load_dwordx2 v[62:63], v[56:57], off offset:3072
	s_nop 0
	global_load_dwordx2 v[56:57], v[56:57], off offset:3584
	v_fma_f32 v70, -v64, v68, 1.0
	v_fmac_f32_e32 v68, v70, v68
	v_div_scale_f32 v70, vcc, 1.0, v47, 1.0
	v_mul_f32_e32 v86, v70, v68
	v_fma_f32 v87, -v64, v86, v70
	v_fmac_f32_e32 v86, v87, v68
	v_fma_f32 v64, -v64, v86, v70
	v_div_fmas_f32 v64, v64, v68, v86
	v_div_fixup_f32 v96, v64, v47, 1.0
	v_pk_mul_f32 v[74:75], v[96:97], v[74:75] op_sel_hi:[0,1]
; #define LAS __attribute__((address_space(3)))
; DI unsigned pk2(float lo, float hi) { const f32x2 v = {lo, hi}; return __builtin_bit_cast(unsigned, __builtin_convertvector(v, bf16x2_t)); }
; DI unsigned pk4_fp8(float a, float b, float c, float d) { unsigned w = 0u; w = __builtin_amdgcn_cvt_pk_fp8_f32(a, b, w, false); w = __builtin_amdgcn_cvt_pk_fp8_f32(c, d, w, true); return w; }
; template <int MODE, bool SB  > DI void norm_phase(const Params& P, const Frame& F, int L, const void* src_, const float* gain, bool combine) {
;     ...
;         for (int j = 0; j < 8; ++j) v[j] = v[j] * rstd * g[j];
;         if (MODE == 4) {
; #pragma unroll
;             for (int j = 0; j < 8; ++j) *(f32x4*)(P.out + (size_t)row * D + 4 * F.lane + 256 * j) = v[j];
;         } else if (MODE == 0 || MODE == 2 || (MODE == 3 && L == 1)) {
;             unsigned* o4 = (unsigned*)((unsigned char*)HN + (size_t)row * D) + F.lane; const float hs = (float)(1 << LS_HN);
; #pragma unroll
;             for (int j = 0; j < 8; ++j) o4[64 * j] = pk4_fp8(v[j][0] * hs, v[j][1] * hs, v[j][2] * hs, v[j][3] * hs);
;         } else {
;             unsigned long long* o8 = (unsigned long long*)(HN + (size_t)row * D) + F.lane;
; #pragma unroll
;             for (int j = 0; j < 8; ++j) o8[64 * j] = (unsigned long long)pk2(v[j][0], v[j][1]) | ((unsigned long long)pk2(v[j][2], v[j][3]) << 32);
;         }
;         if (MODE == 1) {
;             float s[16];
; #pragma unroll
;             for (int q = 0; q < 16; ++q) { float t = 0.f;
; #pragma unroll
;                 for (int j = 0; j < 8; ++j) { const f32x4 w = *(const LAS f32x4*)(F.lds + (size_t)(q * D + 256 * j + 4 * F.lane) * 4); t += (v[j][0] * w[0] + v[j][1] * w[1]) + (v[j][2] * w[2] + v[j][3] * w[3]); }
	v_mov_b32_e32 v68, v65
	v_pk_mul_f32 v[76:77], v[96:97], v[76:77] op_sel_hi:[0,1]
	v_pk_mul_f32 v[92:93], v[8:9], v[74:75]
	v_mov_b32_e32 v75, v80
	v_mov_b32_e32 v80, v79
	v_pk_mul_f32 v[64:65], v[68:69], v[96:97] op_sel_hi:[1,0]
	v_pk_mul_f32 v[90:91], v[10:11], v[76:77]
	v_mov_b32_e32 v74, v78
	v_pk_mul_f32 v[76:77], v[96:97], v[80:81] op_sel_hi:[0,1]
	v_pk_mul_f32 v[86:87], v[12:13], v[64:65]
	v_mov_b32_e32 v64, v170
	v_mov_b32_e32 v65, v172
	v_pk_mul_f32 v[74:75], v[96:97], v[74:75] op_sel_hi:[0,1]
	v_pk_mul_f32 v[88:89], v[2:3], v[76:77]
	v_pk_mul_f32 v[76:77], v[96:97], v[84:85] op_sel_hi:[0,1]
	v_pk_mul_f32 v[68:69], v[72:73], v[96:97] op_sel_hi:[1,0]
	v_pk_mul_f32 v[64:65], v[96:97], v[64:65] op_sel_hi:[0,1]
	v_mov_b32_e32 v172, v171
	v_pk_mul_f32 v[94:95], v[0:1], v[74:75]
	v_pk_mul_f32 v[74:75], v[96:97], v[82:83] op_sel_hi:[0,1]
	v_pk_mul_f32 v[82:83], v[6:7], v[76:77]
	v_pk_mul_f32 v[78:79], v[14:15], v[68:69]
	v_pk_mul_f32 v[68:69], v[96:97], v[172:173] op_sel_hi:[0,1]
	v_pk_mul_f32 v[76:77], v[16:17], v[64:65]
	v_mov_b32_e32 v64, v174
	v_mov_b32_e32 v65, v176
	v_mov_b32_e32 v176, v175
	v_pk_mul_f32 v[84:85], v[4:5], v[74:75]
	v_pk_mul_f32 v[74:75], v[18:19], v[68:69]
	v_pk_mul_f32 v[64:65], v[96:97], v[64:65] op_sel_hi:[0,1]
	v_pk_mul_f32 v[68:69], v[96:97], v[176:177] op_sel_hi:[0,1]
	v_mov_b32_e32 v70, v97
	v_pk_mul_f32 v[72:73], v[22:23], v[68:69]
	v_pk_mul_f32 v[80:81], v[20:21], v[64:65]
	v_pk_mul_f32 v[68:69], v[96:97], v[178:179] op_sel_hi:[0,1]
	v_pk_mul_f32 v[64:65], v[96:97], v[180:181] op_sel_hi:[0,1]
	v_pk_mul_f32 v[70:71], v[70:71], v[96:97] op_sel_hi:[1,0]
	v_pk_mul_f32 v[66:67], v[66:67], v[96:97] op_sel_hi:[1,0]
	v_lshl_add_u64 v[96:97], s[54:55], 0, v[44:45]
	v_add_co_u32_e32 v96, vcc, s20, v96
	v_cvt_pk_bf16_f32 v170, v92, v93
	v_cvt_pk_bf16_f32 v171, v90, v91
	v_addc_co_u32_e32 v97, vcc, 0, v97, vcc
	global_store_dwordx2 v[96:97], v[170:171], off
	v_cvt_pk_bf16_f32 v170, v94, v95
	v_cvt_pk_bf16_f32 v171, v88, v89
	global_store_dwordx2 v[96:97], v[170:171], off offset:512
	v_cvt_pk_bf16_f32 v170, v84, v85
	v_cvt_pk_bf16_f32 v171, v82, v83
	global_store_dwordx2 v[96:97], v[170:171], off offset:1024
	v_cvt_pk_bf16_f32 v170, v86, v87
	v_cvt_pk_bf16_f32 v171, v78, v79
	global_store_dwordx2 v[96:97], v[170:171], off offset:1536
	v_cvt_pk_bf16_f32 v170, v76, v77
	v_cvt_pk_bf16_f32 v171, v74, v75
	v_pk_mul_f32 v[64:65], v[26:27], v[64:65]
	v_pk_mul_f32 v[68:69], v[24:25], v[68:69]
	global_store_dwordx2 v[96:97], v[170:171], off offset:2048
	v_cvt_pk_bf16_f32 v170, v80, v81
	v_cvt_pk_bf16_f32 v171, v72, v73
	global_store_dwordx2 v[96:97], v[170:171], off offset:2560
	v_cvt_pk_bf16_f32 v170, v68, v69
	v_cvt_pk_bf16_f32 v171, v64, v65
	global_store_dwordx2 v[96:97], v[170:171], off offset:3072
	ds_read_b128 v[170:173], v99
	v_pk_mul_f32 v[66:67], v[30:31], v[66:67]
	v_pk_mul_f32 v[70:71], v[28:29], v[70:71]
	v_cvt_pk_bf16_f32 v175, v66, v67
	v_cvt_pk_bf16_f32 v174, v70, v71
	global_store_dwordx2 v[96:97], v[174:175], off offset:3584
	ds_read_b128 v[174:177], v99 offset:1024
	s_waitcnt lgkmcnt(1)
	v_mul_f32_e32 v47, v171, v93
	v_mul_f32_e32 v96, v173, v91
	v_fmac_f32_e32 v47, v170, v92
	v_fmac_f32_e32 v96, v172, v90
	ds_read_b128 v[170:173], v99 offset:2048
	v_add_f32_e32 v47, v47, v96
	s_waitcnt lgkmcnt(1)
	v_mul_f32_e32 v96, v95, v175
	v_mul_f32_e32 v97, v89, v177
	v_fmac_f32_e32 v96, v94, v174
	v_fmac_f32_e32 v97, v88, v176
	ds_read_b128 v[174:177], v99 offset:3072
	v_add_f32_e32 v47, 0, v47
	v_add_f32_e32 v96, v96, v97
	v_add_f32_e32 v47, v96, v47
	s_waitcnt lgkmcnt(1)
	v_mul_f32_e32 v96, v85, v171
	v_mul_f32_e32 v97, v83, v173
	v_fmac_f32_e32 v96, v84, v170
	v_fmac_f32_e32 v97, v82, v172
	ds_read_b128 v[170:173], v99 offset:4096
	v_add_f32_e32 v96, v96, v97
	v_add_f32_e32 v47, v96, v47
	s_waitcnt lgkmcnt(1)
	v_mul_f32_e32 v96, v87, v175
	v_mul_f32_e32 v97, v79, v177
	v_fmac_f32_e32 v96, v86, v174
	v_fmac_f32_e32 v97, v78, v176
	ds_read_b128 v[174:177], v99 offset:5120
	v_add_f32_e32 v96, v96, v97
	v_add_f32_e32 v47, v96, v47
	s_waitcnt lgkmcnt(1)
	v_mul_f32_e32 v96, v77, v171
	v_mul_f32_e32 v97, v75, v173
	v_fmac_f32_e32 v96, v76, v170
	v_fmac_f32_e32 v97, v74, v172
	ds_read_b128 v[170:173], v99 offset:6144
	v_add_f32_e32 v96, v96, v97
	v_add_f32_e32 v47, v96, v47
	s_waitcnt lgkmcnt(1)
	v_mul_f32_e32 v96, v81, v175
	v_mul_f32_e32 v97, v73, v177
	v_fmac_f32_e32 v96, v80, v174
	v_fmac_f32_e32 v97, v72, v176
	ds_read_b128 v[174:177], v99 offset:7168
	v_add_f32_e32 v96, v96, v97
	v_add_f32_e32 v47, v96, v47
	s_waitcnt lgkmcnt(1)
	v_mul_f32_e32 v96, v69, v171
	v_mul_f32_e32 v97, v65, v173
	v_fmac_f32_e32 v96, v68, v170
	v_fmac_f32_e32 v97, v64, v172
	v_add_f32_e32 v96, v96, v97
	ds_read_b128 v[170:173], v99 offset:8192
	v_add_f32_e32 v47, v96, v47
	s_waitcnt lgkmcnt(1)
	v_mul_f32_e32 v96, v71, v175
	v_mul_f32_e32 v97, v67, v177
	v_fmac_f32_e32 v96, v70, v174
	v_fmac_f32_e32 v97, v66, v176
	ds_read_b128 v[174:177], v99 offset:9216
	v_add_f32_e32 v96, v96, v97
	v_add_f32_e32 v47, v96, v47
	s_waitcnt lgkmcnt(1)
	v_mul_f32_e32 v96, v93, v171
	v_mul_f32_e32 v97, v91, v173
	v_fmac_f32_e32 v96, v92, v170
	v_fmac_f32_e32 v97, v90, v172
	ds_read_b128 v[170:173], v99 offset:10240
	v_add_f32_e32 v96, v96, v97
	s_waitcnt lgkmcnt(1)
	v_mul_f32_e32 v97, v95, v175
	v_fmac_f32_e32 v97, v94, v174
	v_mul_f32_e32 v174, v89, v177
	v_fmac_f32_e32 v174, v88, v176
	v_add_f32_e32 v96, 0, v96
	v_add_f32_e32 v97, v97, v174
	ds_read_b128 v[174:177], v99 offset:11264
	v_add_f32_e32 v96, v96, v97
	s_waitcnt lgkmcnt(1)
	v_mul_f32_e32 v97, v85, v171
	v_fmac_f32_e32 v97, v84, v170
	v_mul_f32_e32 v170, v83, v173
	v_fmac_f32_e32 v170, v82, v172
	v_add_f32_e32 v97, v97, v170
	ds_read_b128 v[170:173], v99 offset:12288
	v_add_f32_e32 v96, v96, v97
	s_waitcnt lgkmcnt(1)
; #define LAS __attribute__((address_space(3)))
; template <int MODE, bool SB  > DI void norm_phase(const Params& P, const Frame& F, int L, const void* src_, const float* gain, bool combine) {
;     ...
;             for (int q = 0; q < 16; ++q) { float t = 0.f;
; #pragma unroll
;                 for (int j = 0; j < 8; ++j) { const f32x4 w = *(const LAS f32x4*)(F.lds + (size_t)(q * D + 256 * j + 4 * F.lane) * 4); t += (v[j][0] * w[0] + v[j][1] * w[1]) + (v[j][2] * w[2] + v[j][3] * w[3]); }
;                 s[q] = t; if ((q & 3) == 3) asm volatile("" ::: "memory"); }
	v_mul_f32_e32 v97, v87, v175
	v_fmac_f32_e32 v97, v86, v174
	v_mul_f32_e32 v174, v79, v177
	v_fmac_f32_e32 v174, v78, v176
	v_add_f32_e32 v97, v97, v174
	ds_read_b128 v[174:177], v99 offset:13312
	v_add_f32_e32 v96, v96, v97
	s_waitcnt lgkmcnt(1)
	v_mul_f32_e32 v97, v77, v171
	v_fmac_f32_e32 v97, v76, v170
	v_mul_f32_e32 v170, v75, v173
	v_fmac_f32_e32 v170, v74, v172
	v_add_f32_e32 v97, v97, v170
	ds_read_b128 v[170:173], v99 offset:14336
	v_add_f32_e32 v96, v96, v97
	s_waitcnt lgkmcnt(1)
	v_mul_f32_e32 v97, v81, v175
	v_fmac_f32_e32 v97, v80, v174
	v_mul_f32_e32 v174, v73, v177
	v_fmac_f32_e32 v174, v72, v176
	v_add_f32_e32 v97, v97, v174
	ds_read_b128 v[174:177], v99 offset:15360
	v_add_f32_e32 v96, v96, v97
	s_waitcnt lgkmcnt(1)
	v_mul_f32_e32 v97, v69, v171
	v_fmac_f32_e32 v97, v68, v170
	v_mul_f32_e32 v170, v65, v173
	v_fmac_f32_e32 v170, v64, v172
	v_add_f32_e32 v97, v97, v170
	v_add_f32_e32 v96, v96, v97
	s_waitcnt lgkmcnt(0)
	v_mul_f32_e32 v97, v71, v175
	v_fmac_f32_e32 v97, v70, v174
	v_mul_f32_e32 v174, v67, v177
	ds_read_b128 v[170:173], v99 offset:16384
	v_fmac_f32_e32 v174, v66, v176
	v_add_f32_e32 v97, v97, v174
	ds_read_b128 v[174:177], v99 offset:17408
	v_add_f32_e32 v96, v96, v97
	s_waitcnt lgkmcnt(1)
	v_mul_f32_e32 v97, v93, v171
	v_fmac_f32_e32 v97, v92, v170
	v_mul_f32_e32 v170, v91, v173
	v_fmac_f32_e32 v170, v90, v172
	s_waitcnt lgkmcnt(0)
	v_mul_f32_e32 v175, v95, v175
	v_add_f32_e32 v97, v97, v170
	v_fmac_f32_e32 v175, v94, v174
	v_mul_f32_e32 v174, v89, v177
	ds_read_b128 v[170:173], v99 offset:18432
	v_fmac_f32_e32 v174, v88, v176
	v_add_f32_e32 v97, 0, v97
	v_add_f32_e32 v174, v175, v174
	v_add_f32_e32 v97, v97, v174
	ds_read_b128 v[174:177], v99 offset:19456
	s_waitcnt lgkmcnt(1)
	v_mul_f32_e32 v171, v85, v171
	v_fmac_f32_e32 v171, v84, v170
	v_mul_f32_e32 v170, v83, v173
	v_fmac_f32_e32 v170, v82, v172
	v_add_f32_e32 v170, v171, v170
	s_waitcnt lgkmcnt(0)
	v_mul_f32_e32 v175, v87, v175
	v_add_f32_e32 v97, v97, v170
	v_fmac_f32_e32 v175, v86, v174
	v_mul_f32_e32 v174, v79, v177
	ds_read_b128 v[170:173], v99 offset:20480
	v_fmac_f32_e32 v174, v78, v176
	v_add_f32_e32 v174, v175, v174
	v_add_f32_e32 v97, v97, v174
	ds_read_b128 v[174:177], v99 offset:21504
	s_waitcnt lgkmcnt(1)
	v_mul_f32_e32 v171, v77, v171
	v_fmac_f32_e32 v171, v76, v170
	v_mul_f32_e32 v170, v75, v173
	v_fmac_f32_e32 v170, v74, v172
	v_add_f32_e32 v170, v171, v170
	s_waitcnt lgkmcnt(0)
	v_mul_f32_e32 v175, v81, v175
	v_add_f32_e32 v97, v97, v170
	v_fmac_f32_e32 v175, v80, v174
	v_mul_f32_e32 v174, v73, v177
	ds_read_b128 v[170:173], v99 offset:22528
	v_fmac_f32_e32 v174, v72, v176
	v_add_f32_e32 v174, v175, v174
	v_add_f32_e32 v97, v97, v174
	ds_read_b128 v[174:177], v99 offset:23552
	s_waitcnt lgkmcnt(1)
	v_mul_f32_e32 v171, v69, v171
	v_fmac_f32_e32 v171, v68, v170
	v_mul_f32_e32 v170, v65, v173
	v_fmac_f32_e32 v170, v64, v172
	v_add_f32_e32 v170, v171, v170
	s_waitcnt lgkmcnt(0)
	v_mul_f32_e32 v175, v71, v175
	v_add_f32_e32 v97, v97, v170
	v_fmac_f32_e32 v175, v70, v174
	v_mul_f32_e32 v174, v67, v177
	ds_read_b128 v[170:173], v99 offset:24576
	v_fmac_f32_e32 v174, v66, v176
	v_add_f32_e32 v174, v175, v174
	v_add_f32_e32 v97, v97, v174
	ds_read_b128 v[174:177], v99 offset:25600
	s_waitcnt lgkmcnt(1)
	v_mul_f32_e32 v171, v93, v171
	v_fmac_f32_e32 v171, v92, v170
	v_mul_f32_e32 v170, v91, v173
	v_fmac_f32_e32 v170, v90, v172
	v_add_f32_e32 v170, v171, v170
	s_waitcnt lgkmcnt(0)
	v_mul_f32_e32 v175, v95, v175
	v_add_f32_e32 v178, 0, v170
	v_fmac_f32_e32 v175, v94, v174
	v_mul_f32_e32 v174, v89, v177
	ds_read_b128 v[170:173], v99 offset:26624
	v_fmac_f32_e32 v174, v88, v176
	v_add_f32_e32 v174, v175, v174
	v_add_f32_e32 v178, v178, v174
	ds_read_b128 v[174:177], v99 offset:27648
	s_waitcnt lgkmcnt(1)
	v_mul_f32_e32 v171, v85, v171
	v_fmac_f32_e32 v171, v84, v170
	v_mul_f32_e32 v170, v83, v173
	v_fmac_f32_e32 v170, v82, v172
	v_add_f32_e32 v170, v171, v170
	s_waitcnt lgkmcnt(0)
	v_mul_f32_e32 v175, v87, v175
	v_add_f32_e32 v178, v178, v170
	v_fmac_f32_e32 v175, v86, v174
	v_mul_f32_e32 v174, v79, v177
	ds_read_b128 v[170:173], v99 offset:28672
	v_fmac_f32_e32 v174, v78, v176
	v_add_f32_e32 v174, v175, v174
	v_add_f32_e32 v178, v178, v174
	ds_read_b128 v[174:177], v99 offset:29696
	s_waitcnt lgkmcnt(1)
	v_mul_f32_e32 v171, v77, v171
	v_fmac_f32_e32 v171, v76, v170
	v_mul_f32_e32 v170, v75, v173
	v_fmac_f32_e32 v170, v74, v172
	v_add_f32_e32 v170, v171, v170
	s_waitcnt lgkmcnt(0)
	v_mul_f32_e32 v175, v81, v175
	v_add_f32_e32 v178, v178, v170
	v_fmac_f32_e32 v175, v80, v174
	v_mul_f32_e32 v174, v73, v177
	ds_read_b128 v[170:173], v99 offset:30720
	v_fmac_f32_e32 v174, v72, v176
	v_add_f32_e32 v174, v175, v174
	v_add_f32_e32 v178, v178, v174
	ds_read_b128 v[174:177], v99 offset:31744
	s_waitcnt lgkmcnt(1)
	v_mul_f32_e32 v171, v69, v171
	v_fmac_f32_e32 v171, v68, v170
	v_mul_f32_e32 v170, v65, v173
	v_fmac_f32_e32 v170, v64, v172
	v_add_f32_e32 v170, v171, v170
	s_waitcnt lgkmcnt(0)
	v_mul_f32_e32 v171, v71, v175
	v_fmac_f32_e32 v171, v70, v174
	v_mul_f32_e32 v177, v67, v177
	ds_read_b128 v[172:175], v99 offset:32768
	v_fmac_f32_e32 v177, v66, v176
	v_add_f32_e32 v170, v178, v170
	v_add_f32_e32 v171, v171, v177
	ds_read_b128 v[176:179], v99 offset:33792
	v_add_f32_e32 v170, v170, v171
	s_waitcnt lgkmcnt(1)
	v_mul_f32_e32 v171, v93, v173
	v_fmac_f32_e32 v171, v92, v172
	v_mul_f32_e32 v172, v91, v175
	v_fmac_f32_e32 v172, v90, v174
	s_waitcnt lgkmcnt(0)
	v_mul_f32_e32 v177, v95, v177
	v_add_f32_e32 v171, v171, v172
	v_fmac_f32_e32 v177, v94, v176
	v_mul_f32_e32 v176, v89, v179
	ds_read_b128 v[172:175], v99 offset:34816
	v_fmac_f32_e32 v176, v88, v178
	v_add_f32_e32 v171, 0, v171
	v_add_f32_e32 v176, v177, v176
	v_add_f32_e32 v171, v171, v176
	ds_read_b128 v[176:179], v99 offset:35840
	s_waitcnt lgkmcnt(1)
; #define LAS __attribute__((address_space(3)))
; template <int MODE, bool SB  > DI void norm_phase(const Params& P, const Frame& F, int L, const void* src_, const float* gain, bool combine) {
;     ...
;             for (int q = 0; q < 16; ++q) { float t = 0.f;
; #pragma unroll
;                 for (int j = 0; j < 8; ++j) { const f32x4 w = *(const LAS f32x4*)(F.lds + (size_t)(q * D + 256 * j + 4 * F.lane) * 4); t += (v[j][0] * w[0] + v[j][1] * w[1]) + (v[j][2] * w[2] + v[j][3] * w[3]); }
;                 s[q] = t; if ((q & 3) == 3) asm volatile("" ::: "memory"); }
	v_mul_f32_e32 v173, v85, v173
	v_fmac_f32_e32 v173, v84, v172
	v_mul_f32_e32 v172, v83, v175
	v_fmac_f32_e32 v172, v82, v174
	v_add_f32_e32 v172, v173, v172
	s_waitcnt lgkmcnt(0)
	v_mul_f32_e32 v177, v87, v177
	v_add_f32_e32 v171, v171, v172
	v_fmac_f32_e32 v177, v86, v176
	v_mul_f32_e32 v176, v79, v179
	ds_read_b128 v[172:175], v99 offset:36864
	v_fmac_f32_e32 v176, v78, v178
	v_add_f32_e32 v176, v177, v176
	v_add_f32_e32 v171, v171, v176
	ds_read_b128 v[176:179], v99 offset:37888
	s_waitcnt lgkmcnt(1)
	v_mul_f32_e32 v173, v77, v173
	v_fmac_f32_e32 v173, v76, v172
	v_mul_f32_e32 v172, v75, v175
	v_fmac_f32_e32 v172, v74, v174
	v_add_f32_e32 v172, v173, v172
	s_waitcnt lgkmcnt(0)
	v_mul_f32_e32 v177, v81, v177
	v_add_f32_e32 v171, v171, v172
	v_fmac_f32_e32 v177, v80, v176
	v_mul_f32_e32 v176, v73, v179
	ds_read_b128 v[172:175], v99 offset:38912
	v_fmac_f32_e32 v176, v72, v178
	v_add_f32_e32 v176, v177, v176
	v_add_f32_e32 v171, v171, v176
	ds_read_b128 v[176:179], v99 offset:39936
	s_waitcnt lgkmcnt(1)
	v_mul_f32_e32 v173, v69, v173
	v_fmac_f32_e32 v173, v68, v172
	v_mul_f32_e32 v172, v65, v175
	v_fmac_f32_e32 v172, v64, v174
	v_add_f32_e32 v172, v173, v172
	s_waitcnt lgkmcnt(0)
	v_mul_f32_e32 v177, v71, v177
	v_add_f32_e32 v171, v171, v172
	v_fmac_f32_e32 v177, v70, v176
	v_mul_f32_e32 v176, v67, v179
	ds_read_b128 v[172:175], v99 offset:40960
	v_fmac_f32_e32 v176, v66, v178
	v_add_f32_e32 v176, v177, v176
	v_add_f32_e32 v171, v171, v176
	ds_read_b128 v[176:179], v99 offset:41984
	s_waitcnt lgkmcnt(1)
	v_mul_f32_e32 v173, v93, v173
	v_fmac_f32_e32 v173, v92, v172
	v_mul_f32_e32 v172, v91, v175
	v_fmac_f32_e32 v172, v90, v174
	v_add_f32_e32 v172, v173, v172
	s_waitcnt lgkmcnt(0)
	v_mul_f32_e32 v177, v95, v177
	v_add_f32_e32 v180, 0, v172
	v_fmac_f32_e32 v177, v94, v176
	v_mul_f32_e32 v176, v89, v179
	ds_read_b128 v[172:175], v99 offset:43008
	v_fmac_f32_e32 v176, v88, v178
	v_add_f32_e32 v176, v177, v176
	v_add_f32_e32 v180, v180, v176
	ds_read_b128 v[176:179], v99 offset:44032
	s_waitcnt lgkmcnt(1)
	v_mul_f32_e32 v173, v85, v173
	v_fmac_f32_e32 v173, v84, v172
	v_mul_f32_e32 v172, v83, v175
	v_fmac_f32_e32 v172, v82, v174
	v_add_f32_e32 v172, v173, v172
	s_waitcnt lgkmcnt(0)
	v_mul_f32_e32 v177, v87, v177
	v_add_f32_e32 v180, v180, v172
	v_fmac_f32_e32 v177, v86, v176
	v_mul_f32_e32 v176, v79, v179
	ds_read_b128 v[172:175], v99 offset:45056
	v_fmac_f32_e32 v176, v78, v178
	v_add_f32_e32 v176, v177, v176
	v_add_f32_e32 v180, v180, v176
	ds_read_b128 v[176:179], v99 offset:46080
	s_waitcnt lgkmcnt(1)
	v_mul_f32_e32 v173, v77, v173
	v_fmac_f32_e32 v173, v76, v172
	v_mul_f32_e32 v172, v75, v175
	v_fmac_f32_e32 v172, v74, v174
	v_add_f32_e32 v172, v173, v172
	s_waitcnt lgkmcnt(0)
	v_mul_f32_e32 v177, v81, v177
	v_add_f32_e32 v180, v180, v172
	v_fmac_f32_e32 v177, v80, v176
	v_mul_f32_e32 v176, v73, v179
	ds_read_b128 v[172:175], v99 offset:47104
	v_fmac_f32_e32 v176, v72, v178
	v_add_f32_e32 v176, v177, v176
	v_add_f32_e32 v180, v180, v176
	ds_read_b128 v[176:179], v99 offset:48128
	s_waitcnt lgkmcnt(1)
	v_mul_f32_e32 v173, v69, v173
	v_fmac_f32_e32 v173, v68, v172
	v_mul_f32_e32 v172, v65, v175
	v_fmac_f32_e32 v172, v64, v174
	v_add_f32_e32 v172, v173, v172
	s_waitcnt lgkmcnt(0)
	v_mul_f32_e32 v173, v71, v177
	v_fmac_f32_e32 v173, v70, v176
	v_mul_f32_e32 v179, v67, v179
	ds_read_b128 v[174:177], v99 offset:49152
	v_fmac_f32_e32 v179, v66, v178
	v_add_f32_e32 v172, v180, v172
	v_add_f32_e32 v173, v173, v179
	ds_read_b128 v[178:181], v99 offset:50176
	v_add_f32_e32 v172, v172, v173
	s_waitcnt lgkmcnt(1)
	v_mul_f32_e32 v173, v93, v175
	v_fmac_f32_e32 v173, v92, v174
	v_mul_f32_e32 v174, v91, v177
	v_fmac_f32_e32 v174, v90, v176
	s_waitcnt lgkmcnt(0)
	v_mul_f32_e32 v179, v95, v179
	v_add_f32_e32 v173, v173, v174
	v_fmac_f32_e32 v179, v94, v178
	v_mul_f32_e32 v178, v89, v181
	ds_read_b128 v[174:177], v99 offset:51200
	v_fmac_f32_e32 v178, v88, v180
	v_add_f32_e32 v173, 0, v173
	v_add_f32_e32 v178, v179, v178
	v_add_f32_e32 v173, v173, v178
	ds_read_b128 v[178:181], v99 offset:52224
	s_waitcnt lgkmcnt(1)
	v_mul_f32_e32 v175, v85, v175
	v_fmac_f32_e32 v175, v84, v174
	v_mul_f32_e32 v174, v83, v177
	v_fmac_f32_e32 v174, v82, v176
	v_add_f32_e32 v174, v175, v174
	s_waitcnt lgkmcnt(0)
	v_mul_f32_e32 v179, v87, v179
	v_add_f32_e32 v173, v173, v174
	v_fmac_f32_e32 v179, v86, v178
	v_mul_f32_e32 v178, v79, v181
	ds_read_b128 v[174:177], v99 offset:53248
	v_fmac_f32_e32 v178, v78, v180
	v_add_f32_e32 v178, v179, v178
	v_add_f32_e32 v173, v173, v178
	ds_read_b128 v[178:181], v99 offset:54272
	s_waitcnt lgkmcnt(1)
	v_mul_f32_e32 v175, v77, v175
	v_fmac_f32_e32 v175, v76, v174
	v_mul_f32_e32 v174, v75, v177
	v_fmac_f32_e32 v174, v74, v176
	v_add_f32_e32 v174, v175, v174
	s_waitcnt lgkmcnt(0)
	v_mul_f32_e32 v179, v81, v179
	v_add_f32_e32 v173, v173, v174
	v_fmac_f32_e32 v179, v80, v178
	v_mul_f32_e32 v178, v73, v181
	ds_read_b128 v[174:177], v99 offset:55296
	v_fmac_f32_e32 v178, v72, v180
	v_add_f32_e32 v178, v179, v178
	v_add_f32_e32 v173, v173, v178
	ds_read_b128 v[178:181], v99 offset:56320
	s_waitcnt lgkmcnt(1)
	v_mul_f32_e32 v175, v69, v175
	v_fmac_f32_e32 v175, v68, v174
	v_mul_f32_e32 v174, v65, v177
	v_fmac_f32_e32 v174, v64, v176
	v_add_f32_e32 v174, v175, v174
	s_waitcnt lgkmcnt(0)
	v_mul_f32_e32 v179, v71, v179
	v_add_f32_e32 v173, v173, v174
	v_fmac_f32_e32 v179, v70, v178
	v_mul_f32_e32 v178, v67, v181
	ds_read_b128 v[174:177], v99 offset:57344
	v_fmac_f32_e32 v178, v66, v180
	v_add_f32_e32 v178, v179, v178
	v_add_f32_e32 v173, v173, v178
	ds_read_b128 v[178:181], v99 offset:58368
	s_waitcnt lgkmcnt(1)
; #define LAS __attribute__((address_space(3)))
; template <int MODE, bool SB  > DI void norm_phase(const Params& P, const Frame& F, int L, const void* src_, const float* gain, bool combine) {
;     ...
;             for (int q = 0; q < 16; ++q) { float t = 0.f;
; #pragma unroll
;                 for (int j = 0; j < 8; ++j) { const f32x4 w = *(const LAS f32x4*)(F.lds + (size_t)(q * D + 256 * j + 4 * F.lane) * 4); t += (v[j][0] * w[0] + v[j][1] * w[1]) + (v[j][2] * w[2] + v[j][3] * w[3]); }
;                 s[q] = t; if ((q & 3) == 3) asm volatile("" ::: "memory"); }
	v_mul_f32_e32 v175, v93, v175
	v_fmac_f32_e32 v175, v92, v174
	v_mul_f32_e32 v174, v91, v177
	v_fmac_f32_e32 v174, v90, v176
	v_add_f32_e32 v174, v175, v174
	s_waitcnt lgkmcnt(0)
	v_mul_f32_e32 v179, v95, v179
	v_add_f32_e32 v182, 0, v174
	v_fmac_f32_e32 v179, v94, v178
	v_mul_f32_e32 v178, v89, v181
	ds_read_b128 v[174:177], v99 offset:59392
	v_fmac_f32_e32 v178, v88, v180
	v_add_f32_e32 v178, v179, v178
	v_add_f32_e32 v182, v182, v178
	ds_read_b128 v[178:181], v99 offset:60416
	s_waitcnt lgkmcnt(1)
	v_mul_f32_e32 v175, v85, v175
	v_fmac_f32_e32 v175, v84, v174
	v_mul_f32_e32 v174, v83, v177
	v_fmac_f32_e32 v174, v82, v176
	v_add_f32_e32 v174, v175, v174
	s_waitcnt lgkmcnt(0)
	v_mul_f32_e32 v179, v87, v179
	v_add_f32_e32 v182, v182, v174
	v_fmac_f32_e32 v179, v86, v178
	v_mul_f32_e32 v178, v79, v181
	ds_read_b128 v[174:177], v99 offset:61440
	v_fmac_f32_e32 v178, v78, v180
	v_add_f32_e32 v178, v179, v178
	v_add_f32_e32 v182, v182, v178
	ds_read_b128 v[178:181], v99 offset:62464
	s_waitcnt lgkmcnt(1)
	v_mul_f32_e32 v175, v77, v175
	v_fmac_f32_e32 v175, v76, v174
	v_mul_f32_e32 v174, v75, v177
	v_fmac_f32_e32 v174, v74, v176
	v_add_f32_e32 v174, v175, v174
	s_waitcnt lgkmcnt(0)
	v_mul_f32_e32 v179, v81, v179
	v_add_f32_e32 v182, v182, v174
	v_fmac_f32_e32 v179, v80, v178
	v_mul_f32_e32 v178, v73, v181
	ds_read_b128 v[174:177], v99 offset:63488
	v_fmac_f32_e32 v178, v72, v180
	v_add_f32_e32 v178, v179, v178
	v_add_f32_e32 v182, v182, v178
	ds_read_b128 v[178:181], v99 offset:64512
	s_waitcnt lgkmcnt(1)
	v_mul_f32_e32 v175, v69, v175
	v_fmac_f32_e32 v175, v68, v174
	v_mul_f32_e32 v174, v65, v177
	v_fmac_f32_e32 v174, v64, v176
	v_add_f32_e32 v174, v175, v174
	s_waitcnt lgkmcnt(0)
	v_mul_f32_e32 v175, v71, v179
	v_fmac_f32_e32 v175, v70, v178
	v_mul_f32_e32 v181, v67, v181
	ds_read_b128 v[176:179], v100
	v_fmac_f32_e32 v181, v66, v180
	v_add_f32_e32 v174, v182, v174
	v_add_f32_e32 v175, v175, v181
	ds_read_b128 v[180:183], v101
	v_add_f32_e32 v174, v174, v175
	s_waitcnt lgkmcnt(1)
	v_mul_f32_e32 v175, v93, v177
	v_fmac_f32_e32 v175, v92, v176
	v_mul_f32_e32 v176, v91, v179
	v_fmac_f32_e32 v176, v90, v178
	s_waitcnt lgkmcnt(0)
	v_mul_f32_e32 v181, v95, v181
	v_add_f32_e32 v175, v175, v176
	v_fmac_f32_e32 v181, v94, v180
	v_mul_f32_e32 v180, v89, v183
	ds_read_b128 v[176:179], v102
	v_fmac_f32_e32 v180, v88, v182
	v_add_f32_e32 v175, 0, v175
	v_add_f32_e32 v180, v181, v180
	v_add_f32_e32 v175, v175, v180
	ds_read_b128 v[180:183], v103
	s_waitcnt lgkmcnt(1)
	v_mul_f32_e32 v177, v85, v177
	v_fmac_f32_e32 v177, v84, v176
	v_mul_f32_e32 v176, v83, v179
	v_fmac_f32_e32 v176, v82, v178
	v_add_f32_e32 v176, v177, v176
	s_waitcnt lgkmcnt(0)
	v_mul_f32_e32 v181, v87, v181
	v_add_f32_e32 v175, v175, v176
	v_fmac_f32_e32 v181, v86, v180
	v_mul_f32_e32 v180, v79, v183
	ds_read_b128 v[176:179], v104
	v_fmac_f32_e32 v180, v78, v182
	v_add_f32_e32 v180, v181, v180
	v_add_f32_e32 v175, v175, v180
	ds_read_b128 v[180:183], v105
	s_waitcnt lgkmcnt(1)
	v_mul_f32_e32 v177, v77, v177
	v_fmac_f32_e32 v177, v76, v176
	v_mul_f32_e32 v176, v75, v179
	v_fmac_f32_e32 v176, v74, v178
	v_add_f32_e32 v176, v177, v176
	s_waitcnt lgkmcnt(0)
	v_mul_f32_e32 v181, v81, v181
	v_add_f32_e32 v175, v175, v176
	v_fmac_f32_e32 v181, v80, v180
	v_mul_f32_e32 v180, v73, v183
	ds_read_b128 v[176:179], v106
	v_fmac_f32_e32 v180, v72, v182
	v_add_f32_e32 v180, v181, v180
	v_add_f32_e32 v175, v175, v180
	ds_read_b128 v[180:183], v107
	s_waitcnt lgkmcnt(1)
	v_mul_f32_e32 v177, v69, v177
	v_fmac_f32_e32 v177, v68, v176
	v_mul_f32_e32 v176, v65, v179
	v_fmac_f32_e32 v176, v64, v178
	v_add_f32_e32 v176, v177, v176
	s_waitcnt lgkmcnt(0)
	v_mul_f32_e32 v181, v71, v181
	v_add_f32_e32 v175, v175, v176
	v_fmac_f32_e32 v181, v70, v180
	v_mul_f32_e32 v180, v67, v183
	ds_read_b128 v[176:179], v108
	v_fmac_f32_e32 v180, v66, v182
	v_add_f32_e32 v180, v181, v180
	v_add_f32_e32 v175, v175, v180
	ds_read_b128 v[180:183], v109
	s_waitcnt lgkmcnt(1)
	v_mul_f32_e32 v177, v93, v177
	v_fmac_f32_e32 v177, v92, v176
	v_mul_f32_e32 v176, v91, v179
	v_fmac_f32_e32 v176, v90, v178
	v_add_f32_e32 v176, v177, v176
	s_waitcnt lgkmcnt(0)
	v_mul_f32_e32 v181, v95, v181
	v_add_f32_e32 v184, 0, v176
	v_fmac_f32_e32 v181, v94, v180
	v_mul_f32_e32 v180, v89, v183
	ds_read_b128 v[176:179], v110
	v_fmac_f32_e32 v180, v88, v182
	v_add_f32_e32 v180, v181, v180
	v_add_f32_e32 v184, v184, v180
	ds_read_b128 v[180:183], v111
	s_waitcnt lgkmcnt(1)
	v_mul_f32_e32 v177, v85, v177
	v_fmac_f32_e32 v177, v84, v176
	v_mul_f32_e32 v176, v83, v179
	v_fmac_f32_e32 v176, v82, v178
	v_add_f32_e32 v176, v177, v176
	s_waitcnt lgkmcnt(0)
	v_mul_f32_e32 v181, v87, v181
	v_add_f32_e32 v184, v184, v176
	v_fmac_f32_e32 v181, v86, v180
	v_mul_f32_e32 v180, v79, v183
	ds_read_b128 v[176:179], v112
	v_fmac_f32_e32 v180, v78, v182
	v_add_f32_e32 v180, v181, v180
	v_add_f32_e32 v184, v184, v180
	ds_read_b128 v[180:183], v113
	s_waitcnt lgkmcnt(1)
	v_mul_f32_e32 v177, v77, v177
	v_fmac_f32_e32 v177, v76, v176
	v_mul_f32_e32 v176, v75, v179
	v_fmac_f32_e32 v176, v74, v178
	v_add_f32_e32 v176, v177, v176
	s_waitcnt lgkmcnt(0)
	v_mul_f32_e32 v181, v81, v181
	v_add_f32_e32 v184, v184, v176
	v_fmac_f32_e32 v181, v80, v180
	v_mul_f32_e32 v180, v73, v183
	ds_read_b128 v[176:179], v114
	v_fmac_f32_e32 v180, v72, v182
	v_add_f32_e32 v180, v181, v180
	v_add_f32_e32 v184, v184, v180
	ds_read_b128 v[180:183], v115
	s_waitcnt lgkmcnt(1)
	v_mul_f32_e32 v177, v69, v177
	v_fmac_f32_e32 v177, v68, v176
	v_mul_f32_e32 v176, v65, v179
	v_fmac_f32_e32 v176, v64, v178
	v_add_f32_e32 v176, v177, v176
	s_waitcnt lgkmcnt(0)
; #define LAS __attribute__((address_space(3)))
; template <int MODE, bool SB  > DI void norm_phase(const Params& P, const Frame& F, int L, const void* src_, const float* gain, bool combine) {
;     ...
;             for (int q = 0; q < 16; ++q) { float t = 0.f;
; #pragma unroll
;                 for (int j = 0; j < 8; ++j) { const f32x4 w = *(const LAS f32x4*)(F.lds + (size_t)(q * D + 256 * j + 4 * F.lane) * 4); t += (v[j][0] * w[0] + v[j][1] * w[1]) + (v[j][2] * w[2] + v[j][3] * w[3]); }
;                 s[q] = t; if ((q & 3) == 3) asm volatile("" ::: "memory"); }
	v_mul_f32_e32 v177, v71, v181
	v_mul_f32_e32 v183, v67, v183
	v_fmac_f32_e32 v177, v70, v180
	ds_read_b128 v[178:181], v116
	v_fmac_f32_e32 v183, v66, v182
	v_add_f32_e32 v176, v184, v176
	v_add_f32_e32 v177, v177, v183
	ds_read_b128 v[182:185], v117
	v_add_f32_e32 v176, v176, v177
	s_waitcnt lgkmcnt(1)
	v_mul_f32_e32 v177, v93, v179
	v_fmac_f32_e32 v177, v92, v178
	v_mul_f32_e32 v178, v91, v181
	s_waitcnt lgkmcnt(0)
	v_mul_f32_e32 v183, v95, v183
	v_fmac_f32_e32 v178, v90, v180
	v_fmac_f32_e32 v183, v94, v182
	v_mul_f32_e32 v182, v89, v185
	v_add_f32_e32 v177, v177, v178
	ds_read_b128 v[178:181], v118
	v_fmac_f32_e32 v182, v88, v184
	v_add_f32_e32 v177, 0, v177
	v_add_f32_e32 v182, v183, v182
	v_add_f32_e32 v177, v177, v182
	ds_read_b128 v[182:185], v119
	s_waitcnt lgkmcnt(1)
	v_mul_f32_e32 v179, v85, v179
	v_fmac_f32_e32 v179, v84, v178
	v_mul_f32_e32 v178, v83, v181
	v_fmac_f32_e32 v178, v82, v180
	s_waitcnt lgkmcnt(0)
	v_mul_f32_e32 v183, v87, v183
	v_add_f32_e32 v178, v179, v178
	v_fmac_f32_e32 v183, v86, v182
	v_mul_f32_e32 v182, v79, v185
	v_add_f32_e32 v177, v177, v178
	ds_read_b128 v[178:181], v120
	v_fmac_f32_e32 v182, v78, v184
	v_add_f32_e32 v182, v183, v182
	v_add_f32_e32 v177, v177, v182
	ds_read_b128 v[182:185], v121
	s_waitcnt lgkmcnt(1)
	v_mul_f32_e32 v179, v77, v179
	v_fmac_f32_e32 v179, v76, v178
	v_mul_f32_e32 v178, v75, v181
	v_fmac_f32_e32 v178, v74, v180
	s_waitcnt lgkmcnt(0)
	v_mul_f32_e32 v183, v81, v183
	v_add_f32_e32 v178, v179, v178
	v_fmac_f32_e32 v183, v80, v182
	v_mul_f32_e32 v182, v73, v185
	v_add_f32_e32 v177, v177, v178
	ds_read_b128 v[178:181], v122
	v_fmac_f32_e32 v182, v72, v184
	v_add_f32_e32 v182, v183, v182
	v_add_f32_e32 v177, v177, v182
	ds_read_b128 v[182:185], v123
	s_waitcnt lgkmcnt(1)
	v_mul_f32_e32 v179, v69, v179
	v_fmac_f32_e32 v179, v68, v178
	v_mul_f32_e32 v178, v65, v181
	v_fmac_f32_e32 v178, v64, v180
	s_waitcnt lgkmcnt(0)
	v_mul_f32_e32 v183, v71, v183
	v_add_f32_e32 v178, v179, v178
	v_fmac_f32_e32 v183, v70, v182
	v_mul_f32_e32 v182, v67, v185
	v_add_f32_e32 v177, v177, v178
	ds_read_b128 v[178:181], v124
	v_fmac_f32_e32 v182, v66, v184
	v_add_f32_e32 v182, v183, v182
	v_add_f32_e32 v177, v177, v182
	ds_read_b128 v[182:185], v125
	s_waitcnt lgkmcnt(1)
	v_mul_f32_e32 v179, v93, v179
	v_fmac_f32_e32 v179, v92, v178
	v_mul_f32_e32 v178, v91, v181
	v_fmac_f32_e32 v178, v90, v180
	s_waitcnt lgkmcnt(0)
	v_mul_f32_e32 v183, v95, v183
	v_add_f32_e32 v178, v179, v178
	v_fmac_f32_e32 v183, v94, v182
	v_mul_f32_e32 v182, v89, v185
	v_add_f32_e32 v186, 0, v178
	ds_read_b128 v[178:181], v126
	v_fmac_f32_e32 v182, v88, v184
	v_add_f32_e32 v182, v183, v182
	v_add_f32_e32 v186, v186, v182
	ds_read_b128 v[182:185], v127
	s_waitcnt lgkmcnt(1)
	v_mul_f32_e32 v179, v85, v179
	v_fmac_f32_e32 v179, v84, v178
	v_mul_f32_e32 v178, v83, v181
	v_fmac_f32_e32 v178, v82, v180
	s_waitcnt lgkmcnt(0)
	v_mul_f32_e32 v183, v87, v183
	v_add_f32_e32 v178, v179, v178
	v_fmac_f32_e32 v183, v86, v182
	v_mul_f32_e32 v182, v79, v185
	v_add_f32_e32 v186, v186, v178
	ds_read_b128 v[178:181], v128
	v_fmac_f32_e32 v182, v78, v184
	v_add_f32_e32 v182, v183, v182
	v_add_f32_e32 v186, v186, v182
	ds_read_b128 v[182:185], v129
	s_waitcnt lgkmcnt(1)
	v_mul_f32_e32 v179, v77, v179
	v_fmac_f32_e32 v179, v76, v178
	v_mul_f32_e32 v178, v75, v181
	v_fmac_f32_e32 v178, v74, v180
	s_waitcnt lgkmcnt(0)
	v_mul_f32_e32 v183, v81, v183
	v_add_f32_e32 v178, v179, v178
	v_fmac_f32_e32 v183, v80, v182
	v_mul_f32_e32 v182, v73, v185
	v_add_f32_e32 v186, v186, v178
	ds_read_b128 v[178:181], v130
	v_fmac_f32_e32 v182, v72, v184
	v_add_f32_e32 v182, v183, v182
	v_add_f32_e32 v186, v186, v182
	ds_read_b128 v[182:185], v131
	s_waitcnt lgkmcnt(1)
	v_mul_f32_e32 v179, v69, v179
	v_fmac_f32_e32 v179, v68, v178
	v_mul_f32_e32 v178, v65, v181
	v_fmac_f32_e32 v178, v64, v180
	s_waitcnt lgkmcnt(0)
	v_mul_f32_e32 v183, v71, v183
	v_add_f32_e32 v178, v179, v178
	v_fmac_f32_e32 v183, v70, v182
	v_mul_f32_e32 v182, v67, v185
	v_add_f32_e32 v186, v186, v178
	ds_read_b128 v[178:181], v132
	v_fmac_f32_e32 v182, v66, v184
	v_add_f32_e32 v182, v183, v182
	v_add_f32_e32 v186, v186, v182
	ds_read_b128 v[182:185], v133
	s_waitcnt lgkmcnt(1)
	v_mul_f32_e32 v179, v93, v179
	v_fmac_f32_e32 v179, v92, v178
	v_mul_f32_e32 v178, v91, v181
	v_fmac_f32_e32 v178, v90, v180
	s_waitcnt lgkmcnt(0)
	v_mul_f32_e32 v183, v95, v183
	v_add_f32_e32 v178, v179, v178
	v_fmac_f32_e32 v183, v94, v182
	v_mul_f32_e32 v182, v89, v185
	v_add_f32_e32 v187, 0, v178
	ds_read_b128 v[178:181], v134
	v_fmac_f32_e32 v182, v88, v184
	v_add_f32_e32 v182, v183, v182
	v_add_f32_e32 v187, v187, v182
	ds_read_b128 v[182:185], v135
	s_waitcnt lgkmcnt(1)
	v_mul_f32_e32 v179, v85, v179
	v_fmac_f32_e32 v179, v84, v178
	v_mul_f32_e32 v178, v83, v181
	v_fmac_f32_e32 v178, v82, v180
	s_waitcnt lgkmcnt(0)
	v_mul_f32_e32 v183, v87, v183
	v_add_f32_e32 v178, v179, v178
	v_fmac_f32_e32 v183, v86, v182
	v_mul_f32_e32 v182, v79, v185
	v_add_f32_e32 v187, v187, v178
	ds_read_b128 v[178:181], v136
	v_fmac_f32_e32 v182, v78, v184
	v_add_f32_e32 v182, v183, v182
	v_add_f32_e32 v187, v187, v182
	ds_read_b128 v[182:185], v137
	s_waitcnt lgkmcnt(1)
	v_mul_f32_e32 v179, v77, v179
	v_fmac_f32_e32 v179, v76, v178
	v_mul_f32_e32 v178, v75, v181
	v_fmac_f32_e32 v178, v74, v180
	s_waitcnt lgkmcnt(0)
	v_mul_f32_e32 v183, v81, v183
	v_add_f32_e32 v178, v179, v178
	v_fmac_f32_e32 v183, v80, v182
	v_mul_f32_e32 v182, v73, v185
	v_add_f32_e32 v187, v187, v178
	ds_read_b128 v[178:181], v138
	v_fmac_f32_e32 v182, v72, v184
	v_add_f32_e32 v182, v183, v182
	v_add_f32_e32 v187, v187, v182
	ds_read_b128 v[182:185], v139
	s_waitcnt lgkmcnt(1)
; #define LAS __attribute__((address_space(3)))
; template <int MODE, bool SB  > DI void norm_phase(const Params& P, const Frame& F, int L, const void* src_, const float* gain, bool combine) {
;     ...
;             for (int q = 0; q < 16; ++q) { float t = 0.f;
; #pragma unroll
;                 for (int j = 0; j < 8; ++j) { const f32x4 w = *(const LAS f32x4*)(F.lds + (size_t)(q * D + 256 * j + 4 * F.lane) * 4); t += (v[j][0] * w[0] + v[j][1] * w[1]) + (v[j][2] * w[2] + v[j][3] * w[3]); }
;                 s[q] = t; if ((q & 3) == 3) asm volatile("" ::: "memory"); }
	v_mul_f32_e32 v179, v69, v179
	v_fmac_f32_e32 v179, v68, v178
	v_mul_f32_e32 v178, v65, v181
	v_fmac_f32_e32 v178, v64, v180
	s_waitcnt lgkmcnt(0)
	v_mul_f32_e32 v183, v71, v183
	v_add_f32_e32 v178, v179, v178
	v_fmac_f32_e32 v183, v70, v182
	v_mul_f32_e32 v182, v67, v185
	v_add_f32_e32 v187, v187, v178
	ds_read_b128 v[178:181], v140
	v_fmac_f32_e32 v182, v66, v184
	v_add_f32_e32 v182, v183, v182
	v_add_f32_e32 v187, v187, v182
	ds_read_b128 v[182:185], v141
	s_waitcnt lgkmcnt(1)
	v_mul_f32_e32 v179, v93, v179
	v_fmac_f32_e32 v179, v92, v178
	v_mul_f32_e32 v178, v91, v181
	v_fmac_f32_e32 v178, v90, v180
	s_waitcnt lgkmcnt(0)
	v_mul_f32_e32 v183, v95, v183
	v_add_f32_e32 v178, v179, v178
	v_fmac_f32_e32 v183, v94, v182
	v_mul_f32_e32 v182, v89, v185
	v_add_f32_e32 v188, 0, v178
	ds_read_b128 v[178:181], v142
	v_fmac_f32_e32 v182, v88, v184
	v_add_f32_e32 v182, v183, v182
	v_add_f32_e32 v188, v188, v182
	ds_read_b128 v[182:185], v143
	s_waitcnt lgkmcnt(1)
	v_mul_f32_e32 v179, v85, v179
	v_fmac_f32_e32 v179, v84, v178
	v_mul_f32_e32 v178, v83, v181
	v_fmac_f32_e32 v178, v82, v180
	s_waitcnt lgkmcnt(0)
	v_mul_f32_e32 v183, v87, v183
	v_add_f32_e32 v178, v179, v178
	v_fmac_f32_e32 v183, v86, v182
	v_mul_f32_e32 v182, v79, v185
	v_add_f32_e32 v188, v188, v178
	ds_read_b128 v[178:181], v144
	v_fmac_f32_e32 v182, v78, v184
	v_add_f32_e32 v182, v183, v182
	v_add_f32_e32 v188, v188, v182
	ds_read_b128 v[182:185], v145
	s_waitcnt lgkmcnt(1)
	v_mul_f32_e32 v179, v77, v179
	v_fmac_f32_e32 v179, v76, v178
	v_mul_f32_e32 v178, v75, v181
	v_fmac_f32_e32 v178, v74, v180
	s_waitcnt lgkmcnt(0)
	v_mul_f32_e32 v183, v81, v183
	v_add_f32_e32 v178, v179, v178
	v_fmac_f32_e32 v183, v80, v182
	v_mul_f32_e32 v182, v73, v185
	v_add_f32_e32 v188, v188, v178
	ds_read_b128 v[178:181], v146
	v_fmac_f32_e32 v182, v72, v184
	v_add_f32_e32 v182, v183, v182
	v_add_f32_e32 v188, v188, v182
	ds_read_b128 v[182:185], v147
	s_waitcnt lgkmcnt(1)
	v_mul_f32_e32 v179, v69, v179
	v_fmac_f32_e32 v179, v68, v178
	v_mul_f32_e32 v178, v65, v181
	v_fmac_f32_e32 v178, v64, v180
	s_waitcnt lgkmcnt(0)
	v_mul_f32_e32 v183, v71, v183
	v_add_f32_e32 v178, v179, v178
	v_fmac_f32_e32 v183, v70, v182
	v_mul_f32_e32 v182, v67, v185
	v_add_f32_e32 v188, v188, v178
	ds_read_b128 v[178:181], v148
	v_fmac_f32_e32 v182, v66, v184
	v_add_f32_e32 v182, v183, v182
	v_add_f32_e32 v188, v188, v182
	ds_read_b128 v[182:185], v149
	s_waitcnt lgkmcnt(1)
	v_mul_f32_e32 v179, v93, v179
	v_fmac_f32_e32 v179, v92, v178
	v_mul_f32_e32 v178, v91, v181
	v_fmac_f32_e32 v178, v90, v180
	s_waitcnt lgkmcnt(0)
	v_mul_f32_e32 v183, v95, v183
	v_add_f32_e32 v178, v179, v178
	v_fmac_f32_e32 v183, v94, v182
	v_mul_f32_e32 v182, v89, v185
	v_add_f32_e32 v189, 0, v178
	ds_read_b128 v[178:181], v150
	v_fmac_f32_e32 v182, v88, v184
	v_add_f32_e32 v182, v183, v182
	v_add_f32_e32 v189, v189, v182
	ds_read_b128 v[182:185], v151
	s_waitcnt lgkmcnt(1)
	v_mul_f32_e32 v179, v85, v179
	v_fmac_f32_e32 v179, v84, v178
	v_mul_f32_e32 v178, v83, v181
	v_fmac_f32_e32 v178, v82, v180
	s_waitcnt lgkmcnt(0)
	v_mul_f32_e32 v183, v87, v183
	v_add_f32_e32 v178, v179, v178
	v_fmac_f32_e32 v183, v86, v182
	v_mul_f32_e32 v182, v79, v185
	v_add_f32_e32 v189, v189, v178
	ds_read_b128 v[178:181], v152
	v_fmac_f32_e32 v182, v78, v184
	v_add_f32_e32 v182, v183, v182
	v_add_f32_e32 v189, v189, v182
	ds_read_b128 v[182:185], v153
	s_waitcnt lgkmcnt(1)
	v_mul_f32_e32 v179, v77, v179
	v_fmac_f32_e32 v179, v76, v178
	v_mul_f32_e32 v178, v75, v181
	v_fmac_f32_e32 v178, v74, v180
	s_waitcnt lgkmcnt(0)
	v_mul_f32_e32 v183, v81, v183
	v_add_f32_e32 v178, v179, v178
	v_fmac_f32_e32 v183, v80, v182
	v_mul_f32_e32 v182, v73, v185
	v_add_f32_e32 v189, v189, v178
	ds_read_b128 v[178:181], v154
	v_fmac_f32_e32 v182, v72, v184
	v_add_f32_e32 v182, v183, v182
	v_add_f32_e32 v189, v189, v182
	ds_read_b128 v[182:185], v155
	s_waitcnt lgkmcnt(1)
	v_mul_f32_e32 v179, v69, v179
	v_fmac_f32_e32 v179, v68, v178
	v_mul_f32_e32 v178, v65, v181
	v_fmac_f32_e32 v178, v64, v180
	s_waitcnt lgkmcnt(0)
	v_mul_f32_e32 v183, v71, v183
	v_add_f32_e32 v178, v179, v178
	v_fmac_f32_e32 v183, v70, v182
	v_mul_f32_e32 v182, v67, v185
	v_add_f32_e32 v189, v189, v178
	ds_read_b128 v[178:181], v156
	v_fmac_f32_e32 v182, v66, v184
	v_add_f32_e32 v182, v183, v182
	v_add_f32_e32 v189, v189, v182
	ds_read_b128 v[182:185], v157
	s_waitcnt lgkmcnt(1)
	v_mul_f32_e32 v93, v93, v179
	v_mul_f32_e32 v91, v91, v181
	v_fmac_f32_e32 v93, v92, v178
	v_fmac_f32_e32 v91, v90, v180
	v_add_f32_e32 v90, v93, v91
	s_waitcnt lgkmcnt(0)
	v_mul_f32_e32 v95, v95, v183
	v_mul_f32_e32 v89, v89, v185
	v_add_f32_e32 v178, 0, v90
	v_fmac_f32_e32 v95, v94, v182
	ds_read_b128 v[90:93], v158
	v_fmac_f32_e32 v89, v88, v184
	v_add_f32_e32 v88, v95, v89
	v_add_f32_e32 v88, v178, v88
	ds_read_b128 v[178:181], v159
	s_waitcnt lgkmcnt(1)
	v_mul_f32_e32 v85, v85, v91
	v_mul_f32_e32 v83, v83, v93
	v_fmac_f32_e32 v85, v84, v90
	v_fmac_f32_e32 v83, v82, v92
	v_add_f32_e32 v82, v85, v83
	s_waitcnt lgkmcnt(0)
	v_mul_f32_e32 v87, v87, v179
	v_mul_f32_e32 v79, v79, v181
	v_add_f32_e32 v88, v88, v82
	v_fmac_f32_e32 v87, v86, v178
	ds_read_b128 v[82:85], v160
	v_fmac_f32_e32 v79, v78, v180
	v_add_f32_e32 v78, v87, v79
	v_add_f32_e32 v78, v88, v78
	ds_read_b128 v[86:89], v161
	s_waitcnt lgkmcnt(1)
	v_mul_f32_e32 v77, v77, v83
	v_mul_f32_e32 v75, v75, v85
	v_fmac_f32_e32 v77, v76, v82
	v_fmac_f32_e32 v75, v74, v84
	v_add_f32_e32 v74, v77, v75
	s_waitcnt lgkmcnt(0)
	v_mul_f32_e32 v79, v81, v87
	v_mul_f32_e32 v73, v73, v89
	v_add_f32_e32 v78, v78, v74
	v_fmac_f32_e32 v79, v80, v86
	ds_read_b128 v[74:77], v162
	v_fmac_f32_e32 v73, v72, v88
	v_add_f32_e32 v72, v79, v73
	v_add_f32_e32 v72, v78, v72
	ds_read_b128 v[78:81], v163
	s_waitcnt lgkmcnt(1)
; DI float sigmoidf_(float x) { return __builtin_amdgcn_rcpf(1.0f + __expf(-x)); }
; DI float softplusf_(float x) { return fmaxf(x, 0.f) + log1pf(__expf(-fabsf(x))); }
; template <int MODE, bool SB  > DI void norm_phase(const Params& P, const Frame& F, int L, const void* src_, const float* gain, bool combine) {
;     ...
;             for (int i = 0; i < 8; ++i) { const bool hi = (F.lane & 32) != 0; const float send = hi ? s[i] : s[i + 8], keep = hi ? s[i + 8] : s[i]; s[i] = keep + shx<32>(send); }
; #pragma unroll
;             for (int i = 0; i < 4; ++i) { const bool hi = (F.lane & 16) != 0; const float send = hi ? s[i] : s[i + 4], keep = hi ? s[i + 4] : s[i]; s[i] = keep + shx<16>(send); }
; #pragma unroll
;             for (int i = 0; i < 2; ++i) { const bool hi = (F.lane & 8) != 0; const float send = hi ? s[i] : s[i + 2], keep = hi ? s[i + 2] : s[i]; s[i] = keep + shx<8>(send); }
;             { const bool hi = (F.lane & 4) != 0; const float send = hi ? s[0] : s[1], keep = hi ? s[1] : s[0]; s[0] = keep + shx<4>(send); }
;             float mine = s[0]; mine += shx<2>(mine); mine += shx<1>(mine);
;             if ((F.lane & 3) == 0) { const int gi = ((F.lane >> 5) & 1) * 8 + ((F.lane >> 4) & 1) * 4 + ((F.lane >> 3) & 1) * 2 + ((F.lane >> 2) & 1), h = gi & 3; float r;
;                 if (gi < 4) r = sigmoidf_(mine);
;                 else if (gi < 8) r = -__expf(P.in[I_DN_A_LOG][L * 4 + h]) * softplusf_(mine + P.in[I_DN_DT_BIAS][L * 4 + h]);
;                 else if (gi < 12) r = mine + P.in[I_ML_I_BIAS][L * 4 + h];
;                 else r = -softplusf_(-(mine + P.in[I_ML_F_BIAS][L * 4 + h]));
	v_mul_f32_e32 v69, v69, v75
	v_mul_f32_e32 v65, v65, v77
	v_fmac_f32_e32 v69, v68, v74
	v_fmac_f32_e32 v65, v64, v76
	v_add_f32_e32 v64, v69, v65
	s_waitcnt lgkmcnt(0)
	v_mul_f32_e32 v65, v71, v79
	v_mul_f32_e32 v67, v67, v81
	v_fmac_f32_e32 v65, v70, v78
	v_fmac_f32_e32 v67, v66, v80
	v_add_f32_e32 v64, v72, v64
	v_add_f32_e32 v65, v65, v67
	v_add_f32_e32 v64, v64, v65
	v_cndmask_b32_e64 v65, v47, v175, s[4:5]
	ds_bpermute_b32 v65, v98, v65
	v_cndmask_b32_e64 v66, v96, v176, s[4:5]
	ds_bpermute_b32 v66, v98, v66
	v_cndmask_b32_e64 v67, v97, v177, s[4:5]
	ds_bpermute_b32 v67, v98, v67
	v_cndmask_b32_e64 v47, v175, v47, s[4:5]
	s_waitcnt lgkmcnt(2)
	v_add_f32_e32 v47, v47, v65
	v_cndmask_b32_e64 v65, v176, v96, s[4:5]
	s_waitcnt lgkmcnt(1)
	v_add_f32_e32 v65, v65, v66
	v_cndmask_b32_e64 v66, v177, v97, s[4:5]
	s_waitcnt lgkmcnt(0)
	v_add_f32_e32 v66, v66, v67
	v_cndmask_b32_e64 v67, v170, v186, s[4:5]
	ds_bpermute_b32 v67, v98, v67
	v_cndmask_b32_e64 v69, v171, v187, s[4:5]
	ds_bpermute_b32 v69, v98, v69
	v_cndmask_b32_e64 v70, v172, v188, s[4:5]
	ds_bpermute_b32 v70, v98, v70
	v_cndmask_b32_e64 v68, v186, v170, s[4:5]
	s_waitcnt lgkmcnt(2)
	v_add_f32_e32 v67, v68, v67
	v_cndmask_b32_e64 v68, v187, v171, s[4:5]
	s_waitcnt lgkmcnt(1)
	v_add_f32_e32 v68, v68, v69
	v_cndmask_b32_e64 v69, v188, v172, s[4:5]
	s_waitcnt lgkmcnt(0)
	v_add_f32_e32 v69, v69, v70
	v_cndmask_b32_e64 v70, v173, v189, s[4:5]
	v_cndmask_b32_e64 v72, v174, v64, s[4:5]
	ds_bpermute_b32 v70, v98, v70
	ds_bpermute_b32 v72, v98, v72
	v_cndmask_b32_e64 v71, v189, v173, s[4:5]
	v_cndmask_b32_e64 v64, v64, v174, s[4:5]
	v_cndmask_b32_e64 v73, v47, v68, s[8:9]
	s_waitcnt lgkmcnt(1)
	v_add_f32_e32 v70, v71, v70
	s_waitcnt lgkmcnt(0)
	v_add_f32_e32 v64, v64, v72
	v_cndmask_b32_e64 v47, v68, v47, s[8:9]
	v_cndmask_b32_e64 v68, v65, v69, s[8:9]
	v_cndmask_b32_e64 v65, v69, v65, s[8:9]
	v_cndmask_b32_e64 v69, v66, v70, s[8:9]
	v_cndmask_b32_e64 v71, v67, v64, s[8:9]
	ds_swizzle_b32 v73, v73 offset:swizzle(SWAP,16)
	ds_swizzle_b32 v68, v68 offset:swizzle(SWAP,16)
	ds_swizzle_b32 v69, v69 offset:swizzle(SWAP,16)
	ds_swizzle_b32 v71, v71 offset:swizzle(SWAP,16)
	v_cndmask_b32_e64 v66, v70, v66, s[8:9]
	v_cndmask_b32_e64 v64, v64, v67, s[8:9]
	s_waitcnt lgkmcnt(3)
	v_add_f32_e32 v47, v47, v73
	s_waitcnt lgkmcnt(2)
	v_add_f32_e32 v65, v65, v68
	s_waitcnt lgkmcnt(1)
	v_add_f32_e32 v66, v66, v69
	s_waitcnt lgkmcnt(0)
	v_add_f32_e32 v64, v64, v71
	v_cndmask_b32_e64 v67, v47, v66, s[10:11]
	v_cndmask_b32_e64 v68, v65, v64, s[10:11]
	ds_swizzle_b32 v67, v67 offset:swizzle(SWAP,8)
	ds_swizzle_b32 v68, v68 offset:swizzle(SWAP,8)
	v_cndmask_b32_e64 v47, v66, v47, s[10:11]
	v_cndmask_b32_e64 v64, v64, v65, s[10:11]
	s_waitcnt lgkmcnt(1)
	v_add_f32_e32 v47, v47, v67
	s_waitcnt lgkmcnt(0)
	v_add_f32_e32 v64, v64, v68
	v_cndmask_b32_e64 v65, v47, v64, s[12:13]
	ds_swizzle_b32 v65, v65 offset:swizzle(SWAP,4)
	v_cndmask_b32_e64 v47, v64, v47, s[12:13]
	s_waitcnt lgkmcnt(0)
	v_add_f32_e32 v47, v47, v65
	s_nop 1
	v_add_f32_dpp v47, v47, v47 quad_perm:[2,3,0,1] row_mask:0xf bank_mask:0xf bound_ctrl:1
	s_nop 1
	v_mov_b32_dpp v64, v47 quad_perm:[1,0,3,2] row_mask:0xf bank_mask:0xf bound_ctrl:1
	s_and_saveexec_b64 s[20:21], s[14:15]
	s_cbranch_execz .LBB0_1647
	v_add_f32_e32 v47, v47, v64
	s_and_saveexec_b64 s[24:25], s[16:17]
	s_xor_b64 s[24:25], exec, s[24:25]
	s_cbranch_execz .LBB0_1659
	s_and_saveexec_b64 s[26:27], s[6:7]
	s_xor_b64 s[26:27], exec, s[26:27]
	s_cbranch_execz .LBB0_1656
	s_and_saveexec_b64 s[28:29], s[18:19]
	s_xor_b64 s[28:29], exec, s[28:29]
	s_cbranch_execz .LBB0_1653
	v_mov_b32_e32 v64, v190
	v_add_f32_e32 v64, v47, v64
; DI float softplusf_(float x) { return fmaxf(x, 0.f) + log1pf(__expf(-fabsf(x))); }
; template <int MODE, bool SB  > DI void norm_phase(const Params& P, const Frame& F, int L, const void* src_, const float* gain, bool combine) {
;     ...
;                 else r = -softplusf_(-(mine + P.in[I_ML_F_BIAS][L * 4 + h]));
.LBB0_1653:
	s_andn2_saveexec_b64 s[28:29], s[28:29]
	s_cbranch_execz .LBB0_1655
	v_mov_b32_e32 v64, v191
	v_add_f32_e32 v47, v47, v64
	v_max_f32_e64 v64, -v47, 0
	v_mul_f32_e64 v47, |v47|, s1
	v_exp_f32_e32 v65, v47
	s_nop 0
	v_add_f32_e32 v47, 1.0, v65
	v_add_f32_e32 v66, -1.0, v47
	v_sub_f32_e32 v67, v66, v47
	v_add_f32_e32 v67, 1.0, v67
	v_sub_f32_e32 v66, v65, v66
	v_add_f32_e32 v68, v66, v67
	v_frexp_mant_f32_e32 v66, v47
	v_cmp_gt_f32_e32 vcc, s30, v66
	v_cvt_f64_f32_e32 v[66:67], v47
	v_frexp_exp_i32_f64_e32 v66, v[66:67]
	v_subbrev_co_u32_e32 v74, vcc, 0, v66, vcc
	v_sub_u32_e32 v66, 0, v74
	v_ldexp_f32 v47, v47, v66
	v_ldexp_f32 v66, v68, v66
	v_add_f32_e32 v68, -1.0, v47
	v_add_f32_e32 v67, 1.0, v68
	v_sub_f32_e32 v67, v47, v67
	v_add_f32_e32 v69, v66, v67
	v_add_f32_e32 v67, 1.0, v47
	v_add_f32_e32 v70, -1.0, v67
	v_sub_f32_e32 v47, v47, v70
	v_add_f32_e32 v47, v66, v47
	v_add_f32_e32 v75, v67, v47
	v_rcp_f32_e32 v76, v75
	v_sub_f32_e32 v66, v75, v67
	v_add_f32_e32 v67, v68, v69
	v_sub_f32_e32 v47, v47, v66
	v_mul_f32_e32 v78, v67, v76
	v_sub_f32_e32 v66, v67, v68
	v_mul_f32_e32 v68, v75, v78
	v_fma_f32 v70, v78, v75, -v68
	v_fmac_f32_e32 v70, v78, v47
	v_sub_f32_e32 v77, v69, v66
	v_add_f32_e32 v66, v68, v70
	v_sub_f32_e32 v69, v67, v66
	v_pk_add_f32 v[72:73], v[66:67], v[68:69] neg_lo:[0,1] neg_hi:[0,1]
	v_mov_b32_e32 v71, v66
	v_pk_add_f32 v[66:67], v[72:73], v[70:71] neg_lo:[0,1] neg_hi:[0,1]
	v_cmp_neq_f32_e32 vcc, s33, v65
	v_add_f32_e32 v67, v77, v67
	v_add_f32_e32 v66, v66, v67
	v_add_f32_e32 v67, v69, v66
	v_mul_f32_e32 v77, v76, v67
	v_mul_f32_e32 v68, v75, v77
	v_fma_f32 v70, v77, v75, -v68
	v_fmac_f32_e32 v70, v77, v47
	v_sub_f32_e32 v47, v69, v67
	v_add_f32_e32 v47, v66, v47
	v_add_f32_e32 v66, v68, v70
	v_sub_f32_e32 v69, v67, v66
	v_pk_add_f32 v[72:73], v[66:67], v[68:69] neg_lo:[0,1] neg_hi:[0,1]
	v_mov_b32_e32 v71, v66
	v_pk_add_f32 v[66:67], v[72:73], v[70:71] neg_lo:[0,1] neg_hi:[0,1]
	s_nop 0
	v_add_f32_e32 v47, v47, v67
	v_add_f32_e32 v47, v66, v47
	v_add_f32_e32 v67, v78, v77
	v_add_f32_e32 v47, v69, v47
	v_sub_f32_e32 v66, v67, v78
	v_mul_f32_e32 v47, v76, v47
	v_sub_f32_e32 v66, v77, v66
	v_add_f32_e32 v68, v66, v47
	v_add_f32_e32 v70, v67, v68
	v_cvt_f32_i32_e32 v66, v74
	v_mul_f32_e32 v71, v70, v70
	v_sub_f32_e32 v67, v70, v67
	v_fmamk_f32 v47, v71, 0x3e9b6dac, v166
	v_sub_f32_e32 v67, v68, v67
	v_fmaak_f32 v47, v71, v47, 0x3f2aaada
	v_ldexp_f32 v72, v67, 1
	v_mul_f32_e32 v67, v70, v71
	v_ldexp_f32 v69, v70, 1
	v_pk_mul_f32 v[70:71], v[66:67], v[46:47]
	s_nop 0
	v_fma_f32 v68, v66, s31, -v70
	v_fmac_f32_e32 v68, 0xb102e308, v66
	v_pk_add_f32 v[66:67], v[70:71], v[68:69]
	s_nop 0
	v_sub_f32_e32 v47, v67, v69
	v_sub_f32_e32 v47, v71, v47
	v_add_f32_e32 v73, v72, v47
	v_mov_b32_e32 v72, v70
	v_pk_add_f32 v[70:71], v[66:67], v[70:71] neg_lo:[0,1] neg_hi:[0,1]
	v_pk_add_f32 v[74:75], v[66:67], v[72:73]
	v_mov_b32_e32 v69, v66
	v_mov_b32_e32 v71, v75
	v_pk_add_f32 v[76:77], v[68:69], v[70:71] neg_lo:[0,1] neg_hi:[0,1]
	v_pk_add_f32 v[68:69], v[68:69], v[70:71]
	v_mov_b32_e32 v72, v73
	v_pk_add_f32 v[70:71], v[68:69], v[66:67] op_sel:[1,0] op_sel_hi:[0,1] neg_lo:[0,1] neg_hi:[0,1]
	v_pk_add_f32 v[78:79], v[74:75], v[70:71] op_sel_hi:[1,0] neg_lo:[0,1] neg_hi:[0,1]
	v_mov_b32_e32 v74, v75
	v_mov_b32_e32 v75, v69
	v_pk_mov_b32 v[70:71], v[66:67], v[70:71] op_sel:[1,0]
	v_mov_b32_e32 v73, v66
	v_pk_add_f32 v[70:71], v[74:75], v[70:71] neg_lo:[0,1] neg_hi:[0,1]
	v_mov_b32_e32 v78, v76
	v_pk_add_f32 v[66:67], v[72:73], v[70:71] neg_lo:[0,1] neg_hi:[0,1]
	v_mov_b32_e32 v77, v69
	v_pk_add_f32 v[70:71], v[78:79], v[66:67]
	s_nop 0
	v_pk_add_f32 v[72:73], v[70:71], v[70:71] op_sel:[0,1] op_sel_hi:[1,0]
	s_nop 0
	v_pk_add_f32 v[68:69], v[68:69], v[72:73] op_sel:[1,0] op_sel_hi:[0,1]
	v_mov_b32_e32 v71, v68
	v_pk_add_f32 v[74:75], v[70:71], v[76:77] neg_lo:[0,1] neg_hi:[0,1]
	v_mov_b32_e32 v67, v72
	v_sub_f32_e32 v47, v70, v74
	v_pk_add_f32 v[66:67], v[66:67], v[74:75] neg_lo:[0,1] neg_hi:[0,1]
	v_sub_f32_e32 v47, v76, v47
	v_add_f32_e32 v47, v66, v47
	v_add_f32_e32 v47, v47, v67
	v_add_f32_e32 v47, v68, v47
	v_cndmask_b32_e32 v47, v167, v47, vcc
	v_cmp_ngt_f32_e32 vcc, -1.0, v65
	s_nop 1
	v_cndmask_b32_e32 v47, v168, v47, vcc
	v_cmp_neq_f32_e32 vcc, -1.0, v65
	s_nop 1
	v_cndmask_b32_e32 v47, v169, v47, vcc
	v_cmp_lt_f32_e64 vcc, |v65|, s34
	s_nop 1
	v_cndmask_b32_e32 v47, v47, v65, vcc
	v_add_f32_e32 v47, v64, v47
	v_xor_b32_e32 v64, 0x80000000, v47

; DI float softplusf_(float x) { return fmaxf(x, 0.f) + log1pf(__expf(-fabsf(x))); }
; template <int MODE, bool SB  > DI void norm_phase(const Params& P, const Frame& F, int L, const void* src_, const float* gain, bool combine) {
;     ...
;                 else if (gi < 8) r = -__expf(P.in[I_DN_A_LOG][L * 4 + h]) * softplusf_(mine + P.in[I_DN_DT_BIAS][L * 4 + h]);
.LBB0_1656:
	s_andn2_saveexec_b64 s[26:27], s[26:27]
	s_cbranch_execz .LBB0_1658
	v_mov_b32_e32 v65, v192
	v_mov_b32_e32 v64, v193
	v_add_f32_e32 v47, v47, v65
	v_max_f32_e32 v65, 0, v47
	v_mul_f32_e64 v47, |v47|, s1
	v_exp_f32_e32 v66, v47
	v_mul_f32_e32 v64, 0x3fb8aa3b, v64
	v_exp_f32_e32 v64, v64
	v_add_f32_e32 v47, 1.0, v66
	v_add_f32_e32 v67, -1.0, v47
	v_sub_f32_e32 v68, v67, v47
	v_add_f32_e32 v68, 1.0, v68
	v_sub_f32_e32 v67, v66, v67
	v_add_f32_e32 v67, v67, v68
	v_frexp_mant_f32_e32 v68, v47
	v_cmp_gt_f32_e32 vcc, s30, v68
	v_cvt_f64_f32_e32 v[68:69], v47
	v_frexp_exp_i32_f64_e32 v68, v[68:69]
	v_subbrev_co_u32_e32 v76, vcc, 0, v68, vcc
	v_sub_u32_e32 v68, 0, v76
	v_ldexp_f32 v47, v47, v68
	v_ldexp_f32 v67, v67, v68
	v_add_f32_e32 v68, -1.0, v47
	v_add_f32_e32 v69, 1.0, v68
	v_sub_f32_e32 v69, v47, v69
	v_add_f32_e32 v70, v67, v69
	v_add_f32_e32 v69, 1.0, v47
	v_add_f32_e32 v71, -1.0, v69
	v_sub_f32_e32 v47, v47, v71
	v_add_f32_e32 v47, v67, v47
	v_add_f32_e32 v67, v69, v47
	v_rcp_f32_e32 v77, v67
	v_sub_f32_e32 v69, v67, v69
	v_sub_f32_e32 v47, v47, v69
	v_add_f32_e32 v69, v68, v70
	v_sub_f32_e32 v68, v69, v68
	v_mul_f32_e32 v79, v69, v77
	v_sub_f32_e32 v78, v70, v68
	v_mul_f32_e32 v70, v67, v79
	v_fma_f32 v72, v79, v67, -v70
	v_fmac_f32_e32 v72, v79, v47
	v_add_f32_e32 v68, v70, v72
	v_sub_f32_e32 v71, v69, v68
	v_pk_add_f32 v[74:75], v[68:69], v[70:71] neg_lo:[0,1] neg_hi:[0,1]
	v_mov_b32_e32 v73, v68
	v_pk_add_f32 v[68:69], v[74:75], v[72:73] neg_lo:[0,1] neg_hi:[0,1]
	v_cmp_neq_f32_e32 vcc, s33, v66
	v_add_f32_e32 v69, v78, v69
	v_add_f32_e32 v68, v68, v69
	v_add_f32_e32 v69, v71, v68
	v_mul_f32_e32 v78, v77, v69
	v_mul_f32_e32 v70, v67, v78
	v_fma_f32 v72, v78, v67, -v70
	v_fmac_f32_e32 v72, v78, v47
	v_sub_f32_e32 v47, v71, v69
	v_add_f32_e32 v47, v68, v47
	v_add_f32_e32 v68, v70, v72
	v_sub_f32_e32 v71, v69, v68
	v_pk_add_f32 v[74:75], v[68:69], v[70:71] neg_lo:[0,1] neg_hi:[0,1]
	v_mov_b32_e32 v73, v68
	v_pk_add_f32 v[68:69], v[74:75], v[72:73] neg_lo:[0,1] neg_hi:[0,1]
	v_add_f32_e32 v67, v79, v78
	v_add_f32_e32 v47, v47, v69
	v_add_f32_e32 v47, v68, v47
	v_add_f32_e32 v47, v71, v47
	v_sub_f32_e32 v68, v67, v79
	v_mul_f32_e32 v47, v77, v47
	v_sub_f32_e32 v68, v78, v68
	v_add_f32_e32 v69, v68, v47
	v_add_f32_e32 v70, v67, v69
	v_cvt_f32_i32_e32 v68, v76
	v_mul_f32_e32 v72, v70, v70
	v_fmamk_f32 v47, v72, 0x3e9b6dac, v166
	v_sub_f32_e32 v67, v70, v67
	v_fmaak_f32 v47, v72, v47, 0x3f2aaada
	v_sub_f32_e32 v67, v69, v67
	v_mul_f32_e32 v69, v70, v72
	v_pk_mul_f32 v[72:73], v[68:69], v[46:47]
	v_ldexp_f32 v71, v70, 1
	v_fma_f32 v70, v68, s31, -v72
	v_fmac_f32_e32 v70, 0xb102e308, v68
	v_pk_add_f32 v[68:69], v[72:73], v[70:71]
	v_ldexp_f32 v67, v67, 1
	v_sub_f32_e32 v47, v69, v71
	v_sub_f32_e32 v47, v73, v47
	v_add_f32_e32 v75, v67, v47
	v_mov_b32_e32 v74, v72
	v_pk_add_f32 v[72:73], v[68:69], v[72:73] neg_lo:[0,1] neg_hi:[0,1]
	v_pk_add_f32 v[76:77], v[68:69], v[74:75]
	v_mov_b32_e32 v71, v68
	v_mov_b32_e32 v73, v77
	v_pk_add_f32 v[78:79], v[70:71], v[72:73] neg_lo:[0,1] neg_hi:[0,1]
	v_pk_add_f32 v[70:71], v[70:71], v[72:73]
	v_mov_b32_e32 v74, v75
	v_pk_add_f32 v[72:73], v[70:71], v[68:69] op_sel:[1,0] op_sel_hi:[0,1] neg_lo:[0,1] neg_hi:[0,1]
	v_pk_add_f32 v[80:81], v[76:77], v[72:73] op_sel_hi:[1,0] neg_lo:[0,1] neg_hi:[0,1]
	v_mov_b32_e32 v76, v77
	v_mov_b32_e32 v77, v71
	v_pk_mov_b32 v[72:73], v[68:69], v[72:73] op_sel:[1,0]
	v_mov_b32_e32 v75, v68
	v_pk_add_f32 v[72:73], v[76:77], v[72:73] neg_lo:[0,1] neg_hi:[0,1]
	v_mov_b32_e32 v80, v78
	v_pk_add_f32 v[68:69], v[74:75], v[72:73] neg_lo:[0,1] neg_hi:[0,1]
	v_mov_b32_e32 v79, v71
	v_pk_add_f32 v[72:73], v[80:81], v[68:69]
	s_nop 0
	v_pk_add_f32 v[74:75], v[72:73], v[72:73] op_sel:[0,1] op_sel_hi:[1,0]
	s_nop 0
	v_pk_add_f32 v[70:71], v[70:71], v[74:75] op_sel:[1,0] op_sel_hi:[0,1]
	v_mov_b32_e32 v73, v70
	v_pk_add_f32 v[76:77], v[72:73], v[78:79] neg_lo:[0,1] neg_hi:[0,1]
	v_mov_b32_e32 v69, v74
	v_sub_f32_e32 v47, v72, v76
	v_pk_add_f32 v[68:69], v[68:69], v[76:77] neg_lo:[0,1] neg_hi:[0,1]
	v_sub_f32_e32 v47, v78, v47
	v_add_f32_e32 v47, v68, v47
	v_add_f32_e32 v47, v47, v69
	v_add_f32_e32 v47, v70, v47
	v_cndmask_b32_e32 v47, v167, v47, vcc
	v_cmp_ngt_f32_e32 vcc, -1.0, v66
	s_nop 1
	v_cndmask_b32_e32 v47, v168, v47, vcc
	v_cmp_neq_f32_e32 vcc, -1.0, v66
	s_nop 1
	v_cndmask_b32_e32 v47, v169, v47, vcc
	v_cmp_lt_f32_e64 vcc, |v66|, s34
	s_nop 1
	v_cndmask_b32_e32 v47, v47, v66, vcc
	v_add_f32_e32 v47, v65, v47
	v_mul_f32_e64 v64, v47, -v64

; #define LAS __attribute__((address_space(3)))
; template <int MODE, bool SB  > DI void norm_phase(const Params& P, const Frame& F, int L, const void* src_, const float* gain, bool combine) {
;     ...
;     if (MODE == 2) { const f32x4* w = (const f32x4*)(ws + WS_WRT); for (int i = F.tid; i < NEXP * D / 4; i += NTHR) ((LAS f32x4*)F.lds)[i] = w[i]; if (F.tid < 8) F.MISC[16 + F.tid] = 0u; __syncthreads(); }
.LBB0_2873:
	global_load_dwordx4 v[130:133], v[0:1], off
	v_lshl_add_u64 v[0:1], v[0:1], 0, s[6:7]
	global_load_dwordx4 v[134:137], v[0:1], off
	v_lshl_add_u64 v[0:1], v[0:1], 0, s[6:7]
	global_load_dwordx4 v[138:141], v[0:1], off
	v_lshl_add_u64 v[0:1], v[0:1], 0, s[6:7]
	global_load_dwordx4 v[142:145], v[0:1], off
	v_lshl_add_u64 v[0:1], v[0:1], 0, s[6:7]
	global_load_dwordx4 v[146:149], v[0:1], off
	v_lshl_add_u64 v[0:1], v[0:1], 0, s[6:7]
	global_load_dwordx4 v[150:153], v[0:1], off
	v_lshl_add_u64 v[0:1], v[0:1], 0, s[6:7]
	global_load_dwordx4 v[154:157], v[0:1], off
	v_lshl_add_u64 v[0:1], v[0:1], 0, s[6:7]
	global_load_dwordx4 v[158:161], v[0:1], off
	s_waitcnt vmcnt(7)
	ds_write_b128 v3, v[130:133]
	v_add_u32_e32 v3, 0x2000, v3
	s_waitcnt vmcnt(6)
	ds_write_b128 v3, v[134:137]
	v_add_u32_e32 v3, 0x2000, v3
	s_waitcnt vmcnt(5)
	ds_write_b128 v3, v[138:141]
	v_add_u32_e32 v3, 0x2000, v3
	s_waitcnt vmcnt(4)
	ds_write_b128 v3, v[142:145]
	v_add_u32_e32 v3, 0x2000, v3
	s_waitcnt vmcnt(3)
	ds_write_b128 v3, v[146:149]
	v_add_u32_e32 v3, 0x2000, v3
	s_waitcnt vmcnt(2)
	ds_write_b128 v3, v[150:153]
	v_add_u32_e32 v3, 0x2000, v3
	s_waitcnt vmcnt(1)
	ds_write_b128 v3, v[154:157]
	v_add_u32_e32 v3, 0x2000, v3
	s_waitcnt vmcnt(0)
	ds_write_b128 v3, v[158:161]

.LBB0_2935:
	s_cmp_lt_u32 s3, 0x40001
	s_mov_b64 s[18:19], 0
	s_cselect_b64 s[20:21], -1, 0
	s_mov_b64 s[22:23], -1
	s_and_b64 vcc, exec, s[20:21]
	s_cbranch_vccnz .LBB0_2932
	s_branch .LBB0_2929
	s_nop 0
	s_nop 0
	s_nop 0
	s_nop 0
	s_nop 0
	s_nop 0
	s_nop 0
	s_nop 0
	s_nop 0
	s_nop 0
	s_nop 0

; DI void moe_gather_phase(const Params& P, const Frame& F) {
;     ...
;     for (int i = F.tid >> 7; i < 2 * nr; i += 4) { const int row = r_lo + (i >> 1), s = slots[i];
;         ((u32x4*)(AP + (size_t)s * D))[F.tid & 127] = ((const u32x4*)(HN + (size_t)row * D))[F.tid & 127]; }
.LBB0_3036:
	v_ashrrev_i32_e32 v44, 1, v4
	v_add_u32_e32 v44, s3, v44
	v_ashrrev_i32_e32 v45, 31, v44
	v_lshlrev_b64 v[44:45], 11, v[44:45]
	v_lshl_add_u64 v[44:45], v[0:1], 0, v[44:45]
	global_load_dwordx4 v[48:51], v[44:45], off
	ds_read_b32 v80, v5
	v_add_u32_e32 v4, 4, v4
	v_ashrrev_i32_e32 v44, 1, v4
	v_add_u32_e32 v44, s3, v44
	v_ashrrev_i32_e32 v45, 31, v44
	v_lshlrev_b64 v[44:45], 11, v[44:45]
	v_lshl_add_u64 v[44:45], v[0:1], 0, v[44:45]
	global_load_dwordx4 v[52:55], v[44:45], off
	ds_read_b32 v81, v5 offset:16
	v_add_u32_e32 v4, 4, v4
	v_ashrrev_i32_e32 v44, 1, v4
	v_add_u32_e32 v44, s3, v44
	v_ashrrev_i32_e32 v45, 31, v44
	v_lshlrev_b64 v[44:45], 11, v[44:45]
	v_lshl_add_u64 v[44:45], v[0:1], 0, v[44:45]
	global_load_dwordx4 v[56:59], v[44:45], off
	ds_read_b32 v82, v5 offset:32
	v_add_u32_e32 v4, 4, v4
	v_ashrrev_i32_e32 v44, 1, v4
	v_add_u32_e32 v44, s3, v44
	v_ashrrev_i32_e32 v45, 31, v44
	v_lshlrev_b64 v[44:45], 11, v[44:45]
	v_lshl_add_u64 v[44:45], v[0:1], 0, v[44:45]
	global_load_dwordx4 v[60:63], v[44:45], off
	ds_read_b32 v83, v5 offset:48
	v_add_u32_e32 v4, 4, v4
	v_ashrrev_i32_e32 v44, 1, v4
	v_add_u32_e32 v44, s3, v44
	v_ashrrev_i32_e32 v45, 31, v44
	v_lshlrev_b64 v[44:45], 11, v[44:45]
	v_lshl_add_u64 v[44:45], v[0:1], 0, v[44:45]
	global_load_dwordx4 v[64:67], v[44:45], off
	ds_read_b32 v84, v5 offset:64
	v_add_u32_e32 v4, 4, v4
	v_ashrrev_i32_e32 v44, 1, v4
	v_add_u32_e32 v44, s3, v44
	v_ashrrev_i32_e32 v45, 31, v44
	v_lshlrev_b64 v[44:45], 11, v[44:45]
	v_lshl_add_u64 v[44:45], v[0:1], 0, v[44:45]
	global_load_dwordx4 v[68:71], v[44:45], off
	ds_read_b32 v85, v5 offset:80
	v_add_u32_e32 v4, 4, v4
	v_ashrrev_i32_e32 v44, 1, v4
	v_add_u32_e32 v44, s3, v44
	v_ashrrev_i32_e32 v45, 31, v44
	v_lshlrev_b64 v[44:45], 11, v[44:45]
	v_lshl_add_u64 v[44:45], v[0:1], 0, v[44:45]
	global_load_dwordx4 v[72:75], v[44:45], off
	ds_read_b32 v86, v5 offset:96
	v_add_u32_e32 v4, 4, v4
	v_ashrrev_i32_e32 v44, 1, v4
	v_add_u32_e32 v44, s3, v44
	v_ashrrev_i32_e32 v45, 31, v44
	v_lshlrev_b64 v[44:45], 11, v[44:45]
	v_lshl_add_u64 v[44:45], v[0:1], 0, v[44:45]
	global_load_dwordx4 v[76:79], v[44:45], off
	ds_read_b32 v87, v5 offset:112
	v_add_u32_e32 v4, 4, v4
	v_add_u32_e32 v5, 0x80, v5
	s_waitcnt lgkmcnt(0)
	v_mov_b32_e32 v46, v80
	v_ashrrev_i32_e32 v47, 31, v46
	v_lshlrev_b64 v[46:47], 11, v[46:47]
	v_lshl_add_u64 v[46:47], v[2:3], 0, v[46:47]
	s_waitcnt vmcnt(7)
	global_store_dwordx4 v[46:47], v[48:51], off
	v_mov_b32_e32 v88, v81
	v_ashrrev_i32_e32 v89, 31, v88
	v_lshlrev_b64 v[88:89], 11, v[88:89]
	v_lshl_add_u64 v[88:89], v[2:3], 0, v[88:89]
	s_waitcnt vmcnt(6)
	global_store_dwordx4 v[88:89], v[52:55], off
	v_mov_b32_e32 v46, v82
	v_ashrrev_i32_e32 v47, 31, v46
	v_lshlrev_b64 v[46:47], 11, v[46:47]
	v_lshl_add_u64 v[46:47], v[2:3], 0, v[46:47]
	s_waitcnt vmcnt(5)
	global_store_dwordx4 v[46:47], v[56:59], off
	v_mov_b32_e32 v88, v83
	v_ashrrev_i32_e32 v89, 31, v88
	v_lshlrev_b64 v[88:89], 11, v[88:89]
	v_lshl_add_u64 v[88:89], v[2:3], 0, v[88:89]
	s_waitcnt vmcnt(4)
	global_store_dwordx4 v[88:89], v[60:63], off
	v_mov_b32_e32 v46, v84
	v_ashrrev_i32_e32 v47, 31, v46
	v_lshlrev_b64 v[46:47], 11, v[46:47]
	v_lshl_add_u64 v[46:47], v[2:3], 0, v[46:47]
	s_waitcnt vmcnt(3)
	global_store_dwordx4 v[46:47], v[64:67], off
	v_mov_b32_e32 v88, v85
	v_ashrrev_i32_e32 v89, 31, v88
	v_lshlrev_b64 v[88:89], 11, v[88:89]
	v_lshl_add_u64 v[88:89], v[2:3], 0, v[88:89]
	s_waitcnt vmcnt(2)
	global_store_dwordx4 v[88:89], v[68:71], off
	v_mov_b32_e32 v46, v86
	v_ashrrev_i32_e32 v47, 31, v46
	v_lshlrev_b64 v[46:47], 11, v[46:47]
	v_lshl_add_u64 v[46:47], v[2:3], 0, v[46:47]
	s_waitcnt vmcnt(1)
	global_store_dwordx4 v[46:47], v[72:75], off
	v_mov_b32_e32 v88, v87
	v_ashrrev_i32_e32 v89, 31, v88
	v_lshlrev_b64 v[88:89], 11, v[88:89]
	v_lshl_add_u64 v[88:89], v[2:3], 0, v[88:89]
	s_waitcnt vmcnt(0)
	global_store_dwordx4 v[88:89], v[76:79], off
	v_ashrrev_i32_e32 v44, 1, v4
	v_add_u32_e32 v44, s3, v44
	v_ashrrev_i32_e32 v45, 31, v44
	v_lshlrev_b64 v[44:45], 11, v[44:45]
	v_lshl_add_u64 v[44:45], v[0:1], 0, v[44:45]
	global_load_dwordx4 v[48:51], v[44:45], off
	ds_read_b32 v80, v5
	v_add_u32_e32 v4, 4, v4
	v_ashrrev_i32_e32 v44, 1, v4
	v_add_u32_e32 v44, s3, v44
	v_ashrrev_i32_e32 v45, 31, v44
	v_lshlrev_b64 v[44:45], 11, v[44:45]
	v_lshl_add_u64 v[44:45], v[0:1], 0, v[44:45]
	global_load_dwordx4 v[52:55], v[44:45], off
	ds_read_b32 v81, v5 offset:16
	v_add_u32_e32 v4, 4, v4
	v_ashrrev_i32_e32 v44, 1, v4
	v_add_u32_e32 v44, s3, v44
	v_ashrrev_i32_e32 v45, 31, v44
	v_lshlrev_b64 v[44:45], 11, v[44:45]
	v_lshl_add_u64 v[44:45], v[0:1], 0, v[44:45]
	global_load_dwordx4 v[56:59], v[44:45], off
	ds_read_b32 v82, v5 offset:32
	v_add_u32_e32 v4, 4, v4
	v_ashrrev_i32_e32 v44, 1, v4
	v_add_u32_e32 v44, s3, v44
	v_ashrrev_i32_e32 v45, 31, v44
	v_lshlrev_b64 v[44:45], 11, v[44:45]
	v_lshl_add_u64 v[44:45], v[0:1], 0, v[44:45]
	global_load_dwordx4 v[60:63], v[44:45], off
	ds_read_b32 v83, v5 offset:48
	v_add_u32_e32 v4, 4, v4
	v_ashrrev_i32_e32 v44, 1, v4
	v_add_u32_e32 v44, s3, v44
	v_ashrrev_i32_e32 v45, 31, v44
	v_lshlrev_b64 v[44:45], 11, v[44:45]
	v_lshl_add_u64 v[44:45], v[0:1], 0, v[44:45]
	global_load_dwordx4 v[64:67], v[44:45], off
	ds_read_b32 v84, v5 offset:64
	v_add_u32_e32 v4, 4, v4
	v_ashrrev_i32_e32 v44, 1, v4
	v_add_u32_e32 v44, s3, v44
	v_ashrrev_i32_e32 v45, 31, v44
	v_lshlrev_b64 v[44:45], 11, v[44:45]
	v_lshl_add_u64 v[44:45], v[0:1], 0, v[44:45]
	global_load_dwordx4 v[68:71], v[44:45], off
	ds_read_b32 v85, v5 offset:80
	v_add_u32_e32 v4, 4, v4
	v_ashrrev_i32_e32 v44, 1, v4
	v_add_u32_e32 v44, s3, v44
	v_ashrrev_i32_e32 v45, 31, v44
	v_lshlrev_b64 v[44:45], 11, v[44:45]
	v_lshl_add_u64 v[44:45], v[0:1], 0, v[44:45]
	global_load_dwordx4 v[72:75], v[44:45], off
	ds_read_b32 v86, v5 offset:96
	v_add_u32_e32 v4, 4, v4
	v_ashrrev_i32_e32 v44, 1, v4
	v_add_u32_e32 v44, s3, v44
	v_ashrrev_i32_e32 v45, 31, v44
	v_lshlrev_b64 v[44:45], 11, v[44:45]
	v_lshl_add_u64 v[44:45], v[0:1], 0, v[44:45]
	global_load_dwordx4 v[76:79], v[44:45], off
	ds_read_b32 v87, v5 offset:112
	v_add_u32_e32 v4, 4, v4
	v_add_u32_e32 v5, 0x80, v5
	s_waitcnt lgkmcnt(0)
; DI void moe_gather_phase(const Params& P, const Frame& F) {
;     ...
;     for (int i = F.tid >> 7; i < 2 * nr; i += 4) { const int row = r_lo + (i >> 1), s = slots[i];
;         ((u32x4*)(AP + (size_t)s * D))[F.tid & 127] = ((const u32x4*)(HN + (size_t)row * D))[F.tid & 127]; }
	v_mov_b32_e32 v46, v80
	v_ashrrev_i32_e32 v47, 31, v46
	v_lshlrev_b64 v[46:47], 11, v[46:47]
	v_lshl_add_u64 v[46:47], v[2:3], 0, v[46:47]
	s_waitcnt vmcnt(7)
	global_store_dwordx4 v[46:47], v[48:51], off
	v_mov_b32_e32 v88, v81
	v_ashrrev_i32_e32 v89, 31, v88
	v_lshlrev_b64 v[88:89], 11, v[88:89]
	v_lshl_add_u64 v[88:89], v[2:3], 0, v[88:89]
	s_waitcnt vmcnt(6)
	global_store_dwordx4 v[88:89], v[52:55], off
	v_mov_b32_e32 v46, v82
	v_ashrrev_i32_e32 v47, 31, v46
	v_lshlrev_b64 v[46:47], 11, v[46:47]
	v_lshl_add_u64 v[46:47], v[2:3], 0, v[46:47]
	s_waitcnt vmcnt(5)
	global_store_dwordx4 v[46:47], v[56:59], off
	v_mov_b32_e32 v88, v83
	v_ashrrev_i32_e32 v89, 31, v88
	v_lshlrev_b64 v[88:89], 11, v[88:89]
	v_lshl_add_u64 v[88:89], v[2:3], 0, v[88:89]
	s_waitcnt vmcnt(4)
	global_store_dwordx4 v[88:89], v[60:63], off
	v_mov_b32_e32 v46, v84
	v_ashrrev_i32_e32 v47, 31, v46
	v_lshlrev_b64 v[46:47], 11, v[46:47]
	v_lshl_add_u64 v[46:47], v[2:3], 0, v[46:47]
	s_waitcnt vmcnt(3)
	global_store_dwordx4 v[46:47], v[64:67], off
	v_mov_b32_e32 v88, v85
	v_ashrrev_i32_e32 v89, 31, v88
	v_lshlrev_b64 v[88:89], 11, v[88:89]
	v_lshl_add_u64 v[88:89], v[2:3], 0, v[88:89]
	s_waitcnt vmcnt(2)
	global_store_dwordx4 v[88:89], v[68:71], off
	v_mov_b32_e32 v46, v86
	v_ashrrev_i32_e32 v47, 31, v46
	v_lshlrev_b64 v[46:47], 11, v[46:47]
	v_lshl_add_u64 v[46:47], v[2:3], 0, v[46:47]
	s_waitcnt vmcnt(1)
	global_store_dwordx4 v[46:47], v[72:75], off
	v_mov_b32_e32 v88, v87
	v_ashrrev_i32_e32 v89, 31, v88
	v_lshlrev_b64 v[88:89], 11, v[88:89]
	v_lshl_add_u64 v[88:89], v[2:3], 0, v[88:89]
	s_waitcnt vmcnt(0)
	global_store_dwordx4 v[88:89], v[76:79], off
	v_ashrrev_i32_e32 v44, 1, v4
	v_add_u32_e32 v44, s3, v44
	v_ashrrev_i32_e32 v45, 31, v44
	v_lshlrev_b64 v[44:45], 11, v[44:45]
	v_lshl_add_u64 v[44:45], v[0:1], 0, v[44:45]
	global_load_dwordx4 v[48:51], v[44:45], off
	ds_read_b32 v80, v5
	v_add_u32_e32 v4, 4, v4
	v_ashrrev_i32_e32 v44, 1, v4
	v_add_u32_e32 v44, s3, v44
	v_ashrrev_i32_e32 v45, 31, v44
	v_lshlrev_b64 v[44:45], 11, v[44:45]
	v_lshl_add_u64 v[44:45], v[0:1], 0, v[44:45]
	global_load_dwordx4 v[52:55], v[44:45], off
	ds_read_b32 v81, v5 offset:16
	v_add_u32_e32 v4, 4, v4
	v_ashrrev_i32_e32 v44, 1, v4
	v_add_u32_e32 v44, s3, v44
	v_ashrrev_i32_e32 v45, 31, v44
	v_lshlrev_b64 v[44:45], 11, v[44:45]
	v_lshl_add_u64 v[44:45], v[0:1], 0, v[44:45]
	global_load_dwordx4 v[56:59], v[44:45], off
	ds_read_b32 v82, v5 offset:32
	v_add_u32_e32 v4, 4, v4
	v_ashrrev_i32_e32 v44, 1, v4
	v_add_u32_e32 v44, s3, v44
	v_ashrrev_i32_e32 v45, 31, v44
	v_lshlrev_b64 v[44:45], 11, v[44:45]
	v_lshl_add_u64 v[44:45], v[0:1], 0, v[44:45]
	global_load_dwordx4 v[60:63], v[44:45], off
	ds_read_b32 v83, v5 offset:48
	v_add_u32_e32 v4, 4, v4
	v_ashrrev_i32_e32 v44, 1, v4
	v_add_u32_e32 v44, s3, v44
	v_ashrrev_i32_e32 v45, 31, v44
	v_lshlrev_b64 v[44:45], 11, v[44:45]
	v_lshl_add_u64 v[44:45], v[0:1], 0, v[44:45]
	global_load_dwordx4 v[64:67], v[44:45], off
	ds_read_b32 v84, v5 offset:64
	v_add_u32_e32 v4, 4, v4
	v_ashrrev_i32_e32 v44, 1, v4
	v_add_u32_e32 v44, s3, v44
	v_ashrrev_i32_e32 v45, 31, v44
	v_lshlrev_b64 v[44:45], 11, v[44:45]
	v_lshl_add_u64 v[44:45], v[0:1], 0, v[44:45]
	global_load_dwordx4 v[68:71], v[44:45], off
	ds_read_b32 v85, v5 offset:80
	v_add_u32_e32 v4, 4, v4
	v_ashrrev_i32_e32 v44, 1, v4
	v_add_u32_e32 v44, s3, v44
	v_ashrrev_i32_e32 v45, 31, v44
	v_lshlrev_b64 v[44:45], 11, v[44:45]
	v_lshl_add_u64 v[44:45], v[0:1], 0, v[44:45]
	global_load_dwordx4 v[72:75], v[44:45], off
	ds_read_b32 v86, v5 offset:96
	v_add_u32_e32 v4, 4, v4
	v_ashrrev_i32_e32 v44, 1, v4
	v_add_u32_e32 v44, s3, v44
	v_ashrrev_i32_e32 v45, 31, v44
	v_lshlrev_b64 v[44:45], 11, v[44:45]
	v_lshl_add_u64 v[44:45], v[0:1], 0, v[44:45]
	global_load_dwordx4 v[76:79], v[44:45], off
	ds_read_b32 v87, v5 offset:112
	v_add_u32_e32 v4, 4, v4
	v_add_u32_e32 v5, 0x80, v5
	s_waitcnt lgkmcnt(0)
	v_mov_b32_e32 v46, v80
	v_ashrrev_i32_e32 v47, 31, v46
	v_lshlrev_b64 v[46:47], 11, v[46:47]
	v_lshl_add_u64 v[46:47], v[2:3], 0, v[46:47]
	s_waitcnt vmcnt(7)
	global_store_dwordx4 v[46:47], v[48:51], off
	v_mov_b32_e32 v88, v81
	v_ashrrev_i32_e32 v89, 31, v88
	v_lshlrev_b64 v[88:89], 11, v[88:89]
	v_lshl_add_u64 v[88:89], v[2:3], 0, v[88:89]
	s_waitcnt vmcnt(6)
	global_store_dwordx4 v[88:89], v[52:55], off
	v_mov_b32_e32 v46, v82
	v_ashrrev_i32_e32 v47, 31, v46
	v_lshlrev_b64 v[46:47], 11, v[46:47]
	v_lshl_add_u64 v[46:47], v[2:3], 0, v[46:47]
	s_waitcnt vmcnt(5)
	global_store_dwordx4 v[46:47], v[56:59], off
	v_mov_b32_e32 v88, v83
	v_ashrrev_i32_e32 v89, 31, v88
	v_lshlrev_b64 v[88:89], 11, v[88:89]
	v_lshl_add_u64 v[88:89], v[2:3], 0, v[88:89]
	s_waitcnt vmcnt(4)
; DI void moe_gather_phase(const Params& P, const Frame& F) {
;     ...
;     for (int i = F.tid >> 7; i < 2 * nr; i += 4) { const int row = r_lo + (i >> 1), s = slots[i];
;         ((u32x4*)(AP + (size_t)s * D))[F.tid & 127] = ((const u32x4*)(HN + (size_t)row * D))[F.tid & 127]; }
	global_store_dwordx4 v[88:89], v[60:63], off
	v_mov_b32_e32 v46, v84
	v_ashrrev_i32_e32 v47, 31, v46
	v_lshlrev_b64 v[46:47], 11, v[46:47]
	v_lshl_add_u64 v[46:47], v[2:3], 0, v[46:47]
	s_waitcnt vmcnt(3)
	global_store_dwordx4 v[46:47], v[64:67], off
	v_mov_b32_e32 v88, v85
	v_ashrrev_i32_e32 v89, 31, v88
	v_lshlrev_b64 v[88:89], 11, v[88:89]
	v_lshl_add_u64 v[88:89], v[2:3], 0, v[88:89]
	s_waitcnt vmcnt(2)
	global_store_dwordx4 v[88:89], v[68:71], off
	v_mov_b32_e32 v46, v86
	v_ashrrev_i32_e32 v47, 31, v46
	v_lshlrev_b64 v[46:47], 11, v[46:47]
	v_lshl_add_u64 v[46:47], v[2:3], 0, v[46:47]
	s_waitcnt vmcnt(1)
	global_store_dwordx4 v[46:47], v[72:75], off
	v_mov_b32_e32 v88, v87
	v_ashrrev_i32_e32 v89, 31, v88
	v_lshlrev_b64 v[88:89], 11, v[88:89]
	v_lshl_add_u64 v[88:89], v[2:3], 0, v[88:89]
	s_waitcnt vmcnt(0)
	global_store_dwordx4 v[88:89], v[76:79], off
	v_ashrrev_i32_e32 v44, 1, v4
	v_add_u32_e32 v44, s3, v44
	v_ashrrev_i32_e32 v45, 31, v44
	v_lshlrev_b64 v[44:45], 11, v[44:45]
	v_lshl_add_u64 v[44:45], v[0:1], 0, v[44:45]
	global_load_dwordx4 v[48:51], v[44:45], off
	ds_read_b32 v80, v5
	v_add_u32_e32 v4, 4, v4
	v_ashrrev_i32_e32 v44, 1, v4
	v_add_u32_e32 v44, s3, v44
	v_ashrrev_i32_e32 v45, 31, v44
	v_lshlrev_b64 v[44:45], 11, v[44:45]
	v_lshl_add_u64 v[44:45], v[0:1], 0, v[44:45]
	global_load_dwordx4 v[52:55], v[44:45], off
	ds_read_b32 v81, v5 offset:16
	v_add_u32_e32 v4, 4, v4
	v_ashrrev_i32_e32 v44, 1, v4
	v_add_u32_e32 v44, s3, v44
	v_ashrrev_i32_e32 v45, 31, v44
	v_lshlrev_b64 v[44:45], 11, v[44:45]
	v_lshl_add_u64 v[44:45], v[0:1], 0, v[44:45]
	global_load_dwordx4 v[56:59], v[44:45], off
	ds_read_b32 v82, v5 offset:32
	v_add_u32_e32 v4, 4, v4
	v_ashrrev_i32_e32 v44, 1, v4
	v_add_u32_e32 v44, s3, v44
	v_ashrrev_i32_e32 v45, 31, v44
	v_lshlrev_b64 v[44:45], 11, v[44:45]
	v_lshl_add_u64 v[44:45], v[0:1], 0, v[44:45]
	global_load_dwordx4 v[60:63], v[44:45], off
	ds_read_b32 v83, v5 offset:48
	v_add_u32_e32 v4, 4, v4
	v_ashrrev_i32_e32 v44, 1, v4
	v_add_u32_e32 v44, s3, v44
	v_ashrrev_i32_e32 v45, 31, v44
	v_lshlrev_b64 v[44:45], 11, v[44:45]
	v_lshl_add_u64 v[44:45], v[0:1], 0, v[44:45]
	global_load_dwordx4 v[64:67], v[44:45], off
	ds_read_b32 v84, v5 offset:64
	v_add_u32_e32 v4, 4, v4
	v_ashrrev_i32_e32 v44, 1, v4
	v_add_u32_e32 v44, s3, v44
	v_ashrrev_i32_e32 v45, 31, v44
	v_lshlrev_b64 v[44:45], 11, v[44:45]
	v_lshl_add_u64 v[44:45], v[0:1], 0, v[44:45]
	global_load_dwordx4 v[68:71], v[44:45], off
	ds_read_b32 v85, v5 offset:80
	v_add_u32_e32 v4, 4, v4
	v_ashrrev_i32_e32 v44, 1, v4
	v_add_u32_e32 v44, s3, v44
	v_ashrrev_i32_e32 v45, 31, v44
	v_lshlrev_b64 v[44:45], 11, v[44:45]
	v_lshl_add_u64 v[44:45], v[0:1], 0, v[44:45]
	global_load_dwordx4 v[72:75], v[44:45], off
	ds_read_b32 v86, v5 offset:96
	v_add_u32_e32 v4, 4, v4
	v_ashrrev_i32_e32 v44, 1, v4
	v_add_u32_e32 v44, s3, v44
	v_ashrrev_i32_e32 v45, 31, v44
	v_lshlrev_b64 v[44:45], 11, v[44:45]
	v_lshl_add_u64 v[44:45], v[0:1], 0, v[44:45]
	global_load_dwordx4 v[76:79], v[44:45], off
	ds_read_b32 v87, v5 offset:112
	v_add_u32_e32 v4, 4, v4
	v_add_u32_e32 v5, 0x80, v5
	s_waitcnt lgkmcnt(0)
	v_mov_b32_e32 v46, v80
	v_ashrrev_i32_e32 v47, 31, v46
	v_lshlrev_b64 v[46:47], 11, v[46:47]
	v_lshl_add_u64 v[46:47], v[2:3], 0, v[46:47]
	s_waitcnt vmcnt(7)
	global_store_dwordx4 v[46:47], v[48:51], off
	v_mov_b32_e32 v88, v81
	v_ashrrev_i32_e32 v89, 31, v88
	v_lshlrev_b64 v[88:89], 11, v[88:89]
	v_lshl_add_u64 v[88:89], v[2:3], 0, v[88:89]
	s_waitcnt vmcnt(6)
	global_store_dwordx4 v[88:89], v[52:55], off
	v_mov_b32_e32 v46, v82
	v_ashrrev_i32_e32 v47, 31, v46
	v_lshlrev_b64 v[46:47], 11, v[46:47]
	v_lshl_add_u64 v[46:47], v[2:3], 0, v[46:47]
	s_waitcnt vmcnt(5)
	global_store_dwordx4 v[46:47], v[56:59], off
	v_mov_b32_e32 v88, v83
	v_ashrrev_i32_e32 v89, 31, v88
	v_lshlrev_b64 v[88:89], 11, v[88:89]
	v_lshl_add_u64 v[88:89], v[2:3], 0, v[88:89]
	s_waitcnt vmcnt(4)
	global_store_dwordx4 v[88:89], v[60:63], off
	v_mov_b32_e32 v46, v84
	v_ashrrev_i32_e32 v47, 31, v46
	v_lshlrev_b64 v[46:47], 11, v[46:47]
	v_lshl_add_u64 v[46:47], v[2:3], 0, v[46:47]
	s_waitcnt vmcnt(3)
	global_store_dwordx4 v[46:47], v[64:67], off
	v_mov_b32_e32 v88, v85
	v_ashrrev_i32_e32 v89, 31, v88
	v_lshlrev_b64 v[88:89], 11, v[88:89]
	v_lshl_add_u64 v[88:89], v[2:3], 0, v[88:89]
	s_waitcnt vmcnt(2)
	global_store_dwordx4 v[88:89], v[68:71], off
	v_mov_b32_e32 v46, v86
	v_ashrrev_i32_e32 v47, 31, v46
	v_lshlrev_b64 v[46:47], 11, v[46:47]
	v_lshl_add_u64 v[46:47], v[2:3], 0, v[46:47]
	s_waitcnt vmcnt(1)
	global_store_dwordx4 v[46:47], v[72:75], off
	v_mov_b32_e32 v88, v87
	v_ashrrev_i32_e32 v89, 31, v88
	v_lshlrev_b64 v[88:89], 11, v[88:89]
	v_lshl_add_u64 v[88:89], v[2:3], 0, v[88:89]
	s_waitcnt vmcnt(0)
	global_store_dwordx4 v[88:89], v[76:79], off

; DI void moe_gather_phase(const Params& P, const Frame& F) {
;     ...
;             if (F.bid == 0) for (int t = off / 256; t < (off + pad) / 256; ++t) TILE_E[t] = e;
.LBB0_3091:
	s_add_i32 s3, s3, -1
	global_store_dword v2, v2, s[4:5]
	s_add_u32 s4, s4, 4
	s_addc_u32 s5, s5, 0
	s_cmp_lg_u32 s3, 0
	s_cbranch_scc1 .LBB0_3091
	s_branch .LBB0_2967
	s_nop 0
	s_nop 0
	s_nop 0
	s_nop 0
	s_nop 0
	s_nop 0
	s_nop 0
	s_nop 0
	s_nop 0
	s_nop 0
	s_nop 0
	s_nop 0
	s_nop 0
	s_nop 0
	s_nop 0
	s_nop 0
	s_nop 0
	s_nop 0
	s_nop 0
	s_nop 0
	s_nop 0
	s_nop 0
	s_nop 0
	s_nop 0
	s_nop 0
	s_nop 0
	s_nop 0
	s_nop 0
	s_nop 0
	s_nop 0
	s_nop 0
	s_nop 0
	s_nop 0
	s_nop 0
	s_nop 0
	s_nop 0
	s_nop 0
	s_nop 0
	s_nop 0
	s_nop 0
	s_nop 0
	s_nop 0
	s_nop 0
	s_nop 0
	s_nop 0
	s_nop 0
	s_nop 0
